# GEMM epilogue stores (P1 P3 P4 P7 P8) issued with nt
# speedup vs baseline: 1.0143x; 1.0143x over previous
.LBB0_148:
	s_lshl_b32 s2, s52, 8
	s_and_b32 s52, s2, 0x300
	s_and_b64 s[50:51], s[28:29], exec
	s_cselect_b32 s50, s52, s2
	s_mov_b64 s[40:41], -1
	s_add_i32 s50, s50, s79
	s_andn2_b64 vcc, exec, s[46:47]
	s_ashr_i32 s46, s7, 31
	s_cbranch_vccz .LBB0_155
	s_xor_b64 s[42:43], s[42:43], -1
	s_and_b64 vcc, exec, s[42:43]
	s_cbranch_vccz .LBB0_151
	s_lshl_b32 s2, s38, 2
	v_mul_f32_e32 v6, 0xbd38aa3b, v191
	s_ashr_i32 s40, s50, 4
	s_add_i32 s42, s88, s2
	v_and_b32_e32 v3, 1, v50
	v_exp_f32_e32 v6, v6
	s_ashr_i32 s41, s40, 31
	s_ashr_i32 s43, s42, 31
	v_cmp_eq_u32_e32 vcc, 0, v3
	v_lshlrev_b32_e32 v3, 3, v50
	s_lshl_b64 s[40:41], s[40:41], 15
	s_lshl_b64 s[42:43], s[42:43], 10
	v_add_u32_e32 v4, 24, v3
	v_cndmask_b32_e32 v3, v4, v3, vcc
	s_add_u32 s2, s22, s40
	v_ashrrev_i32_e32 v4, 4, v3
	s_addc_u32 s38, s23, s41
	v_add_f32_e32 v6, 1.0, v6
	v_ashrrev_i32_e32 v5, 31, v4
	s_add_u32 s40, s2, s42
	v_rcp_f32_e32 v7, v6
	v_mul_f32_e32 v6, 0xbd38aa3b, v192
	v_lshlrev_b64 v[4:5], 8, v[4:5]
	s_addc_u32 s41, s38, s43
	v_exp_f32_e32 v6, v6
	v_ashrrev_i32_e32 v3, 31, v2
	v_lshl_add_u64 v[4:5], s[40:41], 0, v[4:5]
	v_lshl_add_u64 v[4:5], v[2:3], 4, v[4:5]
	v_mul_f32_e32 v3, 0xbd38aa3b, v190
	v_exp_f32_e32 v3, v3
	v_add_f32_e32 v6, 1.0, v6
	v_rcp_f32_e32 v8, v6
	v_mul_f32_e32 v6, 0xbd38aa3b, v193
	v_exp_f32_e32 v6, v6
	v_add_f32_e32 v3, 1.0, v3
	v_rcp_f32_e32 v3, v3
	s_mov_b32 s2, 0x8000
	v_add_f32_e32 v6, 1.0, v6
	v_rcp_f32_e32 v9, v6
	v_mov_b32_e32 v6, v199
	v_cvt_pk_fp8_f32 v6, v3, v7
	v_mul_f32_e32 v7, 0xbd38aa3b, v187
	v_exp_f32_e32 v7, v7
	v_mul_f32_e32 v3, 0xbd38aa3b, v186
	v_cvt_pk_fp8_f32 v6, v8, v9 op_sel:[0,0,1]
	v_exp_f32_e32 v3, v3
	v_add_f32_e32 v7, 1.0, v7
	v_rcp_f32_e32 v8, v7
	v_mul_f32_e32 v7, 0xbd38aa3b, v188
	v_exp_f32_e32 v7, v7
	v_add_f32_e32 v3, 1.0, v3
	v_rcp_f32_e32 v3, v3
	s_mov_b64 s[40:41], 0
	v_add_f32_e32 v7, 1.0, v7
	v_rcp_f32_e32 v9, v7
	v_mul_f32_e32 v7, 0xbd38aa3b, v189
	v_exp_f32_e32 v7, v7
	s_nop 0
	v_add_f32_e32 v7, 1.0, v7
	v_rcp_f32_e32 v10, v7
	v_mov_b32_e32 v7, v199
	v_cvt_pk_fp8_f32 v7, v3, v8
	v_mul_f32_e32 v8, 0xbd38aa3b, v183
	v_exp_f32_e32 v8, v8
	v_mul_f32_e32 v3, 0xbd38aa3b, v182
	v_cvt_pk_fp8_f32 v7, v9, v10 op_sel:[0,0,1]
	v_exp_f32_e32 v3, v3
	v_add_f32_e32 v8, 1.0, v8
	v_rcp_f32_e32 v9, v8
	v_mul_f32_e32 v8, 0xbd38aa3b, v184
	v_exp_f32_e32 v8, v8
	v_add_f32_e32 v3, 1.0, v3
	v_rcp_f32_e32 v3, v3
	v_add_f32_e32 v8, 1.0, v8
	v_rcp_f32_e32 v10, v8
	v_mul_f32_e32 v8, 0xbd38aa3b, v185
	v_exp_f32_e32 v8, v8
	s_nop 0
	v_add_f32_e32 v8, 1.0, v8
	v_rcp_f32_e32 v11, v8
	v_mov_b32_e32 v8, v199
	v_cvt_pk_fp8_f32 v8, v3, v9
	v_mul_f32_e32 v9, 0xbd38aa3b, v179
	v_exp_f32_e32 v9, v9
	v_mul_f32_e32 v3, 0xbd38aa3b, v178
	v_cvt_pk_fp8_f32 v8, v10, v11 op_sel:[0,0,1]
	v_exp_f32_e32 v3, v3
	v_add_f32_e32 v9, 1.0, v9
	v_rcp_f32_e32 v10, v9
	v_mul_f32_e32 v9, 0xbd38aa3b, v180
	v_exp_f32_e32 v9, v9
	v_add_f32_e32 v3, 1.0, v3
	v_rcp_f32_e32 v3, v3
	v_permlane16_swap_b32_e32 v6, v8
	v_add_f32_e32 v9, 1.0, v9
	v_rcp_f32_e32 v11, v9
	v_mul_f32_e32 v9, 0xbd38aa3b, v181
	v_exp_f32_e32 v9, v9
	s_nop 0
	v_add_f32_e32 v9, 1.0, v9
	v_rcp_f32_e32 v12, v9
	v_mov_b32_e32 v9, v199
	v_cvt_pk_fp8_f32 v9, v3, v10
	v_mul_f32_e32 v3, 0xbd38aa3b, v174
	v_exp_f32_e32 v3, v3
	v_cvt_pk_fp8_f32 v9, v11, v12 op_sel:[0,0,1]
	v_add_f32_e32 v3, 1.0, v3
	v_rcp_f32_e32 v3, v3
	v_permlane16_swap_b32_e32 v7, v9
	global_store_dwordx4 v[4:5], v[6:9], off nt
	s_nop 1
	v_mul_f32_e32 v6, 0xbd38aa3b, v175
	v_exp_f32_e32 v6, v6
	s_nop 0
	v_add_f32_e32 v6, 1.0, v6
	v_rcp_f32_e32 v7, v6
	v_mul_f32_e32 v6, 0xbd38aa3b, v176
	v_exp_f32_e32 v6, v6
	s_nop 0
	v_add_f32_e32 v6, 1.0, v6
	v_rcp_f32_e32 v8, v6
	v_mul_f32_e32 v6, 0xbd38aa3b, v177
	v_exp_f32_e32 v6, v6
	s_nop 0
	v_add_f32_e32 v6, 1.0, v6
	v_rcp_f32_e32 v9, v6
	v_mov_b32_e32 v6, v199
	v_cvt_pk_fp8_f32 v6, v3, v7
	v_mul_f32_e32 v7, 0xbd38aa3b, v171
	v_exp_f32_e32 v7, v7
	v_mul_f32_e32 v3, 0xbd38aa3b, v170
	v_cvt_pk_fp8_f32 v6, v8, v9 op_sel:[0,0,1]
	v_exp_f32_e32 v3, v3
	v_add_f32_e32 v7, 1.0, v7
	v_rcp_f32_e32 v8, v7
	v_mul_f32_e32 v7, 0xbd38aa3b, v172
	v_exp_f32_e32 v7, v7
	v_add_f32_e32 v3, 1.0, v3
	v_rcp_f32_e32 v3, v3
	v_add_f32_e32 v7, 1.0, v7
	v_rcp_f32_e32 v9, v7
	v_mul_f32_e32 v7, 0xbd38aa3b, v173
	v_exp_f32_e32 v7, v7
	s_nop 0
	v_add_f32_e32 v7, 1.0, v7
	v_rcp_f32_e32 v10, v7
	v_mov_b32_e32 v7, v199
	v_cvt_pk_fp8_f32 v7, v3, v8
	v_mul_f32_e32 v8, 0xbd38aa3b, v167
	v_exp_f32_e32 v8, v8
	v_mul_f32_e32 v3, 0xbd38aa3b, v166
	v_cvt_pk_fp8_f32 v7, v9, v10 op_sel:[0,0,1]
	v_exp_f32_e32 v3, v3
	v_add_f32_e32 v8, 1.0, v8
	v_rcp_f32_e32 v9, v8
	v_mul_f32_e32 v8, 0xbd38aa3b, v168
	v_exp_f32_e32 v8, v8
	v_add_f32_e32 v3, 1.0, v3
	v_rcp_f32_e32 v3, v3
	v_add_f32_e32 v8, 1.0, v8
	v_rcp_f32_e32 v10, v8
	v_mul_f32_e32 v8, 0xbd38aa3b, v169
	v_exp_f32_e32 v8, v8
	s_nop 0
	v_add_f32_e32 v8, 1.0, v8
	v_rcp_f32_e32 v11, v8
	v_mov_b32_e32 v8, v199
	v_cvt_pk_fp8_f32 v8, v3, v9
	v_mul_f32_e32 v9, 0xbd38aa3b, v163
	v_exp_f32_e32 v9, v9
	v_mul_f32_e32 v3, 0xbd38aa3b, v162
	v_cvt_pk_fp8_f32 v8, v10, v11 op_sel:[0,0,1]
	v_exp_f32_e32 v3, v3
	v_add_f32_e32 v9, 1.0, v9
	v_rcp_f32_e32 v10, v9
	v_mul_f32_e32 v9, 0xbd38aa3b, v164
	v_exp_f32_e32 v9, v9
	v_add_f32_e32 v3, 1.0, v3
	v_rcp_f32_e32 v3, v3
	v_permlane16_swap_b32_e32 v6, v8
	v_add_f32_e32 v9, 1.0, v9
	v_rcp_f32_e32 v11, v9
	v_mul_f32_e32 v9, 0xbd38aa3b, v165
	v_exp_f32_e32 v9, v9
	s_nop 0
	v_add_f32_e32 v9, 1.0, v9
	v_rcp_f32_e32 v12, v9
	v_mov_b32_e32 v9, v199
	v_cvt_pk_fp8_f32 v9, v3, v10
	v_add_co_u32_e32 v10, vcc, s2, v4
	v_mul_f32_e32 v3, 0xbd38aa3b, v158
	v_cvt_pk_fp8_f32 v9, v11, v12 op_sel:[0,0,1]
	v_addc_co_u32_e32 v11, vcc, 0, v5, vcc
	v_exp_f32_e32 v3, v3
	v_permlane16_swap_b32_e32 v7, v9
	global_store_dwordx4 v[10:11], v[6:9], off nt
	v_add_f32_e32 v3, 1.0, v3
	v_rcp_f32_e32 v3, v3
	v_mul_f32_e32 v6, 0xbd38aa3b, v159
	v_exp_f32_e32 v6, v6
	s_mov_b32 s2, 0x10000
	v_add_f32_e32 v6, 1.0, v6
	v_rcp_f32_e32 v7, v6
	v_mul_f32_e32 v6, 0xbd38aa3b, v160
	v_exp_f32_e32 v6, v6
	s_nop 0
	v_add_f32_e32 v6, 1.0, v6
	v_rcp_f32_e32 v8, v6
	v_mul_f32_e32 v6, 0xbd38aa3b, v161
	v_exp_f32_e32 v6, v6
	s_nop 0
	v_add_f32_e32 v6, 1.0, v6
	v_rcp_f32_e32 v9, v6
	v_mov_b32_e32 v6, v199
	v_cvt_pk_fp8_f32 v6, v3, v7
	v_mul_f32_e32 v7, 0xbd38aa3b, v155
	v_exp_f32_e32 v7, v7
	v_mul_f32_e32 v3, 0xbd38aa3b, v154
	v_cvt_pk_fp8_f32 v6, v8, v9 op_sel:[0,0,1]
	v_exp_f32_e32 v3, v3
	v_add_f32_e32 v7, 1.0, v7
	v_rcp_f32_e32 v8, v7
	v_mul_f32_e32 v7, 0xbd38aa3b, v156
	v_exp_f32_e32 v7, v7
	v_add_f32_e32 v3, 1.0, v3
	v_rcp_f32_e32 v3, v3
	v_add_f32_e32 v7, 1.0, v7
	v_rcp_f32_e32 v9, v7
	v_mul_f32_e32 v7, 0xbd38aa3b, v157
	v_exp_f32_e32 v7, v7
	s_nop 0
	v_add_f32_e32 v7, 1.0, v7
	v_rcp_f32_e32 v10, v7
	v_mov_b32_e32 v7, v199
	v_cvt_pk_fp8_f32 v7, v3, v8
	v_mul_f32_e32 v8, 0xbd38aa3b, v151
	v_exp_f32_e32 v8, v8
	v_mul_f32_e32 v3, 0xbd38aa3b, v150
	v_cvt_pk_fp8_f32 v7, v9, v10 op_sel:[0,0,1]
	v_exp_f32_e32 v3, v3
	v_add_f32_e32 v8, 1.0, v8
	v_rcp_f32_e32 v9, v8
	v_mul_f32_e32 v8, 0xbd38aa3b, v152
	v_exp_f32_e32 v8, v8
	v_add_f32_e32 v3, 1.0, v3
	v_rcp_f32_e32 v3, v3
	v_add_f32_e32 v8, 1.0, v8
	v_rcp_f32_e32 v10, v8
	v_mul_f32_e32 v8, 0xbd38aa3b, v153
	v_exp_f32_e32 v8, v8
	s_nop 0
	v_add_f32_e32 v8, 1.0, v8
	v_rcp_f32_e32 v11, v8
	v_mov_b32_e32 v8, v199
	v_cvt_pk_fp8_f32 v8, v3, v9
	v_mul_f32_e32 v9, 0xbd38aa3b, v147
	v_exp_f32_e32 v9, v9
	v_mul_f32_e32 v3, 0xbd38aa3b, v146
	v_cvt_pk_fp8_f32 v8, v10, v11 op_sel:[0,0,1]
	v_exp_f32_e32 v3, v3
	v_add_f32_e32 v9, 1.0, v9
	v_rcp_f32_e32 v10, v9
	v_mul_f32_e32 v9, 0xbd38aa3b, v148
	v_exp_f32_e32 v9, v9
	v_add_f32_e32 v3, 1.0, v3
	v_rcp_f32_e32 v3, v3
	v_permlane16_swap_b32_e32 v6, v8
	v_add_f32_e32 v9, 1.0, v9
	v_rcp_f32_e32 v11, v9
	v_mul_f32_e32 v9, 0xbd38aa3b, v149
	v_exp_f32_e32 v9, v9
	s_nop 0
	v_add_f32_e32 v9, 1.0, v9
	v_rcp_f32_e32 v12, v9
	v_mov_b32_e32 v9, v199
	v_cvt_pk_fp8_f32 v9, v3, v10
	v_add_co_u32_e32 v10, vcc, s2, v4
	v_mul_f32_e32 v3, 0xbd38aa3b, v142
	v_cvt_pk_fp8_f32 v9, v11, v12 op_sel:[0,0,1]
	v_addc_co_u32_e32 v11, vcc, 0, v5, vcc
	v_exp_f32_e32 v3, v3
	v_permlane16_swap_b32_e32 v7, v9
	global_store_dwordx4 v[10:11], v[6:9], off nt
	v_add_f32_e32 v3, 1.0, v3
	v_rcp_f32_e32 v3, v3
	v_mul_f32_e32 v6, 0xbd38aa3b, v143
	v_exp_f32_e32 v6, v6
	s_mov_b32 s2, 0x18000
	v_add_f32_e32 v6, 1.0, v6
	v_rcp_f32_e32 v7, v6
	v_mul_f32_e32 v6, 0xbd38aa3b, v144
	v_exp_f32_e32 v6, v6
	s_nop 0
	v_add_f32_e32 v6, 1.0, v6
	v_rcp_f32_e32 v8, v6
	v_mul_f32_e32 v6, 0xbd38aa3b, v145
	v_exp_f32_e32 v6, v6
	s_nop 0
	v_add_f32_e32 v6, 1.0, v6
	v_rcp_f32_e32 v9, v6
	v_mov_b32_e32 v6, v199
	v_cvt_pk_fp8_f32 v6, v3, v7
	v_mul_f32_e32 v7, 0xbd38aa3b, v139
	v_exp_f32_e32 v7, v7
	v_mul_f32_e32 v3, 0xbd38aa3b, v138
	v_cvt_pk_fp8_f32 v6, v8, v9 op_sel:[0,0,1]
	v_exp_f32_e32 v3, v3
	v_add_f32_e32 v7, 1.0, v7
	v_rcp_f32_e32 v8, v7
	v_mul_f32_e32 v7, 0xbd38aa3b, v140
	v_exp_f32_e32 v7, v7
	v_add_f32_e32 v3, 1.0, v3
	v_rcp_f32_e32 v3, v3
	v_add_f32_e32 v7, 1.0, v7
	v_rcp_f32_e32 v9, v7
	v_mul_f32_e32 v7, 0xbd38aa3b, v141
	v_exp_f32_e32 v7, v7
	s_nop 0
	v_add_f32_e32 v7, 1.0, v7
	v_rcp_f32_e32 v10, v7
	v_mov_b32_e32 v7, v199
	v_cvt_pk_fp8_f32 v7, v3, v8
	v_mul_f32_e32 v8, 0xbd38aa3b, v135
	v_exp_f32_e32 v8, v8
	v_mul_f32_e32 v3, 0xbd38aa3b, v134
	v_cvt_pk_fp8_f32 v7, v9, v10 op_sel:[0,0,1]
	v_exp_f32_e32 v3, v3
	v_add_f32_e32 v8, 1.0, v8
	v_rcp_f32_e32 v9, v8
	v_mul_f32_e32 v8, 0xbd38aa3b, v136
	v_exp_f32_e32 v8, v8
	v_add_f32_e32 v3, 1.0, v3
	v_rcp_f32_e32 v3, v3
	v_add_f32_e32 v8, 1.0, v8
	v_rcp_f32_e32 v10, v8
	v_mul_f32_e32 v8, 0xbd38aa3b, v137
	v_exp_f32_e32 v8, v8
	s_nop 0
	v_add_f32_e32 v8, 1.0, v8
	v_rcp_f32_e32 v11, v8
	v_mov_b32_e32 v8, v199
	v_cvt_pk_fp8_f32 v8, v3, v9
	v_mul_f32_e32 v9, 0xbd38aa3b, v131
	v_exp_f32_e32 v9, v9
	v_mul_f32_e32 v3, 0xbd38aa3b, v130
	v_cvt_pk_fp8_f32 v8, v10, v11 op_sel:[0,0,1]
	v_exp_f32_e32 v3, v3
	v_add_f32_e32 v9, 1.0, v9
	v_rcp_f32_e32 v10, v9
	v_mul_f32_e32 v9, 0xbd38aa3b, v132
	v_exp_f32_e32 v9, v9
	v_add_f32_e32 v3, 1.0, v3
	v_rcp_f32_e32 v3, v3
	v_permlane16_swap_b32_e32 v6, v8
	v_add_f32_e32 v9, 1.0, v9
	v_rcp_f32_e32 v11, v9
	v_mul_f32_e32 v9, 0xbd38aa3b, v133
	v_exp_f32_e32 v9, v9
	s_nop 0
	v_add_f32_e32 v9, 1.0, v9
	v_rcp_f32_e32 v12, v9
	v_mov_b32_e32 v9, v199
	v_cvt_pk_fp8_f32 v9, v3, v10
	v_add_co_u32_e32 v10, vcc, s2, v4
	v_mul_f32_e32 v3, 0xbd38aa3b, v126
	v_cvt_pk_fp8_f32 v9, v11, v12 op_sel:[0,0,1]
	v_addc_co_u32_e32 v11, vcc, 0, v5, vcc
	v_exp_f32_e32 v3, v3
	v_permlane16_swap_b32_e32 v7, v9
	global_store_dwordx4 v[10:11], v[6:9], off nt
	v_add_f32_e32 v3, 1.0, v3
	v_rcp_f32_e32 v3, v3
	v_mul_f32_e32 v6, 0xbd38aa3b, v127
	v_exp_f32_e32 v6, v6
	s_mov_b32 s2, 0x40000
	v_add_f32_e32 v6, 1.0, v6
	v_rcp_f32_e32 v7, v6
	v_mul_f32_e32 v6, 0xbd38aa3b, v128
	v_exp_f32_e32 v6, v6
	s_nop 0
	v_add_f32_e32 v6, 1.0, v6
	v_rcp_f32_e32 v8, v6
	v_mul_f32_e32 v6, 0xbd38aa3b, v129
	v_exp_f32_e32 v6, v6
	s_nop 0
	v_add_f32_e32 v6, 1.0, v6
	v_rcp_f32_e32 v9, v6
	v_mov_b32_e32 v6, v199
	v_cvt_pk_fp8_f32 v6, v3, v7
	v_mul_f32_e32 v7, 0xbd38aa3b, v123
	v_exp_f32_e32 v7, v7
	v_mul_f32_e32 v3, 0xbd38aa3b, v122
	v_cvt_pk_fp8_f32 v6, v8, v9 op_sel:[0,0,1]
	v_exp_f32_e32 v3, v3
	v_add_f32_e32 v7, 1.0, v7
	v_rcp_f32_e32 v8, v7
	v_mul_f32_e32 v7, 0xbd38aa3b, v124
	v_exp_f32_e32 v7, v7
	v_add_f32_e32 v3, 1.0, v3
	v_rcp_f32_e32 v3, v3
	v_add_f32_e32 v7, 1.0, v7
	v_rcp_f32_e32 v9, v7
	v_mul_f32_e32 v7, 0xbd38aa3b, v125
	v_exp_f32_e32 v7, v7
	s_nop 0
	v_add_f32_e32 v7, 1.0, v7
	v_rcp_f32_e32 v10, v7
	v_mov_b32_e32 v7, v199
	v_cvt_pk_fp8_f32 v7, v3, v8
	v_mul_f32_e32 v8, 0xbd38aa3b, v119
	v_exp_f32_e32 v8, v8
	v_mul_f32_e32 v3, 0xbd38aa3b, v118
	v_cvt_pk_fp8_f32 v7, v9, v10 op_sel:[0,0,1]
	v_exp_f32_e32 v3, v3
	v_add_f32_e32 v8, 1.0, v8
	v_rcp_f32_e32 v9, v8
	v_mul_f32_e32 v8, 0xbd38aa3b, v120
	v_exp_f32_e32 v8, v8
	v_add_f32_e32 v3, 1.0, v3
	v_rcp_f32_e32 v3, v3
	v_add_f32_e32 v8, 1.0, v8
	v_rcp_f32_e32 v10, v8
	v_mul_f32_e32 v8, 0xbd38aa3b, v121
	v_exp_f32_e32 v8, v8
	s_nop 0
	v_add_f32_e32 v8, 1.0, v8
	v_rcp_f32_e32 v11, v8
	v_mov_b32_e32 v8, v199
	v_cvt_pk_fp8_f32 v8, v3, v9
	v_mul_f32_e32 v9, 0xbd38aa3b, v115
	v_exp_f32_e32 v9, v9
	v_mul_f32_e32 v3, 0xbd38aa3b, v114
	v_cvt_pk_fp8_f32 v8, v10, v11 op_sel:[0,0,1]
	v_exp_f32_e32 v3, v3
	v_add_f32_e32 v9, 1.0, v9
	v_rcp_f32_e32 v10, v9
	v_mul_f32_e32 v9, 0xbd38aa3b, v116
	v_exp_f32_e32 v9, v9
	v_add_f32_e32 v3, 1.0, v3
	v_rcp_f32_e32 v3, v3
	v_permlane16_swap_b32_e32 v6, v8
	v_add_f32_e32 v9, 1.0, v9
	v_rcp_f32_e32 v11, v9
	v_mul_f32_e32 v9, 0xbd38aa3b, v117
	v_exp_f32_e32 v9, v9
	s_nop 0
	v_add_f32_e32 v9, 1.0, v9
	v_rcp_f32_e32 v12, v9
	v_mov_b32_e32 v9, v199
	v_cvt_pk_fp8_f32 v9, v3, v10
	v_add_co_u32_e32 v10, vcc, s2, v4
	v_mul_f32_e32 v3, 0xbd38aa3b, v110
	v_cvt_pk_fp8_f32 v9, v11, v12 op_sel:[0,0,1]
	v_addc_co_u32_e32 v11, vcc, 0, v5, vcc
	v_exp_f32_e32 v3, v3
	v_permlane16_swap_b32_e32 v7, v9
	global_store_dwordx4 v[10:11], v[6:9], off nt
	v_add_f32_e32 v3, 1.0, v3
	v_rcp_f32_e32 v3, v3
	v_mul_f32_e32 v6, 0xbd38aa3b, v111
	v_exp_f32_e32 v6, v6
	s_mov_b32 s2, 0x48000
	v_add_f32_e32 v6, 1.0, v6
	v_rcp_f32_e32 v7, v6
	v_mul_f32_e32 v6, 0xbd38aa3b, v112
	v_exp_f32_e32 v6, v6
	s_nop 0
	v_add_f32_e32 v6, 1.0, v6
	v_rcp_f32_e32 v8, v6
	v_mul_f32_e32 v6, 0xbd38aa3b, v113
	v_exp_f32_e32 v6, v6
	s_nop 0
	v_add_f32_e32 v6, 1.0, v6
	v_rcp_f32_e32 v9, v6
	v_mov_b32_e32 v6, v199
	v_cvt_pk_fp8_f32 v6, v3, v7
	v_mul_f32_e32 v7, 0xbd38aa3b, v107
	v_exp_f32_e32 v7, v7
	v_mul_f32_e32 v3, 0xbd38aa3b, v106
	v_cvt_pk_fp8_f32 v6, v8, v9 op_sel:[0,0,1]
	v_exp_f32_e32 v3, v3
	v_add_f32_e32 v7, 1.0, v7
	v_rcp_f32_e32 v8, v7
	v_mul_f32_e32 v7, 0xbd38aa3b, v108
	v_exp_f32_e32 v7, v7
	v_add_f32_e32 v3, 1.0, v3
	v_rcp_f32_e32 v3, v3
	v_add_f32_e32 v7, 1.0, v7
	v_rcp_f32_e32 v9, v7
	v_mul_f32_e32 v7, 0xbd38aa3b, v109
	v_exp_f32_e32 v7, v7
	s_nop 0
	v_add_f32_e32 v7, 1.0, v7
	v_rcp_f32_e32 v10, v7
	v_mov_b32_e32 v7, v199
	v_cvt_pk_fp8_f32 v7, v3, v8
	v_mul_f32_e32 v8, 0xbd38aa3b, v95
	v_exp_f32_e32 v8, v8
	v_mul_f32_e32 v3, 0xbd38aa3b, v94
	v_cvt_pk_fp8_f32 v7, v9, v10 op_sel:[0,0,1]
	v_exp_f32_e32 v3, v3
	v_add_f32_e32 v8, 1.0, v8
	v_rcp_f32_e32 v9, v8
	v_mul_f32_e32 v8, 0xbd38aa3b, v96
	v_exp_f32_e32 v8, v8
	v_add_f32_e32 v3, 1.0, v3
	v_rcp_f32_e32 v3, v3
	v_add_f32_e32 v8, 1.0, v8
	v_rcp_f32_e32 v10, v8
	v_mul_f32_e32 v8, 0xbd38aa3b, v97
	v_exp_f32_e32 v8, v8
	s_nop 0
	v_add_f32_e32 v8, 1.0, v8
	v_rcp_f32_e32 v11, v8
	v_mov_b32_e32 v8, v199
	v_cvt_pk_fp8_f32 v8, v3, v9
	v_mul_f32_e32 v9, 0xbd38aa3b, v91
	v_exp_f32_e32 v9, v9
	v_mul_f32_e32 v3, 0xbd38aa3b, v90
	v_cvt_pk_fp8_f32 v8, v10, v11 op_sel:[0,0,1]
	v_exp_f32_e32 v3, v3
	v_add_f32_e32 v9, 1.0, v9
	v_rcp_f32_e32 v10, v9
	v_mul_f32_e32 v9, 0xbd38aa3b, v92
	v_exp_f32_e32 v9, v9
	v_add_f32_e32 v3, 1.0, v3
	v_rcp_f32_e32 v3, v3
	v_permlane16_swap_b32_e32 v6, v8
	v_add_f32_e32 v9, 1.0, v9
	v_rcp_f32_e32 v11, v9
	v_mul_f32_e32 v9, 0xbd38aa3b, v93
	v_exp_f32_e32 v9, v9
	s_nop 0
	v_add_f32_e32 v9, 1.0, v9
	v_rcp_f32_e32 v12, v9
	v_mov_b32_e32 v9, v199
	v_cvt_pk_fp8_f32 v9, v3, v10
	v_add_co_u32_e32 v10, vcc, s2, v4
	v_mul_f32_e32 v3, 0xbd38aa3b, v78
	v_cvt_pk_fp8_f32 v9, v11, v12 op_sel:[0,0,1]
	v_addc_co_u32_e32 v11, vcc, 0, v5, vcc
	v_exp_f32_e32 v3, v3
	v_permlane16_swap_b32_e32 v7, v9
	global_store_dwordx4 v[10:11], v[6:9], off nt
	v_add_f32_e32 v3, 1.0, v3
	v_rcp_f32_e32 v3, v3
	v_mul_f32_e32 v6, 0xbd38aa3b, v79
	v_exp_f32_e32 v6, v6
	s_mov_b32 s2, 0x50000
	v_add_f32_e32 v6, 1.0, v6
	v_rcp_f32_e32 v7, v6
	v_mul_f32_e32 v6, 0xbd38aa3b, v80
	v_exp_f32_e32 v6, v6
	s_nop 0
	v_add_f32_e32 v6, 1.0, v6
	v_rcp_f32_e32 v8, v6
	v_mul_f32_e32 v6, 0xbd38aa3b, v81
	v_exp_f32_e32 v6, v6
	s_nop 0
	v_add_f32_e32 v6, 1.0, v6
	v_rcp_f32_e32 v9, v6
	v_mov_b32_e32 v6, v199
	v_cvt_pk_fp8_f32 v6, v3, v7
	v_mul_f32_e32 v7, 0xbd38aa3b, v75
	v_exp_f32_e32 v7, v7
	v_mul_f32_e32 v3, 0xbd38aa3b, v74
	v_cvt_pk_fp8_f32 v6, v8, v9 op_sel:[0,0,1]
	v_exp_f32_e32 v3, v3
	v_add_f32_e32 v7, 1.0, v7
	v_rcp_f32_e32 v8, v7
	v_mul_f32_e32 v7, 0xbd38aa3b, v76
	v_exp_f32_e32 v7, v7
	v_add_f32_e32 v3, 1.0, v3
	v_rcp_f32_e32 v3, v3
	v_add_f32_e32 v7, 1.0, v7
	v_rcp_f32_e32 v9, v7
	v_mul_f32_e32 v7, 0xbd38aa3b, v77
	v_exp_f32_e32 v7, v7
	s_nop 0
	v_add_f32_e32 v7, 1.0, v7
	v_rcp_f32_e32 v10, v7
	v_mov_b32_e32 v7, v199
	v_cvt_pk_fp8_f32 v7, v3, v8
	v_mul_f32_e32 v8, 0xbd38aa3b, v99
	v_exp_f32_e32 v8, v8
	v_mul_f32_e32 v3, 0xbd38aa3b, v98
	v_cvt_pk_fp8_f32 v7, v9, v10 op_sel:[0,0,1]
	v_exp_f32_e32 v3, v3
	v_add_f32_e32 v8, 1.0, v8
	v_rcp_f32_e32 v9, v8
	v_mul_f32_e32 v8, 0xbd38aa3b, v100
	v_exp_f32_e32 v8, v8
	v_add_f32_e32 v3, 1.0, v3
	v_rcp_f32_e32 v3, v3
	v_add_f32_e32 v8, 1.0, v8
	v_rcp_f32_e32 v10, v8
	v_mul_f32_e32 v8, 0xbd38aa3b, v101
	v_exp_f32_e32 v8, v8
	s_nop 0
	v_add_f32_e32 v8, 1.0, v8
	v_rcp_f32_e32 v11, v8
	v_mov_b32_e32 v8, v199
	v_cvt_pk_fp8_f32 v8, v3, v9
	v_mul_f32_e32 v9, 0xbd38aa3b, v103
	v_exp_f32_e32 v9, v9
	v_mul_f32_e32 v3, 0xbd38aa3b, v102
	v_cvt_pk_fp8_f32 v8, v10, v11 op_sel:[0,0,1]
	v_exp_f32_e32 v3, v3
	v_add_f32_e32 v9, 1.0, v9
	v_rcp_f32_e32 v10, v9
	v_mul_f32_e32 v9, 0xbd38aa3b, v104
	v_exp_f32_e32 v9, v9
	v_add_f32_e32 v3, 1.0, v3
	v_rcp_f32_e32 v3, v3
	v_permlane16_swap_b32_e32 v6, v8
	v_add_f32_e32 v9, 1.0, v9
	v_rcp_f32_e32 v11, v9
	v_mul_f32_e32 v9, 0xbd38aa3b, v105
	v_exp_f32_e32 v9, v9
	s_nop 0
	v_add_f32_e32 v9, 1.0, v9
	v_rcp_f32_e32 v12, v9
	v_mov_b32_e32 v9, v199
	v_cvt_pk_fp8_f32 v9, v3, v10
	v_add_co_u32_e32 v10, vcc, s2, v4
	v_mul_f32_e32 v3, 0xbd38aa3b, v70
	v_cvt_pk_fp8_f32 v9, v11, v12 op_sel:[0,0,1]
	v_addc_co_u32_e32 v11, vcc, 0, v5, vcc
	v_exp_f32_e32 v3, v3
	v_permlane16_swap_b32_e32 v7, v9
	global_store_dwordx4 v[10:11], v[6:9], off nt
	v_add_f32_e32 v3, 1.0, v3
	v_rcp_f32_e32 v3, v3
	v_mul_f32_e32 v6, 0xbd38aa3b, v71
	v_exp_f32_e32 v6, v6
	v_add_co_u32_e32 v4, vcc, 0x58000, v4
	v_add_f32_e32 v6, 1.0, v6
	v_rcp_f32_e32 v7, v6
	v_mul_f32_e32 v6, 0xbd38aa3b, v72
	v_exp_f32_e32 v6, v6
	v_addc_co_u32_e32 v5, vcc, 0, v5, vcc
	v_add_f32_e32 v6, 1.0, v6
	v_rcp_f32_e32 v8, v6
	v_mul_f32_e32 v6, 0xbd38aa3b, v73
	v_exp_f32_e32 v6, v6
	s_nop 0
	v_add_f32_e32 v6, 1.0, v6
	v_rcp_f32_e32 v9, v6
	v_mov_b32_e32 v6, v199
	v_cvt_pk_fp8_f32 v6, v3, v7
	v_mul_f32_e32 v7, 0xbd38aa3b, v67
	v_exp_f32_e32 v7, v7
	v_mul_f32_e32 v3, 0xbd38aa3b, v66
	v_cvt_pk_fp8_f32 v6, v8, v9 op_sel:[0,0,1]
	v_exp_f32_e32 v3, v3
	v_add_f32_e32 v7, 1.0, v7
	v_rcp_f32_e32 v8, v7
	v_mul_f32_e32 v7, 0xbd38aa3b, v68
	v_exp_f32_e32 v7, v7
	v_add_f32_e32 v3, 1.0, v3
	v_rcp_f32_e32 v3, v3
	v_add_f32_e32 v7, 1.0, v7
	v_rcp_f32_e32 v9, v7
	v_mul_f32_e32 v7, 0xbd38aa3b, v69
	v_exp_f32_e32 v7, v7
	s_nop 0
	v_add_f32_e32 v7, 1.0, v7
	v_rcp_f32_e32 v10, v7
	v_mov_b32_e32 v7, v199
	v_cvt_pk_fp8_f32 v7, v3, v8
	v_mul_f32_e32 v8, 0xbd38aa3b, v83
	v_exp_f32_e32 v8, v8
	v_mul_f32_e32 v3, 0xbd38aa3b, v82
	v_cvt_pk_fp8_f32 v7, v9, v10 op_sel:[0,0,1]
	v_exp_f32_e32 v3, v3
	v_add_f32_e32 v8, 1.0, v8
	v_rcp_f32_e32 v9, v8
	v_mul_f32_e32 v8, 0xbd38aa3b, v84
	v_exp_f32_e32 v8, v8
	v_add_f32_e32 v3, 1.0, v3
	v_rcp_f32_e32 v3, v3
	v_add_f32_e32 v8, 1.0, v8
	v_rcp_f32_e32 v10, v8
	v_mul_f32_e32 v8, 0xbd38aa3b, v85
	v_exp_f32_e32 v8, v8
	s_nop 0
	v_add_f32_e32 v8, 1.0, v8
	v_rcp_f32_e32 v11, v8
	v_mov_b32_e32 v8, v199
	v_cvt_pk_fp8_f32 v8, v3, v9
	v_mul_f32_e32 v9, 0xbd38aa3b, v87
	v_exp_f32_e32 v9, v9
	v_mul_f32_e32 v3, 0xbd38aa3b, v86
	v_cvt_pk_fp8_f32 v8, v10, v11 op_sel:[0,0,1]
	v_exp_f32_e32 v3, v3
	v_add_f32_e32 v9, 1.0, v9
	v_rcp_f32_e32 v10, v9
	v_mul_f32_e32 v9, 0xbd38aa3b, v88
	v_exp_f32_e32 v9, v9
	v_add_f32_e32 v3, 1.0, v3
	v_rcp_f32_e32 v3, v3
	v_permlane16_swap_b32_e32 v6, v8
	v_add_f32_e32 v9, 1.0, v9
	v_rcp_f32_e32 v11, v9
	v_mul_f32_e32 v9, 0xbd38aa3b, v89
	v_exp_f32_e32 v9, v9
	s_nop 0
	v_add_f32_e32 v9, 1.0, v9
	v_rcp_f32_e32 v12, v9
	v_mov_b32_e32 v9, v199
	v_cvt_pk_fp8_f32 v9, v3, v10
	v_cvt_pk_fp8_f32 v9, v11, v12 op_sel:[0,0,1]
	s_nop 1
	v_permlane16_swap_b32_e32 v7, v9
	global_store_dwordx4 v[4:5], v[6:9], off nt
.LBB0_151:
	s_andn2_b64 vcc, exec, s[40:41]
	s_cbranch_vccnz .LBB0_153
	v_pk_mul_f32 v[8:9], v[190:191], s[36:37] op_sel_hi:[1,0]
	v_pk_mul_f32 v[10:11], v[186:187], s[36:37] op_sel_hi:[1,0]
	v_mov_b32_e32 v6, v199
	v_mov_b32_e32 v7, v199
	v_cvt_pk_fp8_f32 v6, v8, v9
	v_cvt_pk_fp8_f32 v7, v10, v11
	v_pk_mul_f32 v[8:9], v[192:193], s[36:37] op_sel_hi:[1,0]
	v_pk_mul_f32 v[10:11], v[188:189], s[36:37] op_sel_hi:[1,0]
	v_cvt_pk_fp8_f32 v6, v8, v9 op_sel:[0,0,1]
	v_cvt_pk_fp8_f32 v7, v10, v11 op_sel:[0,0,1]
	v_pk_mul_f32 v[10:11], v[182:183], s[36:37] op_sel_hi:[1,0]
	v_pk_mul_f32 v[12:13], v[178:179], s[36:37] op_sel_hi:[1,0]
	v_mov_b32_e32 v8, v199
	v_mov_b32_e32 v9, v199
	v_cvt_pk_fp8_f32 v8, v10, v11
	v_cvt_pk_fp8_f32 v9, v12, v13
	s_add_u32 s2, s62, s7
	v_and_b32_e32 v3, 1, v50
	v_lshlrev_b32_e32 v4, 3, v50
	s_addc_u32 s38, s63, s46
	v_add_u32_e32 v5, 24, v4
	v_cmp_eq_u32_e32 vcc, 0, v3
	v_pk_mul_f32 v[10:11], v[184:185], s[36:37] op_sel_hi:[1,0]
	v_pk_mul_f32 v[12:13], v[180:181], s[36:37] op_sel_hi:[1,0]
	s_add_u32 s40, s2, s89
	v_cndmask_b32_e32 v4, v5, v4, vcc
	v_cvt_pk_fp8_f32 v8, v10, v11 op_sel:[0,0,1]
	v_cvt_pk_fp8_f32 v9, v12, v13 op_sel:[0,0,1]
	s_addc_u32 s41, s38, 0
	v_ashrrev_i32_e32 v5, 31, v4
	v_add_u32_e32 v3, s50, v2
	v_lshl_add_u64 v[4:5], s[40:41], 0, v[4:5]
	v_ashrrev_i32_e32 v14, 31, v3
	v_mad_u64_u32 v[10:11], s[40:41], s58, v3, v[4:5]
	v_mul_lo_u32 v12, s58, v14
	v_mul_lo_u32 v13, s59, v3
	v_add3_u32 v11, v13, v11, v12
	v_permlane16_swap_b32_e32 v6, v8
	v_permlane16_swap_b32_e32 v7, v9
	global_store_dwordx4 v[10:11], v[6:9], off nt
	v_pk_mul_f32 v[10:11], v[170:171], s[36:37] op_sel_hi:[1,0]
	v_pk_mul_f32 v[12:13], v[162:163], s[36:37] op_sel_hi:[1,0]
	v_pk_mul_f32 v[8:9], v[174:175], s[36:37] op_sel_hi:[1,0]
	v_mov_b32_e32 v6, v199
	v_mov_b32_e32 v7, v199
	v_cvt_pk_fp8_f32 v6, v8, v9
	v_cvt_pk_fp8_f32 v7, v10, v11
	v_pk_mul_f32 v[8:9], v[176:177], s[36:37] op_sel_hi:[1,0]
	v_pk_mul_f32 v[10:11], v[172:173], s[36:37] op_sel_hi:[1,0]
	v_cvt_pk_fp8_f32 v6, v8, v9 op_sel:[0,0,1]
	v_cvt_pk_fp8_f32 v7, v10, v11 op_sel:[0,0,1]
	v_pk_mul_f32 v[10:11], v[166:167], s[36:37] op_sel_hi:[1,0]
	v_mov_b32_e32 v8, v199
	v_mov_b32_e32 v9, v199
	v_cvt_pk_fp8_f32 v8, v10, v11
	v_cvt_pk_fp8_f32 v9, v12, v13
	v_pk_mul_f32 v[10:11], v[168:169], s[36:37] op_sel_hi:[1,0]
	v_pk_mul_f32 v[12:13], v[164:165], s[36:37] op_sel_hi:[1,0]
	v_cvt_pk_fp8_f32 v8, v10, v11 op_sel:[0,0,1]
	v_cvt_pk_fp8_f32 v9, v12, v13 op_sel:[0,0,1]
	v_add_u32_e32 v14, 16, v3
	v_ashrrev_i32_e32 v15, 31, v14
	v_mad_u64_u32 v[10:11], s[40:41], s58, v14, v[4:5]
	v_mul_lo_u32 v12, s58, v15
	v_mul_lo_u32 v13, s59, v14
	v_add3_u32 v11, v13, v11, v12
	v_permlane16_swap_b32_e32 v6, v8
	v_permlane16_swap_b32_e32 v7, v9
	global_store_dwordx4 v[10:11], v[6:9], off nt
	v_pk_mul_f32 v[10:11], v[154:155], s[36:37] op_sel_hi:[1,0]
	v_pk_mul_f32 v[12:13], v[146:147], s[36:37] op_sel_hi:[1,0]
	v_pk_mul_f32 v[8:9], v[158:159], s[36:37] op_sel_hi:[1,0]
	v_mov_b32_e32 v6, v199
	v_mov_b32_e32 v7, v199
	v_cvt_pk_fp8_f32 v6, v8, v9
	v_cvt_pk_fp8_f32 v7, v10, v11
	v_pk_mul_f32 v[8:9], v[160:161], s[36:37] op_sel_hi:[1,0]
	v_pk_mul_f32 v[10:11], v[156:157], s[36:37] op_sel_hi:[1,0]
	v_cvt_pk_fp8_f32 v6, v8, v9 op_sel:[0,0,1]
	v_cvt_pk_fp8_f32 v7, v10, v11 op_sel:[0,0,1]
	v_pk_mul_f32 v[10:11], v[150:151], s[36:37] op_sel_hi:[1,0]
	v_mov_b32_e32 v8, v199
	v_mov_b32_e32 v9, v199
	v_cvt_pk_fp8_f32 v8, v10, v11
	v_cvt_pk_fp8_f32 v9, v12, v13
	v_pk_mul_f32 v[10:11], v[152:153], s[36:37] op_sel_hi:[1,0]
	v_pk_mul_f32 v[12:13], v[148:149], s[36:37] op_sel_hi:[1,0]
	v_cvt_pk_fp8_f32 v8, v10, v11 op_sel:[0,0,1]
	v_cvt_pk_fp8_f32 v9, v12, v13 op_sel:[0,0,1]
	v_add_u32_e32 v14, 32, v3
	v_ashrrev_i32_e32 v15, 31, v14
	v_mad_u64_u32 v[10:11], s[40:41], s58, v14, v[4:5]
	v_mul_lo_u32 v12, s58, v15
	v_mul_lo_u32 v13, s59, v14
	v_add3_u32 v11, v13, v11, v12
	v_permlane16_swap_b32_e32 v6, v8
	v_permlane16_swap_b32_e32 v7, v9
	global_store_dwordx4 v[10:11], v[6:9], off nt
	v_pk_mul_f32 v[10:11], v[138:139], s[36:37] op_sel_hi:[1,0]
	v_pk_mul_f32 v[12:13], v[130:131], s[36:37] op_sel_hi:[1,0]
	v_pk_mul_f32 v[8:9], v[142:143], s[36:37] op_sel_hi:[1,0]
	v_mov_b32_e32 v6, v199
	v_mov_b32_e32 v7, v199
	v_cvt_pk_fp8_f32 v6, v8, v9
	v_cvt_pk_fp8_f32 v7, v10, v11
	v_pk_mul_f32 v[8:9], v[144:145], s[36:37] op_sel_hi:[1,0]
	v_pk_mul_f32 v[10:11], v[140:141], s[36:37] op_sel_hi:[1,0]
	v_cvt_pk_fp8_f32 v6, v8, v9 op_sel:[0,0,1]
	v_cvt_pk_fp8_f32 v7, v10, v11 op_sel:[0,0,1]
	v_pk_mul_f32 v[10:11], v[134:135], s[36:37] op_sel_hi:[1,0]
	v_mov_b32_e32 v8, v199
	v_mov_b32_e32 v9, v199
	v_cvt_pk_fp8_f32 v8, v10, v11
	v_cvt_pk_fp8_f32 v9, v12, v13
	v_pk_mul_f32 v[10:11], v[136:137], s[36:37] op_sel_hi:[1,0]
	v_pk_mul_f32 v[12:13], v[132:133], s[36:37] op_sel_hi:[1,0]
	v_cvt_pk_fp8_f32 v8, v10, v11 op_sel:[0,0,1]
	v_cvt_pk_fp8_f32 v9, v12, v13 op_sel:[0,0,1]
	v_add_u32_e32 v14, 48, v3
	v_ashrrev_i32_e32 v15, 31, v14
	v_mad_u64_u32 v[10:11], s[40:41], s58, v14, v[4:5]
	v_mul_lo_u32 v12, s58, v15
	v_mul_lo_u32 v13, s59, v14
	v_add3_u32 v11, v13, v11, v12
	v_permlane16_swap_b32_e32 v6, v8
	v_permlane16_swap_b32_e32 v7, v9
	global_store_dwordx4 v[10:11], v[6:9], off nt
	v_pk_mul_f32 v[10:11], v[122:123], s[36:37] op_sel_hi:[1,0]
	v_pk_mul_f32 v[12:13], v[114:115], s[36:37] op_sel_hi:[1,0]
	v_pk_mul_f32 v[8:9], v[126:127], s[36:37] op_sel_hi:[1,0]
	v_mov_b32_e32 v6, v199
	v_mov_b32_e32 v7, v199
	v_cvt_pk_fp8_f32 v6, v8, v9
	v_cvt_pk_fp8_f32 v7, v10, v11
	v_pk_mul_f32 v[8:9], v[128:129], s[36:37] op_sel_hi:[1,0]
	v_pk_mul_f32 v[10:11], v[124:125], s[36:37] op_sel_hi:[1,0]
	v_cvt_pk_fp8_f32 v6, v8, v9 op_sel:[0,0,1]
	v_cvt_pk_fp8_f32 v7, v10, v11 op_sel:[0,0,1]
	v_pk_mul_f32 v[10:11], v[118:119], s[36:37] op_sel_hi:[1,0]
	v_mov_b32_e32 v8, v199
	v_mov_b32_e32 v9, v199
	v_cvt_pk_fp8_f32 v8, v10, v11
	v_cvt_pk_fp8_f32 v9, v12, v13
	v_pk_mul_f32 v[10:11], v[120:121], s[36:37] op_sel_hi:[1,0]
	v_pk_mul_f32 v[12:13], v[116:117], s[36:37] op_sel_hi:[1,0]
	v_cvt_pk_fp8_f32 v8, v10, v11 op_sel:[0,0,1]
	v_cvt_pk_fp8_f32 v9, v12, v13 op_sel:[0,0,1]
	v_add_u32_e32 v14, 0x80, v3
	v_ashrrev_i32_e32 v15, 31, v14
	v_mad_u64_u32 v[10:11], s[40:41], s58, v14, v[4:5]
	v_mul_lo_u32 v12, s58, v15
	v_mul_lo_u32 v13, s59, v14
	v_add3_u32 v11, v13, v11, v12
	v_permlane16_swap_b32_e32 v6, v8
	v_permlane16_swap_b32_e32 v7, v9
	global_store_dwordx4 v[10:11], v[6:9], off nt
	v_pk_mul_f32 v[10:11], v[106:107], s[36:37] op_sel_hi:[1,0]
	v_pk_mul_f32 v[12:13], v[90:91], s[36:37] op_sel_hi:[1,0]
	v_pk_mul_f32 v[8:9], v[110:111], s[36:37] op_sel_hi:[1,0]
	v_mov_b32_e32 v6, v199
	v_mov_b32_e32 v7, v199
	v_cvt_pk_fp8_f32 v6, v8, v9
	v_cvt_pk_fp8_f32 v7, v10, v11
	v_pk_mul_f32 v[8:9], v[112:113], s[36:37] op_sel_hi:[1,0]
	v_pk_mul_f32 v[10:11], v[108:109], s[36:37] op_sel_hi:[1,0]
	v_cvt_pk_fp8_f32 v6, v8, v9 op_sel:[0,0,1]
	v_cvt_pk_fp8_f32 v7, v10, v11 op_sel:[0,0,1]
	v_pk_mul_f32 v[10:11], v[94:95], s[36:37] op_sel_hi:[1,0]
	v_mov_b32_e32 v8, v199
	v_mov_b32_e32 v9, v199
	v_cvt_pk_fp8_f32 v8, v10, v11
	v_cvt_pk_fp8_f32 v9, v12, v13
	v_pk_mul_f32 v[10:11], v[96:97], s[36:37] op_sel_hi:[1,0]
	v_pk_mul_f32 v[12:13], v[92:93], s[36:37] op_sel_hi:[1,0]
	v_cvt_pk_fp8_f32 v8, v10, v11 op_sel:[0,0,1]
	v_cvt_pk_fp8_f32 v9, v12, v13 op_sel:[0,0,1]
	v_add_u32_e32 v14, 0x90, v3
	v_ashrrev_i32_e32 v15, 31, v14
	v_mad_u64_u32 v[10:11], s[40:41], s58, v14, v[4:5]
	v_mul_lo_u32 v12, s58, v15
	v_mul_lo_u32 v13, s59, v14
	v_add3_u32 v11, v13, v11, v12
	v_permlane16_swap_b32_e32 v6, v8
	v_permlane16_swap_b32_e32 v7, v9
	global_store_dwordx4 v[10:11], v[6:9], off nt
	v_pk_mul_f32 v[10:11], v[74:75], s[36:37] op_sel_hi:[1,0]
	v_pk_mul_f32 v[12:13], v[102:103], s[36:37] op_sel_hi:[1,0]
	v_pk_mul_f32 v[8:9], v[78:79], s[36:37] op_sel_hi:[1,0]
	v_mov_b32_e32 v6, v199
	v_mov_b32_e32 v7, v199
	v_cvt_pk_fp8_f32 v6, v8, v9
	v_cvt_pk_fp8_f32 v7, v10, v11
	v_pk_mul_f32 v[8:9], v[80:81], s[36:37] op_sel_hi:[1,0]
	v_pk_mul_f32 v[10:11], v[76:77], s[36:37] op_sel_hi:[1,0]
	v_cvt_pk_fp8_f32 v6, v8, v9 op_sel:[0,0,1]
	v_cvt_pk_fp8_f32 v7, v10, v11 op_sel:[0,0,1]
	v_pk_mul_f32 v[10:11], v[98:99], s[36:37] op_sel_hi:[1,0]
	v_mov_b32_e32 v8, v199
	v_mov_b32_e32 v9, v199
	v_cvt_pk_fp8_f32 v8, v10, v11
	v_cvt_pk_fp8_f32 v9, v12, v13
	v_pk_mul_f32 v[10:11], v[100:101], s[36:37] op_sel_hi:[1,0]
	v_pk_mul_f32 v[12:13], v[104:105], s[36:37] op_sel_hi:[1,0]
	v_cvt_pk_fp8_f32 v8, v10, v11 op_sel:[0,0,1]
	v_cvt_pk_fp8_f32 v9, v12, v13 op_sel:[0,0,1]
	v_add_u32_e32 v14, 0xa0, v3
	v_ashrrev_i32_e32 v15, 31, v14
	v_mad_u64_u32 v[10:11], s[40:41], s58, v14, v[4:5]
	v_mul_lo_u32 v12, s58, v15
	v_mul_lo_u32 v13, s59, v14
	v_add3_u32 v11, v13, v11, v12
	v_permlane16_swap_b32_e32 v6, v8
	v_permlane16_swap_b32_e32 v7, v9
	global_store_dwordx4 v[10:11], v[6:9], off nt
	v_pk_mul_f32 v[10:11], v[66:67], s[36:37] op_sel_hi:[1,0]
	v_pk_mul_f32 v[12:13], v[86:87], s[36:37] op_sel_hi:[1,0]
	v_pk_mul_f32 v[8:9], v[70:71], s[36:37] op_sel_hi:[1,0]
	v_mov_b32_e32 v6, v199
	v_mov_b32_e32 v7, v199
	v_cvt_pk_fp8_f32 v6, v8, v9
	v_cvt_pk_fp8_f32 v7, v10, v11
	v_pk_mul_f32 v[8:9], v[72:73], s[36:37] op_sel_hi:[1,0]
	v_pk_mul_f32 v[10:11], v[68:69], s[36:37] op_sel_hi:[1,0]
	v_cvt_pk_fp8_f32 v6, v8, v9 op_sel:[0,0,1]
	v_cvt_pk_fp8_f32 v7, v10, v11 op_sel:[0,0,1]
	v_pk_mul_f32 v[10:11], v[82:83], s[36:37] op_sel_hi:[1,0]
	v_mov_b32_e32 v8, v199
	v_mov_b32_e32 v9, v199
	v_cvt_pk_fp8_f32 v8, v10, v11
	v_cvt_pk_fp8_f32 v9, v12, v13
	v_pk_mul_f32 v[10:11], v[84:85], s[36:37] op_sel_hi:[1,0]
	v_pk_mul_f32 v[12:13], v[88:89], s[36:37] op_sel_hi:[1,0]
	v_cvt_pk_fp8_f32 v8, v10, v11 op_sel:[0,0,1]
	v_cvt_pk_fp8_f32 v9, v12, v13 op_sel:[0,0,1]
	v_add_u32_e32 v3, 0xb0, v3
	v_ashrrev_i32_e32 v14, 31, v3
	v_mad_u64_u32 v[4:5], s[40:41], s58, v3, v[4:5]
	v_mul_lo_u32 v10, s58, v14
	v_mul_lo_u32 v3, s59, v3
	v_add3_u32 v5, v3, v5, v10
	v_permlane16_swap_b32_e32 v6, v8
	v_permlane16_swap_b32_e32 v7, v9
	global_store_dwordx4 v[4:5], v[6:9], off nt

.LBB0_156:
	v_add_u32_e32 v201, s50, v2
	v_lshlrev_b32_e32 v2, 2, v2
	v_and_b32_e32 v6, 60, v2
	v_lshrrev_b32_e32 v2, 2, v201
	v_and_b32_e32 v2, 0x1fc, v2
	v_add_u32_e32 v2, v2, v50
	v_lshl_or_b32 v2, v2, 6, v6
	v_ashrrev_i32_e32 v3, 31, v2
	v_lshl_add_u64 v[2:3], v[2:3], 2, s[24:25]
	v_add_co_u32_e32 v4, vcc, 0x20000, v2
	v_add_u32_e32 v221, 16, v201
	s_nop 0
	v_addc_co_u32_e32 v5, vcc, 0, v3, vcc
	global_load_dwordx4 v[56:59], v[2:3], off
	global_load_dwordx4 v[60:63], v[4:5], off
	v_lshrrev_b32_e32 v2, 2, v221
	v_and_b32_e32 v2, 0x1fc, v2
	v_add_u32_e32 v2, v2, v50
	v_lshl_or_b32 v2, v2, 6, v6
	v_ashrrev_i32_e32 v3, 31, v2
	v_lshl_add_u64 v[2:3], v[2:3], 2, s[24:25]
	v_add_co_u32_e32 v4, vcc, s90, v2
	v_add_u32_e32 v236, 32, v201
	s_nop 0
	v_addc_co_u32_e32 v5, vcc, 0, v3, vcc
	global_load_dwordx4 v[204:207], v[2:3], off
	global_load_dwordx4 v[208:211], v[4:5], off
	v_lshrrev_b32_e32 v2, 2, v236
	v_and_b32_e32 v2, 0x1fc, v2
	v_add_u32_e32 v2, v2, v50
	v_lshl_or_b32 v2, v2, 6, v6
	v_ashrrev_i32_e32 v3, 31, v2
	v_lshl_add_u64 v[2:3], v[2:3], 2, s[24:25]
	v_add_co_u32_e32 v4, vcc, s90, v2
	v_add_u32_e32 v237, 48, v201
	s_nop 0
	v_addc_co_u32_e32 v5, vcc, 0, v3, vcc
	global_load_dwordx4 v[46:49], v[2:3], off
	global_load_dwordx4 v[42:45], v[4:5], off
	v_lshrrev_b32_e32 v2, 2, v237
	v_and_b32_e32 v2, 0x1fc, v2
	v_add_u32_e32 v2, v2, v50
	v_lshl_or_b32 v2, v2, 6, v6
	v_ashrrev_i32_e32 v3, 31, v2
	v_lshl_add_u64 v[2:3], v[2:3], 2, s[24:25]
	v_add_co_u32_e32 v4, vcc, s90, v2
	v_add_u32_e32 v55, 0x80, v201
	s_nop 0
	v_addc_co_u32_e32 v5, vcc, 0, v3, vcc
	global_load_dwordx4 v[38:41], v[2:3], off
	global_load_dwordx4 v[34:37], v[4:5], off
	v_lshrrev_b32_e32 v2, 2, v55
	v_and_b32_e32 v2, 0x1fc, v2
	v_add_u32_e32 v2, v2, v50
	v_lshl_or_b32 v2, v2, 6, v6
	v_ashrrev_i32_e32 v3, 31, v2
	v_lshl_add_u64 v[2:3], v[2:3], 2, s[24:25]
	v_add_co_u32_e32 v4, vcc, s90, v2
	v_add_u32_e32 v54, 0x90, v201
	s_nop 0
	v_addc_co_u32_e32 v5, vcc, 0, v3, vcc
	global_load_dwordx4 v[30:33], v[2:3], off
	global_load_dwordx4 v[26:29], v[4:5], off
	v_lshrrev_b32_e32 v2, 2, v54
	v_and_b32_e32 v2, 0x1fc, v2
	v_add_u32_e32 v2, v2, v50
	v_lshl_or_b32 v2, v2, 6, v6
	v_ashrrev_i32_e32 v3, 31, v2
	v_lshl_add_u64 v[2:3], v[2:3], 2, s[24:25]
	v_add_co_u32_e32 v4, vcc, s90, v2
	v_add_u32_e32 v53, 0xa0, v201
	s_nop 0
	v_addc_co_u32_e32 v5, vcc, 0, v3, vcc
	global_load_dwordx4 v[22:25], v[2:3], off
	global_load_dwordx4 v[18:21], v[4:5], off
	v_lshrrev_b32_e32 v2, 2, v53
	v_and_b32_e32 v2, 0x1fc, v2
	v_add_u32_e32 v2, v2, v50
	v_lshl_or_b32 v2, v2, 6, v6
	v_ashrrev_i32_e32 v3, 31, v2
	v_lshl_add_u64 v[2:3], v[2:3], 2, s[24:25]
	v_add_co_u32_e32 v4, vcc, s90, v2
	v_add_u32_e32 v52, 0xb0, v201
	s_nop 0
	v_addc_co_u32_e32 v5, vcc, 0, v3, vcc
	global_load_dwordx4 v[14:17], v[2:3], off
	global_load_dwordx4 v[10:13], v[4:5], off
	v_lshrrev_b32_e32 v2, 2, v52
	v_and_b32_e32 v2, 0x1fc, v2
	v_add_u32_e32 v2, v2, v50
	v_lshl_or_b32 v2, v2, 6, v6
	v_ashrrev_i32_e32 v3, 31, v2
	v_lshl_add_u64 v[2:3], v[2:3], 2, s[24:25]
	v_add_co_u32_e32 v4, vcc, s90, v2
	v_and_b32_e32 v51, 1, v50
	s_nop 0
	v_addc_co_u32_e32 v5, vcc, 0, v3, vcc
	v_lshlrev_b32_e32 v50, 3, v50
	v_add_u32_e32 v64, 24, v50
	v_cmp_eq_u32_e32 vcc, 0, v51
	s_add_u32 s2, s62, s7
	s_waitcnt vmcnt(0)
	v_lshlrev_b32_e32 v65, 16, v57
	v_cndmask_b32_e32 v50, v64, v50, vcc
	v_lshlrev_b32_e32 v64, 16, v56
	v_and_b32_e32 v56, 0xffff0000, v56
	v_and_b32_e32 v57, 0xffff0000, v57
	s_addc_u32 s7, s63, s46
	v_pk_mul_f32 v[228:229], v[182:183], v[56:57]
	s_add_u32 s40, s2, s89
	v_lshlrev_b32_e32 v224, 16, v60
	v_lshlrev_b32_e32 v225, 16, v61
	v_pk_fma_f32 v[228:229], v[190:191], v[64:65], v[228:229] neg_lo:[0,0,1] neg_hi:[0,0,1]
	v_pk_mul_f32 v[64:65], v[182:183], v[64:65]
	s_addc_u32 s41, s7, 0
	v_ashrrev_i32_e32 v51, 31, v50
	v_lshlrev_b32_e32 v222, 16, v58
	v_lshlrev_b32_e32 v223, 16, v59
	v_and_b32_e32 v60, 0xffff0000, v60
	v_and_b32_e32 v61, 0xffff0000, v61
	v_pk_fma_f32 v[64:65], v[190:191], v[56:57], v[64:65]
	v_pk_mul_f32 v[56:57], v[178:179], v[224:225]
	v_lshl_add_u64 v[50:51], s[40:41], 0, v[50:51]
	v_and_b32_e32 v58, 0xffff0000, v58
	v_and_b32_e32 v59, 0xffff0000, v59
	v_lshlrev_b32_e32 v226, 16, v62
	v_lshlrev_b32_e32 v227, 16, v63
	v_pk_mul_f32 v[232:233], v[178:179], v[60:61]
	v_pk_mul_f32 v[182:183], v[184:185], v[222:223]
	v_pk_fma_f32 v[60:61], v[186:187], v[60:61], v[56:57]
	v_ashrrev_i32_e32 v56, 31, v201
	v_and_b32_e32 v62, 0xffff0000, v62
	v_and_b32_e32 v63, 0xffff0000, v63
	v_pk_mul_f32 v[230:231], v[184:185], v[58:59]
	v_pk_fma_f32 v[182:183], v[192:193], v[58:59], v[182:183]
	v_pk_mul_f32 v[58:59], v[180:181], v[226:227]
	v_mad_u64_u32 v[178:179], s[40:41], s58, v201, v[50:51]
	v_mul_lo_u32 v56, s58, v56
	v_mul_lo_u32 v57, s59, v201
	v_pk_mul_f32 v[234:235], v[180:181], v[62:63]
	v_pk_fma_f32 v[232:233], v[186:187], v[224:225], v[232:233] neg_lo:[0,0,1] neg_hi:[0,0,1]
	v_pk_fma_f32 v[62:63], v[188:189], v[62:63], v[58:59]
	v_add3_u32 v179, v57, v179, v56
	v_mov_b32_e32 v56, v199
	v_mov_b32_e32 v57, v199
	v_mov_b32_e32 v58, v199
	v_mov_b32_e32 v59, v199
	v_cvt_pk_fp8_f32 v56, v228, v229
	v_cvt_pk_fp8_f32 v57, v232, v233
	v_cvt_pk_fp8_f32 v58, v64, v65
	v_cvt_pk_fp8_f32 v59, v60, v61
	v_pk_fma_f32 v[230:231], v[192:193], v[222:223], v[230:231] neg_lo:[0,0,1] neg_hi:[0,0,1]
	v_pk_fma_f32 v[234:235], v[188:189], v[226:227], v[234:235] neg_lo:[0,0,1] neg_hi:[0,0,1]
	v_cvt_pk_fp8_f32 v56, v230, v231 op_sel:[0,0,1]
	v_cvt_pk_fp8_f32 v58, v182, v183 op_sel:[0,0,1]
	v_cvt_pk_fp8_f32 v57, v234, v235 op_sel:[0,0,1]
	v_cvt_pk_fp8_f32 v59, v62, v63 op_sel:[0,0,1]
	v_and_b32_e32 v60, 0xffff0000, v204
	v_permlane16_swap_b32_e32 v56, v58
	v_permlane16_swap_b32_e32 v57, v59
	v_and_b32_e32 v61, 0xffff0000, v205
	global_load_dwordx4 v[6:9], v[2:3], off
	s_nop 0
	global_load_dwordx4 v[2:5], v[4:5], off
	global_store_dwordx4 v[178:179], v[56:59], off nt
	v_pk_mul_f32 v[184:185], v[166:167], v[60:61]
	v_and_b32_e32 v62, 0xffff0000, v206
	v_lshlrev_b32_e32 v56, 16, v204
	v_lshlrev_b32_e32 v57, 16, v205
	v_and_b32_e32 v63, 0xffff0000, v207
	v_lshlrev_b32_e32 v64, 16, v208
	v_lshlrev_b32_e32 v65, 16, v209
	v_pk_fma_f32 v[184:185], v[174:175], v[56:57], v[184:185] neg_lo:[0,0,1] neg_hi:[0,0,1]
	v_pk_mul_f32 v[56:57], v[166:167], v[56:57]
	v_lshlrev_b32_e32 v58, 16, v206
	v_lshlrev_b32_e32 v59, 16, v207
	v_and_b32_e32 v180, 0xffff0000, v208
	v_and_b32_e32 v181, 0xffff0000, v209
	v_pk_mul_f32 v[186:187], v[168:169], v[62:63]
	v_pk_fma_f32 v[60:61], v[174:175], v[60:61], v[56:57]
	v_pk_mul_f32 v[56:57], v[162:163], v[64:65]
	v_lshlrev_b32_e32 v178, 16, v210
	v_lshlrev_b32_e32 v179, 16, v211
	v_and_b32_e32 v182, 0xffff0000, v210
	v_and_b32_e32 v183, 0xffff0000, v211
	v_pk_fma_f32 v[186:187], v[176:177], v[58:59], v[186:187] neg_lo:[0,0,1] neg_hi:[0,0,1]
	v_pk_mul_f32 v[188:189], v[162:163], v[180:181]
	v_pk_mul_f32 v[58:59], v[168:169], v[58:59]
	v_pk_fma_f32 v[162:163], v[170:171], v[180:181], v[56:57]
	v_ashrrev_i32_e32 v56, 31, v221
	v_pk_mul_f32 v[190:191], v[164:165], v[182:183]
	v_pk_fma_f32 v[62:63], v[176:177], v[62:63], v[58:59]
	v_pk_mul_f32 v[58:59], v[164:165], v[178:179]
	v_mad_u64_u32 v[164:165], s[40:41], s58, v221, v[50:51]
	v_mul_lo_u32 v56, s58, v56
	v_mul_lo_u32 v57, s59, v221
	v_pk_fma_f32 v[188:189], v[170:171], v[64:65], v[188:189] neg_lo:[0,0,1] neg_hi:[0,0,1]
	v_pk_fma_f32 v[64:65], v[172:173], v[182:183], v[58:59]
	v_add3_u32 v165, v57, v165, v56
	v_mov_b32_e32 v56, v199
	v_mov_b32_e32 v57, v199
	v_mov_b32_e32 v58, v199
	v_mov_b32_e32 v59, v199
	v_cvt_pk_fp8_f32 v56, v184, v185
	v_cvt_pk_fp8_f32 v57, v188, v189
	v_cvt_pk_fp8_f32 v58, v60, v61
	v_cvt_pk_fp8_f32 v59, v162, v163
	v_pk_fma_f32 v[190:191], v[172:173], v[178:179], v[190:191] neg_lo:[0,0,1] neg_hi:[0,0,1]
	v_cvt_pk_fp8_f32 v56, v186, v187 op_sel:[0,0,1]
	v_cvt_pk_fp8_f32 v58, v62, v63 op_sel:[0,0,1]
	v_cvt_pk_fp8_f32 v57, v190, v191 op_sel:[0,0,1]
	v_cvt_pk_fp8_f32 v59, v64, v65 op_sel:[0,0,1]
	v_lshlrev_b32_e32 v60, 16, v42
	v_permlane16_swap_b32_e32 v56, v58
	v_permlane16_swap_b32_e32 v57, v59
	global_store_dwordx4 v[164:165], v[56:59], off nt
	v_lshlrev_b32_e32 v61, 16, v43
	v_and_b32_e32 v42, 0xffff0000, v42
	v_lshlrev_b32_e32 v56, 16, v46
	v_lshlrev_b32_e32 v57, 16, v47
	v_and_b32_e32 v46, 0xffff0000, v46
	v_and_b32_e32 v47, 0xffff0000, v47
	v_pk_mul_f32 v[64:65], v[150:151], v[46:47]
	v_lshlrev_b32_e32 v58, 16, v48
	v_lshlrev_b32_e32 v59, 16, v49
	v_and_b32_e32 v48, 0xffff0000, v48
	v_and_b32_e32 v49, 0xffff0000, v49
	v_pk_fma_f32 v[64:65], v[158:159], v[56:57], v[64:65] neg_lo:[0,0,1] neg_hi:[0,0,1]
	v_pk_mul_f32 v[56:57], v[150:151], v[56:57]
	v_and_b32_e32 v43, 0xffff0000, v43
	v_pk_mul_f32 v[162:163], v[152:153], v[48:49]
	v_pk_fma_f32 v[46:47], v[158:159], v[46:47], v[56:57]
	v_pk_mul_f32 v[56:57], v[146:147], v[60:61]
	v_lshlrev_b32_e32 v62, 16, v44
	v_lshlrev_b32_e32 v63, 16, v45
	v_pk_fma_f32 v[162:163], v[160:161], v[58:59], v[162:163] neg_lo:[0,0,1] neg_hi:[0,0,1]
	v_pk_mul_f32 v[164:165], v[146:147], v[42:43]
	v_pk_mul_f32 v[58:59], v[152:153], v[58:59]
	v_pk_fma_f32 v[56:57], v[154:155], v[42:43], v[56:57]
	v_ashrrev_i32_e32 v42, 31, v236
	v_and_b32_e32 v44, 0xffff0000, v44
	v_and_b32_e32 v45, 0xffff0000, v45
	v_pk_fma_f32 v[164:165], v[154:155], v[60:61], v[164:165] neg_lo:[0,0,1] neg_hi:[0,0,1]
	v_pk_fma_f32 v[48:49], v[160:161], v[48:49], v[58:59]
	v_pk_mul_f32 v[58:59], v[148:149], v[62:63]
	v_mad_u64_u32 v[60:61], s[40:41], s58, v236, v[50:51]
	v_mul_lo_u32 v42, s58, v42
	v_mul_lo_u32 v43, s59, v236
	v_pk_mul_f32 v[166:167], v[148:149], v[44:45]
	v_pk_fma_f32 v[58:59], v[156:157], v[44:45], v[58:59]
	v_add3_u32 v61, v43, v61, v42
	v_mov_b32_e32 v42, v199
	v_mov_b32_e32 v43, v199
	v_mov_b32_e32 v44, v199
	v_mov_b32_e32 v45, v199
	v_cvt_pk_fp8_f32 v42, v64, v65
	v_cvt_pk_fp8_f32 v43, v164, v165
	v_cvt_pk_fp8_f32 v44, v46, v47
	v_cvt_pk_fp8_f32 v45, v56, v57
	v_pk_fma_f32 v[166:167], v[156:157], v[62:63], v[166:167] neg_lo:[0,0,1] neg_hi:[0,0,1]
	v_cvt_pk_fp8_f32 v42, v162, v163 op_sel:[0,0,1]
	v_cvt_pk_fp8_f32 v44, v48, v49 op_sel:[0,0,1]
	v_cvt_pk_fp8_f32 v43, v166, v167 op_sel:[0,0,1]
	v_cvt_pk_fp8_f32 v45, v58, v59 op_sel:[0,0,1]
	v_lshlrev_b32_e32 v46, 16, v34
	v_permlane16_swap_b32_e32 v42, v44
	v_permlane16_swap_b32_e32 v43, v45
	global_store_dwordx4 v[60:61], v[42:45], off nt
	v_lshlrev_b32_e32 v47, 16, v35
	v_and_b32_e32 v34, 0xffff0000, v34
	v_lshlrev_b32_e32 v42, 16, v38
	v_lshlrev_b32_e32 v43, 16, v39
	v_and_b32_e32 v38, 0xffff0000, v38
	v_and_b32_e32 v39, 0xffff0000, v39
	v_pk_mul_f32 v[56:57], v[134:135], v[38:39]
	v_lshlrev_b32_e32 v44, 16, v40
	v_lshlrev_b32_e32 v45, 16, v41
	v_and_b32_e32 v40, 0xffff0000, v40
	v_and_b32_e32 v41, 0xffff0000, v41
	v_pk_fma_f32 v[56:57], v[142:143], v[42:43], v[56:57] neg_lo:[0,0,1] neg_hi:[0,0,1]
	v_pk_mul_f32 v[42:43], v[134:135], v[42:43]
	v_and_b32_e32 v35, 0xffff0000, v35
	v_pk_mul_f32 v[58:59], v[136:137], v[40:41]
	v_pk_fma_f32 v[38:39], v[142:143], v[38:39], v[42:43]
	v_pk_mul_f32 v[42:43], v[130:131], v[46:47]
	v_lshlrev_b32_e32 v48, 16, v36
	v_lshlrev_b32_e32 v49, 16, v37
	v_pk_fma_f32 v[58:59], v[144:145], v[44:45], v[58:59] neg_lo:[0,0,1] neg_hi:[0,0,1]
	v_pk_mul_f32 v[60:61], v[130:131], v[34:35]
	v_pk_mul_f32 v[44:45], v[136:137], v[44:45]
	v_pk_fma_f32 v[42:43], v[138:139], v[34:35], v[42:43]
	v_ashrrev_i32_e32 v34, 31, v237
	v_and_b32_e32 v36, 0xffff0000, v36
	v_and_b32_e32 v37, 0xffff0000, v37
	v_pk_fma_f32 v[60:61], v[138:139], v[46:47], v[60:61] neg_lo:[0,0,1] neg_hi:[0,0,1]
	v_pk_fma_f32 v[40:41], v[144:145], v[40:41], v[44:45]
	v_pk_mul_f32 v[44:45], v[132:133], v[48:49]
	v_mad_u64_u32 v[46:47], s[40:41], s58, v237, v[50:51]
	v_mul_lo_u32 v34, s58, v34
	v_mul_lo_u32 v35, s59, v237
	v_pk_mul_f32 v[62:63], v[132:133], v[36:37]
	v_pk_fma_f32 v[44:45], v[140:141], v[36:37], v[44:45]
	v_add3_u32 v47, v35, v47, v34
	v_mov_b32_e32 v34, v199
	v_mov_b32_e32 v35, v199
	v_mov_b32_e32 v36, v199
	v_mov_b32_e32 v37, v199
	v_cvt_pk_fp8_f32 v34, v56, v57
	v_cvt_pk_fp8_f32 v35, v60, v61
	v_cvt_pk_fp8_f32 v36, v38, v39
	v_cvt_pk_fp8_f32 v37, v42, v43
	v_pk_fma_f32 v[62:63], v[140:141], v[48:49], v[62:63] neg_lo:[0,0,1] neg_hi:[0,0,1]
	v_cvt_pk_fp8_f32 v34, v58, v59 op_sel:[0,0,1]
	v_cvt_pk_fp8_f32 v36, v40, v41 op_sel:[0,0,1]
	v_cvt_pk_fp8_f32 v35, v62, v63 op_sel:[0,0,1]
	v_cvt_pk_fp8_f32 v37, v44, v45 op_sel:[0,0,1]
	v_lshlrev_b32_e32 v38, 16, v26
	v_permlane16_swap_b32_e32 v34, v36
	v_permlane16_swap_b32_e32 v35, v37
	global_store_dwordx4 v[46:47], v[34:37], off nt
	v_lshlrev_b32_e32 v39, 16, v27
	v_and_b32_e32 v26, 0xffff0000, v26
	v_lshlrev_b32_e32 v34, 16, v30
	v_lshlrev_b32_e32 v35, 16, v31
	v_and_b32_e32 v30, 0xffff0000, v30
	v_and_b32_e32 v31, 0xffff0000, v31
	v_pk_mul_f32 v[42:43], v[118:119], v[30:31]
	v_lshlrev_b32_e32 v36, 16, v32
	v_lshlrev_b32_e32 v37, 16, v33
	v_and_b32_e32 v32, 0xffff0000, v32
	v_and_b32_e32 v33, 0xffff0000, v33
	v_pk_fma_f32 v[42:43], v[126:127], v[34:35], v[42:43] neg_lo:[0,0,1] neg_hi:[0,0,1]
	v_pk_mul_f32 v[34:35], v[118:119], v[34:35]
	v_and_b32_e32 v27, 0xffff0000, v27
	v_pk_mul_f32 v[44:45], v[120:121], v[32:33]
	v_pk_fma_f32 v[30:31], v[126:127], v[30:31], v[34:35]
	v_pk_mul_f32 v[34:35], v[114:115], v[38:39]
	v_lshlrev_b32_e32 v40, 16, v28
	v_lshlrev_b32_e32 v41, 16, v29
	v_pk_fma_f32 v[44:45], v[128:129], v[36:37], v[44:45] neg_lo:[0,0,1] neg_hi:[0,0,1]
	v_pk_mul_f32 v[46:47], v[114:115], v[26:27]
	v_pk_mul_f32 v[36:37], v[120:121], v[36:37]
	v_pk_fma_f32 v[34:35], v[122:123], v[26:27], v[34:35]
	v_ashrrev_i32_e32 v26, 31, v55
	v_and_b32_e32 v28, 0xffff0000, v28
	v_and_b32_e32 v29, 0xffff0000, v29
	v_pk_fma_f32 v[46:47], v[122:123], v[38:39], v[46:47] neg_lo:[0,0,1] neg_hi:[0,0,1]
	v_pk_fma_f32 v[32:33], v[128:129], v[32:33], v[36:37]
	v_pk_mul_f32 v[36:37], v[116:117], v[40:41]
	v_mad_u64_u32 v[38:39], s[40:41], s58, v55, v[50:51]
	v_mul_lo_u32 v26, s58, v26
	v_mul_lo_u32 v27, s59, v55
	v_pk_mul_f32 v[48:49], v[116:117], v[28:29]
	v_pk_fma_f32 v[36:37], v[124:125], v[28:29], v[36:37]
	v_add3_u32 v39, v27, v39, v26
	v_mov_b32_e32 v26, v199
	v_mov_b32_e32 v27, v199
	v_mov_b32_e32 v28, v199
	v_mov_b32_e32 v29, v199
	v_cvt_pk_fp8_f32 v26, v42, v43
	v_cvt_pk_fp8_f32 v27, v46, v47
	v_cvt_pk_fp8_f32 v28, v30, v31
	v_cvt_pk_fp8_f32 v29, v34, v35
	v_pk_fma_f32 v[48:49], v[124:125], v[40:41], v[48:49] neg_lo:[0,0,1] neg_hi:[0,0,1]
	v_cvt_pk_fp8_f32 v26, v44, v45 op_sel:[0,0,1]
	v_cvt_pk_fp8_f32 v28, v32, v33 op_sel:[0,0,1]
	v_cvt_pk_fp8_f32 v27, v48, v49 op_sel:[0,0,1]
	v_cvt_pk_fp8_f32 v29, v36, v37 op_sel:[0,0,1]
	v_lshlrev_b32_e32 v30, 16, v18
	v_permlane16_swap_b32_e32 v26, v28
	v_permlane16_swap_b32_e32 v27, v29
	global_store_dwordx4 v[38:39], v[26:29], off nt
	v_lshlrev_b32_e32 v31, 16, v19
	v_and_b32_e32 v18, 0xffff0000, v18
	v_lshlrev_b32_e32 v26, 16, v22
	v_lshlrev_b32_e32 v27, 16, v23
	v_and_b32_e32 v22, 0xffff0000, v22
	v_and_b32_e32 v23, 0xffff0000, v23
	v_pk_mul_f32 v[34:35], v[94:95], v[22:23]
	v_lshlrev_b32_e32 v28, 16, v24
	v_lshlrev_b32_e32 v29, 16, v25
	v_and_b32_e32 v24, 0xffff0000, v24
	v_and_b32_e32 v25, 0xffff0000, v25
	v_pk_fma_f32 v[34:35], v[110:111], v[26:27], v[34:35] neg_lo:[0,0,1] neg_hi:[0,0,1]
	v_pk_mul_f32 v[26:27], v[94:95], v[26:27]
	v_and_b32_e32 v19, 0xffff0000, v19
	v_pk_mul_f32 v[36:37], v[96:97], v[24:25]
	v_pk_fma_f32 v[22:23], v[110:111], v[22:23], v[26:27]
	v_pk_mul_f32 v[26:27], v[90:91], v[30:31]
	v_lshlrev_b32_e32 v32, 16, v20
	v_lshlrev_b32_e32 v33, 16, v21
	v_pk_fma_f32 v[36:37], v[112:113], v[28:29], v[36:37] neg_lo:[0,0,1] neg_hi:[0,0,1]
	v_pk_mul_f32 v[38:39], v[90:91], v[18:19]
	v_pk_mul_f32 v[28:29], v[96:97], v[28:29]
	v_pk_fma_f32 v[26:27], v[106:107], v[18:19], v[26:27]
	v_ashrrev_i32_e32 v18, 31, v54
	v_and_b32_e32 v20, 0xffff0000, v20
	v_and_b32_e32 v21, 0xffff0000, v21
	v_pk_fma_f32 v[38:39], v[106:107], v[30:31], v[38:39] neg_lo:[0,0,1] neg_hi:[0,0,1]
	v_pk_fma_f32 v[24:25], v[112:113], v[24:25], v[28:29]
	v_pk_mul_f32 v[28:29], v[92:93], v[32:33]
	v_mad_u64_u32 v[30:31], s[40:41], s58, v54, v[50:51]
	v_mul_lo_u32 v18, s58, v18
	v_mul_lo_u32 v19, s59, v54
	v_pk_mul_f32 v[40:41], v[92:93], v[20:21]
	v_pk_fma_f32 v[28:29], v[108:109], v[20:21], v[28:29]
	v_add3_u32 v31, v19, v31, v18
	v_mov_b32_e32 v18, v199
	v_mov_b32_e32 v19, v199
	v_mov_b32_e32 v20, v199
	v_mov_b32_e32 v21, v199
	v_cvt_pk_fp8_f32 v18, v34, v35
	v_cvt_pk_fp8_f32 v19, v38, v39
	v_cvt_pk_fp8_f32 v20, v22, v23
	v_cvt_pk_fp8_f32 v21, v26, v27
	v_pk_fma_f32 v[40:41], v[108:109], v[32:33], v[40:41] neg_lo:[0,0,1] neg_hi:[0,0,1]
	v_cvt_pk_fp8_f32 v18, v36, v37 op_sel:[0,0,1]
	v_cvt_pk_fp8_f32 v20, v24, v25 op_sel:[0,0,1]
	v_cvt_pk_fp8_f32 v19, v40, v41 op_sel:[0,0,1]
	v_cvt_pk_fp8_f32 v21, v28, v29 op_sel:[0,0,1]
	v_lshlrev_b32_e32 v22, 16, v10
	v_permlane16_swap_b32_e32 v18, v20
	v_permlane16_swap_b32_e32 v19, v21
	global_store_dwordx4 v[30:31], v[18:21], off nt
	v_lshlrev_b32_e32 v23, 16, v11
	v_and_b32_e32 v10, 0xffff0000, v10
	v_lshlrev_b32_e32 v18, 16, v14
	v_lshlrev_b32_e32 v19, 16, v15
	v_and_b32_e32 v14, 0xffff0000, v14
	v_and_b32_e32 v15, 0xffff0000, v15
	v_pk_mul_f32 v[26:27], v[98:99], v[14:15]
	v_lshlrev_b32_e32 v20, 16, v16
	v_lshlrev_b32_e32 v21, 16, v17
	v_and_b32_e32 v16, 0xffff0000, v16
	v_and_b32_e32 v17, 0xffff0000, v17
	v_pk_fma_f32 v[26:27], v[78:79], v[18:19], v[26:27] neg_lo:[0,0,1] neg_hi:[0,0,1]
	v_pk_mul_f32 v[18:19], v[98:99], v[18:19]
	v_and_b32_e32 v11, 0xffff0000, v11
	v_pk_mul_f32 v[28:29], v[100:101], v[16:17]
	v_pk_fma_f32 v[14:15], v[78:79], v[14:15], v[18:19]
	v_pk_mul_f32 v[18:19], v[102:103], v[22:23]
	v_lshlrev_b32_e32 v24, 16, v12
	v_lshlrev_b32_e32 v25, 16, v13
	v_pk_fma_f32 v[28:29], v[80:81], v[20:21], v[28:29] neg_lo:[0,0,1] neg_hi:[0,0,1]
	v_pk_mul_f32 v[30:31], v[102:103], v[10:11]
	v_pk_mul_f32 v[20:21], v[100:101], v[20:21]
	v_pk_fma_f32 v[18:19], v[74:75], v[10:11], v[18:19]
	v_ashrrev_i32_e32 v10, 31, v53
	v_and_b32_e32 v12, 0xffff0000, v12
	v_and_b32_e32 v13, 0xffff0000, v13
	v_pk_fma_f32 v[30:31], v[74:75], v[22:23], v[30:31] neg_lo:[0,0,1] neg_hi:[0,0,1]
	v_pk_fma_f32 v[16:17], v[80:81], v[16:17], v[20:21]
	v_pk_mul_f32 v[20:21], v[104:105], v[24:25]
	v_mad_u64_u32 v[22:23], s[40:41], s58, v53, v[50:51]
	v_mul_lo_u32 v10, s58, v10
	v_mul_lo_u32 v11, s59, v53
	v_pk_mul_f32 v[32:33], v[104:105], v[12:13]
	v_pk_fma_f32 v[20:21], v[76:77], v[12:13], v[20:21]
	v_add3_u32 v23, v11, v23, v10
	v_mov_b32_e32 v10, v199
	v_mov_b32_e32 v11, v199
	v_mov_b32_e32 v12, v199
	v_mov_b32_e32 v13, v199
	v_cvt_pk_fp8_f32 v10, v26, v27
	v_cvt_pk_fp8_f32 v11, v30, v31
	v_cvt_pk_fp8_f32 v12, v14, v15
	v_cvt_pk_fp8_f32 v13, v18, v19
	v_pk_fma_f32 v[32:33], v[76:77], v[24:25], v[32:33] neg_lo:[0,0,1] neg_hi:[0,0,1]
	v_cvt_pk_fp8_f32 v10, v28, v29 op_sel:[0,0,1]
	v_cvt_pk_fp8_f32 v12, v16, v17 op_sel:[0,0,1]
	v_cvt_pk_fp8_f32 v11, v32, v33 op_sel:[0,0,1]
	v_cvt_pk_fp8_f32 v13, v20, v21 op_sel:[0,0,1]
	s_waitcnt vmcnt(6)
	v_lshlrev_b32_e32 v14, 16, v2
	v_permlane16_swap_b32_e32 v10, v12
	v_permlane16_swap_b32_e32 v11, v13
	global_store_dwordx4 v[22:23], v[10:13], off nt
	v_lshlrev_b32_e32 v15, 16, v3
	v_and_b32_e32 v2, 0xffff0000, v2
	v_lshlrev_b32_e32 v10, 16, v6
	v_lshlrev_b32_e32 v11, 16, v7
	v_and_b32_e32 v6, 0xffff0000, v6
	v_and_b32_e32 v7, 0xffff0000, v7
	v_pk_mul_f32 v[18:19], v[82:83], v[6:7]
	v_lshlrev_b32_e32 v12, 16, v8
	v_lshlrev_b32_e32 v13, 16, v9
	v_and_b32_e32 v8, 0xffff0000, v8
	v_and_b32_e32 v9, 0xffff0000, v9
	v_pk_fma_f32 v[18:19], v[70:71], v[10:11], v[18:19] neg_lo:[0,0,1] neg_hi:[0,0,1]
	v_pk_mul_f32 v[10:11], v[82:83], v[10:11]
	v_and_b32_e32 v3, 0xffff0000, v3
	v_pk_mul_f32 v[20:21], v[84:85], v[8:9]
	v_pk_fma_f32 v[6:7], v[70:71], v[6:7], v[10:11]
	v_pk_mul_f32 v[10:11], v[86:87], v[14:15]
	v_lshlrev_b32_e32 v16, 16, v4
	v_lshlrev_b32_e32 v17, 16, v5
	v_pk_fma_f32 v[20:21], v[72:73], v[12:13], v[20:21] neg_lo:[0,0,1] neg_hi:[0,0,1]
	v_pk_mul_f32 v[22:23], v[86:87], v[2:3]
	v_pk_mul_f32 v[12:13], v[84:85], v[12:13]
	v_pk_fma_f32 v[10:11], v[66:67], v[2:3], v[10:11]
	v_ashrrev_i32_e32 v2, 31, v52
	v_and_b32_e32 v4, 0xffff0000, v4
	v_and_b32_e32 v5, 0xffff0000, v5
	v_pk_fma_f32 v[22:23], v[66:67], v[14:15], v[22:23] neg_lo:[0,0,1] neg_hi:[0,0,1]
	v_pk_fma_f32 v[8:9], v[72:73], v[8:9], v[12:13]
	v_pk_mul_f32 v[12:13], v[88:89], v[16:17]
	v_mad_u64_u32 v[14:15], s[40:41], s58, v52, v[50:51]
	v_mul_lo_u32 v2, s58, v2
	v_mul_lo_u32 v3, s59, v52
	v_pk_mul_f32 v[24:25], v[88:89], v[4:5]
	v_pk_fma_f32 v[12:13], v[68:69], v[4:5], v[12:13]
	v_add3_u32 v15, v3, v15, v2
	v_mov_b32_e32 v2, v199
	v_mov_b32_e32 v3, v199
	v_mov_b32_e32 v4, v199
	v_mov_b32_e32 v5, v199
	v_cvt_pk_fp8_f32 v2, v18, v19
	v_cvt_pk_fp8_f32 v3, v22, v23
	v_cvt_pk_fp8_f32 v4, v6, v7
	v_cvt_pk_fp8_f32 v5, v10, v11
	v_pk_fma_f32 v[24:25], v[68:69], v[16:17], v[24:25] neg_lo:[0,0,1] neg_hi:[0,0,1]
	v_cvt_pk_fp8_f32 v2, v20, v21 op_sel:[0,0,1]
	v_cvt_pk_fp8_f32 v4, v8, v9 op_sel:[0,0,1]
	v_cvt_pk_fp8_f32 v3, v24, v25 op_sel:[0,0,1]
	v_cvt_pk_fp8_f32 v5, v12, v13 op_sel:[0,0,1]
	v_permlane16_swap_b32_e32 v2, v4
	s_nop 0
	v_permlane16_swap_b32_e32 v3, v5
	global_store_dwordx4 v[14:15], v[2:5], off nt
	s_and_b64 vcc, exec, s[4:5]
	s_mov_b64 s[4:5], -1
	s_cbranch_vccnz .LBB0_118

.LBB0_493:
	s_lshl_b32 s2, s79, 8
	s_add_i32 s28, s2, s59
	s_add_i32 s26, s62, s52
	s_ashr_i32 s2, s28, 4
	s_ashr_i32 s27, s26, 31
	s_lshl_b64 s[26:27], s[26:27], 10
	s_ashr_i32 s3, s2, 31
	v_lshl_add_u64 v[2:3], v[202:203], 0, s[26:27]
	s_lshl_b64 s[26:27], s[2:3], 15
	v_lshl_add_u64 v[4:5], v[2:3], 0, s[26:27]
	s_or_b32 s26, s2, 1
	s_ashr_i32 s27, s26, 31
	s_lshl_b64 s[26:27], s[26:27], 15
	v_lshl_add_u64 v[6:7], v[2:3], 0, s[26:27]
	s_or_b32 s26, s2, 2
	s_or_b32 s2, s2, 3
	s_ashr_i32 s27, s26, 31
	s_ashr_i32 s3, s2, 31
	s_waitcnt vmcnt(0)
	s_lshl_b64 s[26:27], s[26:27], 15
	s_lshl_b64 s[2:3], s[2:3], 15
	global_load_dwordx4 v[22:25], v[4:5], off
	global_load_dwordx4 v[26:29], v[6:7], off
	v_lshl_add_u64 v[6:7], v[2:3], 0, s[26:27]
	v_lshl_add_u64 v[2:3], v[2:3], 0, s[2:3]
	global_load_dwordx4 v[30:33], v[6:7], off
	global_load_dwordx4 v[18:21], v[2:3], off
	v_add_co_u32_e32 v2, vcc, s1, v4
	s_waitcnt vmcnt(0)
	v_mov_b32_e32 v34, v24
	v_addc_co_u32_e32 v3, vcc, 0, v5, vcc
	v_add_co_u32_e32 v6, vcc, s64, v4
	v_mov_b32_e32 v36, v25
	s_nop 0
	v_addc_co_u32_e32 v7, vcc, 0, v5, vcc
	global_load_dwordx4 v[14:17], v[2:3], off
	global_load_dwordx4 v[10:13], v[6:7], off
	v_add_co_u32_e32 v2, vcc, s54, v4
	v_permlane16_swap_b32_e32 v22, v34
	s_nop 0
	v_addc_co_u32_e32 v3, vcc, 0, v5, vcc
	global_load_dwordx4 v[6:9], v[2:3], off
	v_add_co_u32_e32 v2, vcc, s65, v4
	v_permlane16_swap_b32_e32 v23, v36
	s_nop 0
	v_addc_co_u32_e32 v3, vcc, 0, v5, vcc
	global_load_dwordx4 v[2:5], v[2:3], off
	v_mov_b32_e32 v44, v20
	v_mov_b32_e32 v45, v21
	v_cvt_pk_f32_fp8_sdwa v[20:21], v22 src0_sel:WORD_1
	v_cvt_pk_f32_fp8_e32 v[24:25], v23
	v_mov_b32_e32 v40, v28
	v_mov_b32_e32 v41, v29
	v_pk_mul_f32 v[20:21], v[20:21], s[0:1] op_sel_hi:[1,0]
	v_mov_b32_e32 v42, v32
	v_pk_mul_f32 v[28:29], v[192:193], v[20:21]
	v_pk_mul_f32 v[20:21], v[24:25], s[0:1] op_sel_hi:[1,0]
	v_mov_b32_e32 v43, v33
	v_cvt_pk_f32_fp8_sdwa v[32:33], v34 src0_sel:WORD_1
	v_permlane16_swap_b32_e32 v26, v40
	v_pk_mul_f32 v[32:33], v[32:33], s[0:1] op_sel_hi:[1,0]
	v_permlane16_swap_b32_e32 v27, v41
	v_pk_mul_f32 v[32:33], v[184:185], v[32:33]
	v_permlane16_swap_b32_e32 v30, v42
	v_permlane16_swap_b32_e32 v31, v43
	v_permlane16_swap_b32_e32 v18, v44
	v_permlane16_swap_b32_e32 v19, v45
	s_and_b64 vcc, exec, s[4:5]
	s_mov_b64 s[4:5], -1
	s_waitcnt vmcnt(3)
	v_mov_b32_e32 v46, v16
	v_mov_b32_e32 v47, v17
	v_cvt_pk_f32_fp8_e32 v[16:17], v22
	v_cvt_pk_f32_fp8_sdwa v[22:23], v23 src0_sel:WORD_1
	s_waitcnt vmcnt(2)
	v_mov_b32_e32 v48, v12
	v_mov_b32_e32 v49, v13
	v_pk_mul_f32 v[16:17], v[16:17], s[0:1] op_sel_hi:[1,0]
	v_pk_mul_f32 v[22:23], v[22:23], s[0:1] op_sel_hi:[1,0]
	v_pk_mul_f32 v[16:17], v[190:191], v[16:17]
	v_pk_mul_f32 v[24:25], v[188:189], v[22:23]
	v_pk_mul_f32 v[22:23], v[186:187], v[20:21]
	v_cvt_pk_f32_fp8_e32 v[20:21], v34
	v_cvt_pk_f32_fp8_e32 v[34:35], v36
	v_cvt_pk_f32_fp8_sdwa v[36:37], v36 src0_sel:WORD_1
	s_waitcnt vmcnt(1)
	v_mov_b32_e32 v50, v8
	v_pk_mul_f32 v[20:21], v[20:21], s[0:1] op_sel_hi:[1,0]
	v_or_b32_e32 v8, s28, v217
	v_pk_mul_f32 v[38:39], v[182:183], v[20:21]
	v_pk_mul_f32 v[20:21], v[34:35], s[0:1] op_sel_hi:[1,0]
	v_pk_mul_f32 v[34:35], v[36:37], s[0:1] op_sel_hi:[1,0]
	v_pk_mul_f32 v[36:37], v[178:179], v[20:21]
	v_mov_b32_e32 v21, v199
	v_mov_b32_e32 v20, v199
	v_cvt_pk_fp8_f32 v21, v22, v23
	v_mov_b32_e32 v22, v199
	v_mov_b32_e32 v23, v199
	v_cvt_pk_fp8_f32 v20, v16, v17
	v_cvt_pk_fp8_f32 v22, v38, v39
	v_cvt_pk_fp8_f32 v23, v36, v37
	v_mov_b32_e32 v51, v9
	v_pk_mul_f32 v[34:35], v[180:181], v[34:35]
	v_ashrrev_i32_e32 v9, 31, v8
	s_waitcnt vmcnt(0)
	v_mov_b32_e32 v12, v4
	v_lshl_or_b32 v4, s78, 8, v221
	v_cvt_pk_fp8_f32 v20, v28, v29 op_sel:[0,0,1]
	v_cvt_pk_fp8_f32 v21, v24, v25 op_sel:[0,0,1]
	v_cvt_pk_fp8_f32 v22, v32, v33 op_sel:[0,0,1]
	v_cvt_pk_fp8_f32 v23, v34, v35 op_sel:[0,0,1]
	v_lshlrev_b64 v[16:17], 10, v[8:9]
	v_mov_b32_e32 v13, v5
	v_ashrrev_i32_e32 v5, 31, v4
	v_lshl_add_u64 v[16:17], s[14:15], 0, v[16:17]
	v_lshl_add_u64 v[16:17], v[16:17], 0, v[4:5]
	v_lshl_add_u64 v[16:17], v[16:17], 0, v[204:205]
	v_lshl_add_u64 v[16:17], v[16:17], 0, v[206:207]
	v_permlane16_swap_b32_e32 v20, v22
	v_permlane16_swap_b32_e32 v21, v23
	global_store_dwordx4 v[16:17], v[20:23], off nt
	v_cvt_pk_f32_fp8_sdwa v[24:25], v27 src0_sel:WORD_1
	v_cvt_pk_f32_fp8_e32 v[16:17], v26
	v_cvt_pk_f32_fp8_sdwa v[20:21], v26 src0_sel:WORD_1
	v_cvt_pk_f32_fp8_e32 v[22:23], v27
	v_cvt_pk_f32_fp8_e32 v[32:33], v41
	v_cvt_pk_f32_fp8_sdwa v[34:35], v41 src0_sel:WORD_1
	v_pk_mul_f32 v[20:21], v[20:21], s[0:1] op_sel_hi:[1,0]
	v_pk_mul_f32 v[16:17], v[16:17], s[0:1] op_sel_hi:[1,0]
	v_pk_mul_f32 v[26:27], v[176:177], v[20:21]
	v_pk_mul_f32 v[20:21], v[22:23], s[0:1] op_sel_hi:[1,0]
	v_pk_mul_f32 v[22:23], v[24:25], s[0:1] op_sel_hi:[1,0]
	v_cvt_pk_f32_fp8_sdwa v[28:29], v40 src0_sel:WORD_1
	v_pk_mul_f32 v[24:25], v[172:173], v[22:23]
	v_pk_mul_f32 v[22:23], v[170:171], v[20:21]
	v_cvt_pk_f32_fp8_e32 v[20:21], v40
	v_pk_mul_f32 v[16:17], v[174:175], v[16:17]
	v_pk_mul_f32 v[28:29], v[28:29], s[0:1] op_sel_hi:[1,0]
	v_permlane16_swap_b32_e32 v14, v46
	v_pk_mul_f32 v[20:21], v[20:21], s[0:1] op_sel_hi:[1,0]
	v_pk_mul_f32 v[28:29], v[168:169], v[28:29]
	v_pk_mul_f32 v[36:37], v[166:167], v[20:21]
	v_pk_mul_f32 v[20:21], v[32:33], s[0:1] op_sel_hi:[1,0]
	v_pk_mul_f32 v[32:33], v[34:35], s[0:1] op_sel_hi:[1,0]
	v_pk_mul_f32 v[34:35], v[162:163], v[20:21]
	v_mov_b32_e32 v21, v199
	v_mov_b32_e32 v20, v199
	v_cvt_pk_fp8_f32 v21, v22, v23
	v_mov_b32_e32 v22, v199
	v_mov_b32_e32 v23, v199
	v_cvt_pk_fp8_f32 v20, v16, v17
	v_cvt_pk_fp8_f32 v22, v36, v37
	v_cvt_pk_fp8_f32 v23, v34, v35
	v_or_b32_e32 v16, 16, v8
	v_pk_mul_f32 v[32:33], v[164:165], v[32:33]
	v_ashrrev_i32_e32 v17, 31, v16
	v_cvt_pk_fp8_f32 v20, v26, v27 op_sel:[0,0,1]
	v_cvt_pk_fp8_f32 v21, v24, v25 op_sel:[0,0,1]
	v_cvt_pk_fp8_f32 v22, v28, v29 op_sel:[0,0,1]
	v_cvt_pk_fp8_f32 v23, v32, v33 op_sel:[0,0,1]
	v_lshlrev_b64 v[16:17], 10, v[16:17]
	v_lshl_add_u64 v[16:17], s[14:15], 0, v[16:17]
	v_lshl_add_u64 v[16:17], v[16:17], 0, v[4:5]
	v_lshl_add_u64 v[16:17], v[16:17], 0, v[204:205]
	v_lshl_add_u64 v[16:17], v[16:17], 0, v[206:207]
	v_permlane16_swap_b32_e32 v20, v22
	v_permlane16_swap_b32_e32 v21, v23
	global_store_dwordx4 v[16:17], v[20:23], off nt
	v_cvt_pk_f32_fp8_sdwa v[24:25], v31 src0_sel:WORD_1
	v_cvt_pk_f32_fp8_e32 v[16:17], v30
	v_cvt_pk_f32_fp8_sdwa v[20:21], v30 src0_sel:WORD_1
	v_cvt_pk_f32_fp8_e32 v[22:23], v31
	v_cvt_pk_f32_fp8_e32 v[30:31], v43
	v_cvt_pk_f32_fp8_sdwa v[32:33], v43 src0_sel:WORD_1
	v_pk_mul_f32 v[20:21], v[20:21], s[0:1] op_sel_hi:[1,0]
	v_pk_mul_f32 v[16:17], v[16:17], s[0:1] op_sel_hi:[1,0]
	v_pk_mul_f32 v[26:27], v[160:161], v[20:21]
	v_pk_mul_f32 v[20:21], v[22:23], s[0:1] op_sel_hi:[1,0]
	v_pk_mul_f32 v[22:23], v[24:25], s[0:1] op_sel_hi:[1,0]
	v_cvt_pk_f32_fp8_sdwa v[28:29], v42 src0_sel:WORD_1
	v_pk_mul_f32 v[24:25], v[156:157], v[22:23]
	v_pk_mul_f32 v[22:23], v[154:155], v[20:21]
	v_cvt_pk_f32_fp8_e32 v[20:21], v42
	v_pk_mul_f32 v[16:17], v[158:159], v[16:17]
	v_pk_mul_f32 v[28:29], v[28:29], s[0:1] op_sel_hi:[1,0]
	v_permlane16_swap_b32_e32 v15, v47
	v_pk_mul_f32 v[20:21], v[20:21], s[0:1] op_sel_hi:[1,0]
	v_pk_mul_f32 v[28:29], v[152:153], v[28:29]
	v_pk_mul_f32 v[34:35], v[150:151], v[20:21]
	v_pk_mul_f32 v[20:21], v[30:31], s[0:1] op_sel_hi:[1,0]
	v_pk_mul_f32 v[30:31], v[32:33], s[0:1] op_sel_hi:[1,0]
	v_pk_mul_f32 v[32:33], v[146:147], v[20:21]
	v_mov_b32_e32 v21, v199
	v_mov_b32_e32 v20, v199
	v_cvt_pk_fp8_f32 v21, v22, v23
	v_mov_b32_e32 v22, v199
	v_mov_b32_e32 v23, v199
	v_cvt_pk_fp8_f32 v20, v16, v17
	v_cvt_pk_fp8_f32 v22, v34, v35
	v_cvt_pk_fp8_f32 v23, v32, v33
	v_or_b32_e32 v16, 32, v8
	v_pk_mul_f32 v[30:31], v[148:149], v[30:31]
	v_ashrrev_i32_e32 v17, 31, v16
	v_cvt_pk_fp8_f32 v20, v26, v27 op_sel:[0,0,1]
	v_cvt_pk_fp8_f32 v21, v24, v25 op_sel:[0,0,1]
	v_cvt_pk_fp8_f32 v22, v28, v29 op_sel:[0,0,1]
	v_cvt_pk_fp8_f32 v23, v30, v31 op_sel:[0,0,1]
	v_lshlrev_b64 v[16:17], 10, v[16:17]
	v_lshl_add_u64 v[16:17], s[14:15], 0, v[16:17]
	v_lshl_add_u64 v[16:17], v[16:17], 0, v[4:5]
	v_lshl_add_u64 v[16:17], v[16:17], 0, v[204:205]
	v_lshl_add_u64 v[16:17], v[16:17], 0, v[206:207]
	v_permlane16_swap_b32_e32 v20, v22
	v_permlane16_swap_b32_e32 v21, v23
	global_store_dwordx4 v[16:17], v[20:23], off nt
	v_cvt_pk_f32_fp8_e32 v[16:17], v18
	v_cvt_pk_f32_fp8_e32 v[28:29], v45
	v_cvt_pk_f32_fp8_sdwa v[20:21], v18 src0_sel:WORD_1
	v_cvt_pk_f32_fp8_e32 v[22:23], v19
	v_cvt_pk_f32_fp8_sdwa v[18:19], v19 src0_sel:WORD_1
	v_pk_mul_f32 v[16:17], v[16:17], s[0:1] op_sel_hi:[1,0]
	v_cvt_pk_f32_fp8_sdwa v[30:31], v45 src0_sel:WORD_1
	v_pk_mul_f32 v[24:25], v[142:143], v[16:17]
	v_pk_mul_f32 v[16:17], v[22:23], s[0:1] op_sel_hi:[1,0]
	v_pk_mul_f32 v[18:19], v[18:19], s[0:1] op_sel_hi:[1,0]
	v_cvt_pk_f32_fp8_sdwa v[26:27], v44 src0_sel:WORD_1
	v_pk_mul_f32 v[22:23], v[140:141], v[18:19]
	v_pk_mul_f32 v[18:19], v[138:139], v[16:17]
	v_cvt_pk_f32_fp8_e32 v[16:17], v44
	v_pk_mul_f32 v[20:21], v[20:21], s[0:1] op_sel_hi:[1,0]
	v_pk_mul_f32 v[26:27], v[26:27], s[0:1] op_sel_hi:[1,0]
	v_pk_mul_f32 v[20:21], v[144:145], v[20:21]
	v_pk_mul_f32 v[16:17], v[16:17], s[0:1] op_sel_hi:[1,0]
	v_pk_mul_f32 v[26:27], v[136:137], v[26:27]
	v_pk_mul_f32 v[32:33], v[134:135], v[16:17]
	v_pk_mul_f32 v[16:17], v[28:29], s[0:1] op_sel_hi:[1,0]
	v_pk_mul_f32 v[28:29], v[30:31], s[0:1] op_sel_hi:[1,0]
	v_pk_mul_f32 v[30:31], v[130:131], v[16:17]
	v_mov_b32_e32 v16, v199
	v_cvt_pk_fp8_f32 v16, v24, v25
	v_mov_b32_e32 v17, v199
	v_cvt_pk_fp8_f32 v17, v18, v19
	v_mov_b32_e32 v18, v199
	v_mov_b32_e32 v19, v199
	v_cvt_pk_fp8_f32 v18, v32, v33
	v_cvt_pk_fp8_f32 v19, v30, v31
	v_cvt_pk_fp8_f32 v16, v20, v21 op_sel:[0,0,1]
	v_or_b32_e32 v20, 48, v8
	v_pk_mul_f32 v[28:29], v[132:133], v[28:29]
	v_ashrrev_i32_e32 v21, 31, v20
	v_cvt_pk_fp8_f32 v17, v22, v23 op_sel:[0,0,1]
	v_cvt_pk_fp8_f32 v18, v26, v27 op_sel:[0,0,1]
	v_cvt_pk_fp8_f32 v19, v28, v29 op_sel:[0,0,1]
	v_lshlrev_b64 v[20:21], 10, v[20:21]
	v_lshl_add_u64 v[20:21], s[14:15], 0, v[20:21]
	v_lshl_add_u64 v[20:21], v[20:21], 0, v[4:5]
	v_lshl_add_u64 v[20:21], v[20:21], 0, v[204:205]
	v_lshl_add_u64 v[20:21], v[20:21], 0, v[206:207]
	v_permlane16_swap_b32_e32 v16, v18
	v_permlane16_swap_b32_e32 v17, v19
	global_store_dwordx4 v[20:21], v[16:19], off nt
	v_cvt_pk_f32_fp8_sdwa v[20:21], v14 src0_sel:WORD_1
	v_cvt_pk_f32_fp8_e32 v[22:23], v15
	v_cvt_pk_f32_fp8_e32 v[16:17], v14
	v_cvt_pk_f32_fp8_sdwa v[14:15], v15 src0_sel:WORD_1
	v_cvt_pk_f32_fp8_e32 v[28:29], v47
	v_cvt_pk_f32_fp8_sdwa v[30:31], v47 src0_sel:WORD_1
	v_pk_mul_f32 v[16:17], v[16:17], s[0:1] op_sel_hi:[1,0]
	v_pk_mul_f32 v[14:15], v[14:15], s[0:1] op_sel_hi:[1,0]
	v_pk_mul_f32 v[16:17], v[126:127], v[16:17]
	v_pk_mul_f32 v[24:25], v[124:125], v[14:15]
	v_cvt_pk_f32_fp8_e32 v[14:15], v46
	v_pk_mul_f32 v[22:23], v[22:23], s[0:1] op_sel_hi:[1,0]
	v_cvt_pk_f32_fp8_sdwa v[26:27], v46 src0_sel:WORD_1
	v_pk_mul_f32 v[22:23], v[122:123], v[22:23]
	v_pk_mul_f32 v[14:15], v[14:15], s[0:1] op_sel_hi:[1,0]
	v_add_u32_e32 v18, 0x80, v8
	v_pk_mul_f32 v[32:33], v[118:119], v[14:15]
	v_pk_mul_f32 v[14:15], v[28:29], s[0:1] op_sel_hi:[1,0]
	v_pk_mul_f32 v[28:29], v[30:31], s[0:1] op_sel_hi:[1,0]
	v_pk_mul_f32 v[30:31], v[114:115], v[14:15]
	v_mov_b32_e32 v14, v199
	v_cvt_pk_fp8_f32 v14, v16, v17
	v_mov_b32_e32 v15, v199
	v_mov_b32_e32 v16, v199
	v_mov_b32_e32 v17, v199
	v_cvt_pk_fp8_f32 v15, v22, v23
	v_cvt_pk_fp8_f32 v16, v32, v33
	v_cvt_pk_fp8_f32 v17, v30, v31
	v_pk_mul_f32 v[20:21], v[20:21], s[0:1] op_sel_hi:[1,0]
	v_pk_mul_f32 v[26:27], v[26:27], s[0:1] op_sel_hi:[1,0]
	v_pk_mul_f32 v[20:21], v[128:129], v[20:21]
	v_pk_mul_f32 v[26:27], v[120:121], v[26:27]
	v_pk_mul_f32 v[28:29], v[116:117], v[28:29]
	v_ashrrev_i32_e32 v19, 31, v18
	v_cvt_pk_fp8_f32 v14, v20, v21 op_sel:[0,0,1]
	v_cvt_pk_fp8_f32 v15, v24, v25 op_sel:[0,0,1]
	v_cvt_pk_fp8_f32 v16, v26, v27 op_sel:[0,0,1]
	v_cvt_pk_fp8_f32 v17, v28, v29 op_sel:[0,0,1]
	v_lshlrev_b64 v[18:19], 10, v[18:19]
	v_lshl_add_u64 v[18:19], s[14:15], 0, v[18:19]
	v_lshl_add_u64 v[18:19], v[18:19], 0, v[4:5]
	v_lshl_add_u64 v[18:19], v[18:19], 0, v[204:205]
	v_permlane16_swap_b32_e32 v10, v48
	v_lshl_add_u64 v[18:19], v[18:19], 0, v[206:207]
	v_permlane16_swap_b32_e32 v14, v16
	v_permlane16_swap_b32_e32 v15, v17
	v_permlane16_swap_b32_e32 v11, v49
	global_store_dwordx4 v[18:19], v[14:17], off nt
	v_cvt_pk_f32_fp8_e32 v[18:19], v11
	v_cvt_pk_f32_fp8_e32 v[24:25], v49
	v_cvt_pk_f32_fp8_e32 v[14:15], v10
	v_cvt_pk_f32_fp8_sdwa v[16:17], v10 src0_sel:WORD_1
	v_cvt_pk_f32_fp8_sdwa v[26:27], v49 src0_sel:WORD_1
	v_cvt_pk_f32_fp8_sdwa v[10:11], v11 src0_sel:WORD_1
	v_pk_mul_f32 v[14:15], v[14:15], s[0:1] op_sel_hi:[1,0]
	v_pk_mul_f32 v[16:17], v[16:17], s[0:1] op_sel_hi:[1,0]
	v_cvt_pk_f32_fp8_sdwa v[22:23], v48 src0_sel:WORD_1
	v_pk_mul_f32 v[20:21], v[112:113], v[16:17]
	v_pk_mul_f32 v[16:17], v[110:111], v[14:15]
	v_pk_mul_f32 v[14:15], v[18:19], s[0:1] op_sel_hi:[1,0]
	v_pk_mul_f32 v[10:11], v[10:11], s[0:1] op_sel_hi:[1,0]
	v_pk_mul_f32 v[18:19], v[106:107], v[14:15]
	v_cvt_pk_f32_fp8_e32 v[14:15], v48
	v_pk_mul_f32 v[10:11], v[108:109], v[10:11]
	v_pk_mul_f32 v[22:23], v[22:23], s[0:1] op_sel_hi:[1,0]
	v_permlane16_swap_b32_e32 v6, v50
	v_pk_mul_f32 v[14:15], v[14:15], s[0:1] op_sel_hi:[1,0]
	v_pk_mul_f32 v[22:23], v[104:105], v[22:23]
	v_pk_mul_f32 v[28:29], v[102:103], v[14:15]
	v_pk_mul_f32 v[14:15], v[24:25], s[0:1] op_sel_hi:[1,0]
	v_pk_mul_f32 v[24:25], v[26:27], s[0:1] op_sel_hi:[1,0]
	v_pk_mul_f32 v[26:27], v[98:99], v[14:15]
	v_mov_b32_e32 v15, v199
	v_mov_b32_e32 v14, v199
	v_cvt_pk_fp8_f32 v15, v18, v19
	v_cvt_pk_fp8_f32 v14, v16, v17
	v_mov_b32_e32 v16, v199
	v_mov_b32_e32 v17, v199
	v_cvt_pk_fp8_f32 v16, v28, v29
	v_cvt_pk_fp8_f32 v17, v26, v27
	v_cvt_pk_fp8_f32 v15, v10, v11 op_sel:[0,0,1]
	v_add_u32_e32 v10, 0x90, v8
	v_pk_mul_f32 v[24:25], v[100:101], v[24:25]
	v_ashrrev_i32_e32 v11, 31, v10
	v_cvt_pk_fp8_f32 v14, v20, v21 op_sel:[0,0,1]
	v_cvt_pk_fp8_f32 v16, v22, v23 op_sel:[0,0,1]
	v_cvt_pk_fp8_f32 v17, v24, v25 op_sel:[0,0,1]
	v_lshlrev_b64 v[10:11], 10, v[10:11]
	v_lshl_add_u64 v[10:11], s[14:15], 0, v[10:11]
	v_lshl_add_u64 v[10:11], v[10:11], 0, v[4:5]
	v_lshl_add_u64 v[10:11], v[10:11], 0, v[204:205]
	v_lshl_add_u64 v[10:11], v[10:11], 0, v[206:207]
	v_permlane16_swap_b32_e32 v14, v16
	v_permlane16_swap_b32_e32 v15, v17
	v_permlane16_swap_b32_e32 v7, v51
	global_store_dwordx4 v[10:11], v[14:17], off nt
	v_cvt_pk_f32_fp8_e32 v[22:23], v51
	v_cvt_pk_f32_fp8_sdwa v[24:25], v51 src0_sel:WORD_1
	v_cvt_pk_f32_fp8_sdwa v[14:15], v6 src0_sel:WORD_1
	v_cvt_pk_f32_fp8_e32 v[16:17], v7
	v_cvt_pk_f32_fp8_e32 v[10:11], v6
	v_cvt_pk_f32_fp8_sdwa v[6:7], v7 src0_sel:WORD_1
	v_pk_mul_f32 v[14:15], v[14:15], s[0:1] op_sel_hi:[1,0]
	v_cvt_pk_f32_fp8_sdwa v[20:21], v50 src0_sel:WORD_1
	v_pk_mul_f32 v[18:19], v[88:89], v[14:15]
	v_pk_mul_f32 v[14:15], v[16:17], s[0:1] op_sel_hi:[1,0]
	v_pk_mul_f32 v[10:11], v[10:11], s[0:1] op_sel_hi:[1,0]
	v_pk_mul_f32 v[16:17], v[82:83], v[14:15]
	v_cvt_pk_f32_fp8_e32 v[14:15], v50
	v_pk_mul_f32 v[10:11], v[86:87], v[10:11]
	v_pk_mul_f32 v[6:7], v[6:7], s[0:1] op_sel_hi:[1,0]
	v_pk_mul_f32 v[20:21], v[20:21], s[0:1] op_sel_hi:[1,0]
	v_pk_mul_f32 v[14:15], v[14:15], s[0:1] op_sel_hi:[1,0]
	v_pk_mul_f32 v[6:7], v[84:85], v[6:7]
	v_pk_mul_f32 v[26:27], v[94:95], v[14:15]
	v_pk_mul_f32 v[14:15], v[22:23], s[0:1] op_sel_hi:[1,0]
	v_pk_mul_f32 v[22:23], v[24:25], s[0:1] op_sel_hi:[1,0]
	v_pk_mul_f32 v[24:25], v[90:91], v[14:15]
	v_mov_b32_e32 v15, v199
	v_cvt_pk_fp8_f32 v15, v16, v17
	v_mov_b32_e32 v14, v199
	v_mov_b32_e32 v16, v199
	v_mov_b32_e32 v17, v199
	v_cvt_pk_fp8_f32 v14, v10, v11
	v_cvt_pk_fp8_f32 v16, v26, v27
	v_cvt_pk_fp8_f32 v17, v24, v25
	v_cvt_pk_fp8_f32 v15, v6, v7 op_sel:[0,0,1]
	v_add_u32_e32 v6, 0xa0, v8
	v_pk_mul_f32 v[20:21], v[96:97], v[20:21]
	v_pk_mul_f32 v[22:23], v[92:93], v[22:23]
	v_ashrrev_i32_e32 v7, 31, v6
	v_cvt_pk_fp8_f32 v14, v18, v19 op_sel:[0,0,1]
	v_cvt_pk_fp8_f32 v16, v20, v21 op_sel:[0,0,1]
	v_cvt_pk_fp8_f32 v17, v22, v23 op_sel:[0,0,1]
	v_lshlrev_b64 v[6:7], 10, v[6:7]
	v_lshl_add_u64 v[6:7], s[14:15], 0, v[6:7]
	v_lshl_add_u64 v[6:7], v[6:7], 0, v[4:5]
	v_permlane16_swap_b32_e32 v2, v12
	v_lshl_add_u64 v[6:7], v[6:7], 0, v[204:205]
	v_permlane16_swap_b32_e32 v3, v13
	v_lshl_add_u64 v[6:7], v[6:7], 0, v[206:207]
	v_permlane16_swap_b32_e32 v14, v16
	v_permlane16_swap_b32_e32 v15, v17
	v_cvt_pk_f32_fp8_sdwa v[10:11], v2 src0_sel:WORD_1
	global_store_dwordx4 v[6:7], v[14:17], off nt
	v_cvt_pk_f32_fp8_e32 v[20:21], v13
	v_cvt_pk_f32_fp8_e32 v[6:7], v2
	v_cvt_pk_f32_fp8_e32 v[14:15], v3
	v_pk_mul_f32 v[10:11], v[10:11], s[0:1] op_sel_hi:[1,0]
	v_cvt_pk_f32_fp8_sdwa v[18:19], v12 src0_sel:WORD_1
	v_pk_mul_f32 v[16:17], v[72:73], v[10:11]
	v_pk_mul_f32 v[10:11], v[14:15], s[0:1] op_sel_hi:[1,0]
	v_cvt_pk_f32_fp8_sdwa v[2:3], v3 src0_sel:WORD_1
	v_pk_mul_f32 v[14:15], v[66:67], v[10:11]
	v_cvt_pk_f32_fp8_e32 v[10:11], v12
	v_cvt_pk_f32_fp8_sdwa v[12:13], v13 src0_sel:WORD_1
	v_pk_mul_f32 v[6:7], v[6:7], s[0:1] op_sel_hi:[1,0]
	v_pk_mul_f32 v[2:3], v[2:3], s[0:1] op_sel_hi:[1,0]
	v_pk_mul_f32 v[10:11], v[10:11], s[0:1] op_sel_hi:[1,0]
	v_pk_mul_f32 v[12:13], v[12:13], s[0:1] op_sel_hi:[1,0]
	v_pk_mul_f32 v[22:23], v[78:79], v[10:11]
	v_pk_mul_f32 v[10:11], v[20:21], s[0:1] op_sel_hi:[1,0]
	v_pk_mul_f32 v[6:7], v[70:71], v[6:7]
	v_pk_mul_f32 v[24:25], v[74:75], v[10:11]
	v_mov_b32_e32 v11, v199
	v_cvt_pk_fp8_f32 v11, v14, v15
	v_pk_mul_f32 v[20:21], v[76:77], v[12:13]
	v_mov_b32_e32 v10, v199
	v_mov_b32_e32 v12, v199
	v_mov_b32_e32 v13, v199
	v_cvt_pk_fp8_f32 v10, v6, v7
	v_cvt_pk_fp8_f32 v12, v22, v23
	v_cvt_pk_fp8_f32 v13, v24, v25
	v_pk_mul_f32 v[2:3], v[68:69], v[2:3]
	v_pk_mul_f32 v[18:19], v[18:19], s[0:1] op_sel_hi:[1,0]
	v_cvt_pk_fp8_f32 v11, v2, v3 op_sel:[0,0,1]
	v_add_u32_e32 v2, 0xb0, v8
	v_pk_mul_f32 v[18:19], v[80:81], v[18:19]
	v_ashrrev_i32_e32 v3, 31, v2
	v_cvt_pk_fp8_f32 v10, v16, v17 op_sel:[0,0,1]
	v_cvt_pk_fp8_f32 v12, v18, v19 op_sel:[0,0,1]
	v_cvt_pk_fp8_f32 v13, v20, v21 op_sel:[0,0,1]
	v_lshlrev_b64 v[2:3], 10, v[2:3]
	v_lshl_add_u64 v[2:3], s[14:15], 0, v[2:3]
	v_lshl_add_u64 v[2:3], v[2:3], 0, v[4:5]
	v_lshl_add_u64 v[2:3], v[2:3], 0, v[204:205]
	v_lshl_add_u64 v[2:3], v[2:3], 0, v[206:207]
	v_permlane16_swap_b32_e32 v10, v12
	v_permlane16_swap_b32_e32 v11, v13
	global_store_dwordx4 v[2:3], v[10:13], off nt
	s_cbranch_vccnz .LBB0_470
	s_andn2_b64 vcc, exec, s[10:11]
	s_cbranch_vccnz .LBB0_469
	s_barrier
	s_branch .LBB0_469

.LBB0_579:
	s_lshl_b32 s2, s57, 8
	s_add_i32 s2, s2, s59
	s_lshl_b32 s36, s34, 8
	v_or_b32_e32 v2, s36, v222
	v_or_b32_e32 v212, s2, v219
	v_ashrrev_i32_e32 v3, 31, v2
	v_ashrrev_i32_e32 v213, 31, v212
	v_lshl_add_u64 v[214:215], v[2:3], 2, s[80:81]
	v_lshlrev_b64 v[2:3], 12, v[212:213]
	v_or_b32_e32 v210, 16, v212
	v_or_b32_e32 v208, 32, v212
	s_waitcnt vmcnt(0)
	v_lshl_add_u64 v[6:7], v[214:215], 0, v[2:3]
	v_or_b32_e32 v206, 48, v212
	v_ashrrev_i32_e32 v211, 31, v210
	v_ashrrev_i32_e32 v209, 31, v208
	global_load_dwordx4 v[2:5], v[6:7], off nt
	global_load_dwordx4 v[54:57], v[6:7], off offset:64 nt
	global_load_dwordx4 v[58:61], v[6:7], off offset:128 nt
	global_load_dwordx4 v[62:65], v[6:7], off offset:192 nt
	v_ashrrev_i32_e32 v207, 31, v206
	v_lshlrev_b64 v[6:7], 12, v[210:211]
	v_lshlrev_b64 v[8:9], 12, v[208:209]
	v_lshlrev_b64 v[10:11], 12, v[206:207]
	v_lshl_add_u64 v[6:7], v[214:215], 0, v[6:7]
	v_lshl_add_u64 v[8:9], v[214:215], 0, v[8:9]
	v_lshl_add_u64 v[226:227], v[214:215], 0, v[10:11]
	global_load_dwordx4 v[22:25], v[6:7], off nt
	global_load_dwordx4 v[50:53], v[6:7], off offset:64 nt
	global_load_dwordx4 v[46:49], v[6:7], off offset:128 nt
	global_load_dwordx4 v[42:45], v[6:7], off offset:192 nt
	global_load_dwordx4 v[38:41], v[8:9], off nt
	global_load_dwordx4 v[34:37], v[8:9], off offset:64 nt
	global_load_dwordx4 v[30:33], v[8:9], off offset:128 nt
	global_load_dwordx4 v[26:29], v[8:9], off offset:192 nt
	global_load_dwordx4 v[18:21], v[226:227], off nt
	global_load_dwordx4 v[14:17], v[226:227], off offset:64 nt
	global_load_dwordx4 v[10:13], v[226:227], off offset:128 nt
	s_nop 0
	global_load_dwordx4 v[6:9], v[226:227], off offset:192 nt
	s_lshl_b32 s34, s34, 2
	s_ashr_i32 s35, s34, 31
	s_or_b64 s[34:35], s[34:35], s[12:13]
	s_waitcnt vmcnt(0)
	v_pk_mul_f32 v[4:5], v[4:5], s[24:25] op_sel_hi:[1,0]
	v_pk_mul_f32 v[2:3], v[2:3], s[24:25] op_sel_hi:[1,0]
	v_pk_mul_f32 v[56:57], v[56:57], s[24:25] op_sel_hi:[1,0]
	v_pk_mul_f32 v[54:55], v[54:55], s[24:25] op_sel_hi:[1,0]
	v_pk_mul_f32 v[60:61], v[60:61], s[24:25] op_sel_hi:[1,0]
	v_pk_fma_f32 v[4:5], v[192:193], s[26:27], v[4:5] op_sel_hi:[1,0,1]
	v_pk_fma_f32 v[2:3], v[190:191], s[26:27], v[2:3] op_sel_hi:[1,0,1]
	v_pk_fma_f32 v[188:189], v[188:189], s[26:27], v[56:57] op_sel_hi:[1,0,1]
	v_pk_fma_f32 v[186:187], v[186:187], s[26:27], v[54:55] op_sel_hi:[1,0,1]
	v_pk_mul_f32 v[58:59], v[58:59], s[24:25] op_sel_hi:[1,0]
	v_pk_fma_f32 v[184:185], v[184:185], s[26:27], v[60:61] op_sel_hi:[1,0,1]
	v_add_f32_e32 v54, v2, v3
	v_add_f32_e32 v55, v4, v5
	v_mul_f32_e32 v56, v3, v3
	v_mul_f32_e32 v57, v5, v5
	v_mul_f32_e32 v60, v187, v187
	v_mul_f32_e32 v61, v189, v189
	v_pk_mul_f32 v[64:65], v[64:65], s[24:25] op_sel_hi:[1,0]
	v_pk_mul_f32 v[62:63], v[62:63], s[24:25] op_sel_hi:[1,0]
	v_pk_fma_f32 v[182:183], v[182:183], s[26:27], v[58:59] op_sel_hi:[1,0,1]
	v_add_f32_e32 v58, v186, v187
	v_add_f32_e32 v59, v188, v189
	v_add_f32_e32 v54, v54, v55
	v_fmac_f32_e32 v56, v2, v2
	v_fmac_f32_e32 v57, v4, v4
	v_fmac_f32_e32 v60, v186, v186
	v_fmac_f32_e32 v61, v188, v188
	v_pk_fma_f32 v[180:181], v[180:181], s[26:27], v[64:65] op_sel_hi:[1,0,1]
	v_pk_fma_f32 v[178:179], v[178:179], s[26:27], v[62:63] op_sel_hi:[1,0,1]
	v_mul_f32_e32 v64, v183, v183
	v_mul_f32_e32 v65, v185, v185
	v_add_f32_e32 v55, v58, v59
	v_add_f32_e32 v54, 0, v54
	v_add_f32_e32 v56, v56, v57
	v_add_f32_e32 v57, v60, v61
	v_add_f32_e32 v62, v182, v183
	v_add_f32_e32 v63, v184, v185
	v_mul_f32_e32 v192, v179, v179
	v_fmac_f32_e32 v64, v182, v182
	v_fmac_f32_e32 v65, v184, v184
	v_add_f32_e32 v54, v54, v55
	v_add_f32_e32 v55, v56, v57
	v_mul_f32_e32 v56, v181, v181
	v_add_f32_e32 v190, v178, v179
	v_add_f32_e32 v191, v180, v181
	v_add_f32_e32 v58, v62, v63
	v_fmac_f32_e32 v192, v178, v178
	v_add_f32_e32 v60, v64, v65
	v_fmac_f32_e32 v56, v180, v180
	v_add_f32_e32 v59, v190, v191
	v_add_f32_e32 v54, v54, v58
	v_add_f32_e32 v55, v55, v60
	v_add_f32_e32 v56, v192, v56
	v_add_f32_e32 v54, v54, v59
	v_add_f32_e32 v55, v55, v56
	v_mov_b32_e32 v56, v54
	v_mov_b32_e32 v57, v55
	s_nop 0
	v_permlane16_swap_b32_e32 v54, v56
	v_permlane16_swap_b32_e32 v55, v57
	v_add_f32_e32 v54, v54, v56
	v_add_f32_e32 v55, v55, v57
	v_mov_b32_e32 v56, v54
	v_mov_b32_e32 v57, v55
	s_nop 0
	v_permlane32_swap_b32_e32 v54, v56
	v_permlane32_swap_b32_e32 v55, v57
	s_and_saveexec_b64 s[38:39], s[4:5]
	s_cbranch_execz .LBB0_581
	v_pk_add_f32 v[54:55], v[54:55], v[56:57]
	v_lshlrev_b64 v[56:57], 7, v[212:213]
	v_lshl_add_u64 v[56:57], s[16:17], 0, v[56:57]
	v_lshl_add_u64 v[56:57], s[34:35], 3, v[56:57]
	global_store_dwordx2 v[56:57], v[54:55], off nt
.LBB0_581:
	s_or_b64 exec, exec, s[38:39]
	v_pk_mul_f32 v[24:25], v[24:25], s[24:25] op_sel_hi:[1,0]
	v_pk_mul_f32 v[22:23], v[22:23], s[24:25] op_sel_hi:[1,0]
	v_pk_fma_f32 v[24:25], v[176:177], s[26:27], v[24:25] op_sel_hi:[1,0,1]
	v_pk_fma_f32 v[22:23], v[174:175], s[26:27], v[22:23] op_sel_hi:[1,0,1]
	v_pk_mul_f32 v[42:43], v[42:43], s[24:25] op_sel_hi:[1,0]
	v_pk_mul_f32 v[44:45], v[44:45], s[24:25] op_sel_hi:[1,0]
	v_pk_fma_f32 v[162:163], v[162:163], s[26:27], v[42:43] op_sel_hi:[1,0,1]
	v_add_f32_e32 v42, v22, v23
	v_add_f32_e32 v43, v24, v25
	v_pk_mul_f32 v[52:53], v[52:53], s[24:25] op_sel_hi:[1,0]
	v_pk_mul_f32 v[50:51], v[50:51], s[24:25] op_sel_hi:[1,0]
	v_pk_fma_f32 v[164:165], v[164:165], s[26:27], v[44:45] op_sel_hi:[1,0,1]
	v_add_f32_e32 v42, v42, v43
	v_mul_f32_e32 v43, v23, v23
	v_mul_f32_e32 v44, v25, v25
	v_pk_fma_f32 v[172:173], v[172:173], s[26:27], v[52:53] op_sel_hi:[1,0,1]
	v_pk_fma_f32 v[170:171], v[170:171], s[26:27], v[50:51] op_sel_hi:[1,0,1]
	v_fmac_f32_e32 v43, v22, v22
	v_fmac_f32_e32 v44, v24, v24
	v_add_f32_e32 v43, v43, v44
	v_add_f32_e32 v44, v170, v171
	v_add_f32_e32 v45, v172, v173
	v_add_f32_e32 v42, 0, v42
	v_add_f32_e32 v44, v44, v45
	v_add_f32_e32 v42, v42, v44
	v_mul_f32_e32 v44, v171, v171
	v_mul_f32_e32 v45, v173, v173
	v_pk_mul_f32 v[48:49], v[48:49], s[24:25] op_sel_hi:[1,0]
	v_pk_mul_f32 v[46:47], v[46:47], s[24:25] op_sel_hi:[1,0]
	v_fmac_f32_e32 v44, v170, v170
	v_fmac_f32_e32 v45, v172, v172
	v_pk_fma_f32 v[168:169], v[168:169], s[26:27], v[48:49] op_sel_hi:[1,0,1]
	v_pk_fma_f32 v[166:167], v[166:167], s[26:27], v[46:47] op_sel_hi:[1,0,1]
	v_add_f32_e32 v44, v44, v45
	v_add_f32_e32 v43, v43, v44
	v_add_f32_e32 v44, v166, v167
	v_add_f32_e32 v45, v168, v169
	v_add_f32_e32 v44, v44, v45
	v_add_f32_e32 v42, v42, v44
	v_mul_f32_e32 v44, v167, v167
	v_mul_f32_e32 v45, v169, v169
	v_fmac_f32_e32 v44, v166, v166
	v_fmac_f32_e32 v45, v168, v168
	v_add_f32_e32 v44, v44, v45
	v_add_f32_e32 v43, v43, v44
	v_add_f32_e32 v44, v162, v163
	v_add_f32_e32 v45, v164, v165
	v_add_f32_e32 v44, v44, v45
	v_add_f32_e32 v42, v42, v44
	v_mul_f32_e32 v44, v163, v163
	v_mul_f32_e32 v45, v165, v165
	v_fmac_f32_e32 v44, v162, v162
	v_fmac_f32_e32 v45, v164, v164
	v_add_f32_e32 v44, v44, v45
	v_add_f32_e32 v43, v43, v44
	v_mov_b32_e32 v44, v42
	v_mov_b32_e32 v45, v43
	s_nop 0
	v_permlane16_swap_b32_e32 v42, v44
	v_permlane16_swap_b32_e32 v43, v45
	v_add_f32_e32 v42, v42, v44
	v_add_f32_e32 v43, v43, v45
	v_mov_b32_e32 v44, v42
	v_mov_b32_e32 v45, v43
	s_nop 0
	v_permlane32_swap_b32_e32 v42, v44
	v_permlane32_swap_b32_e32 v43, v45
	s_and_saveexec_b64 s[38:39], s[4:5]
	s_cbranch_execz .LBB0_583
	v_pk_add_f32 v[42:43], v[42:43], v[44:45]
	v_lshlrev_b64 v[44:45], 7, v[210:211]
	v_lshl_add_u64 v[44:45], s[16:17], 0, v[44:45]
	v_lshl_add_u64 v[44:45], s[34:35], 3, v[44:45]
	global_store_dwordx2 v[44:45], v[42:43], off nt
.LBB0_583:
	s_or_b64 exec, exec, s[38:39]
	v_pk_mul_f32 v[40:41], v[40:41], s[24:25] op_sel_hi:[1,0]
	v_pk_mul_f32 v[38:39], v[38:39], s[24:25] op_sel_hi:[1,0]
	v_pk_fma_f32 v[44:45], v[160:161], s[26:27], v[40:41] op_sel_hi:[1,0,1]
	v_pk_fma_f32 v[42:43], v[158:159], s[26:27], v[38:39] op_sel_hi:[1,0,1]
	v_pk_mul_f32 v[26:27], v[26:27], s[24:25] op_sel_hi:[1,0]
	v_pk_mul_f32 v[28:29], v[28:29], s[24:25] op_sel_hi:[1,0]
	v_pk_fma_f32 v[146:147], v[146:147], s[26:27], v[26:27] op_sel_hi:[1,0,1]
	v_add_f32_e32 v26, v42, v43
	v_add_f32_e32 v27, v44, v45
	v_pk_mul_f32 v[36:37], v[36:37], s[24:25] op_sel_hi:[1,0]
	v_pk_mul_f32 v[34:35], v[34:35], s[24:25] op_sel_hi:[1,0]
	v_pk_fma_f32 v[148:149], v[148:149], s[26:27], v[28:29] op_sel_hi:[1,0,1]
	v_add_f32_e32 v26, v26, v27
	v_mul_f32_e32 v27, v43, v43
	v_mul_f32_e32 v28, v45, v45
	v_pk_fma_f32 v[156:157], v[156:157], s[26:27], v[36:37] op_sel_hi:[1,0,1]
	v_pk_fma_f32 v[154:155], v[154:155], s[26:27], v[34:35] op_sel_hi:[1,0,1]
	v_fmac_f32_e32 v27, v42, v42
	v_fmac_f32_e32 v28, v44, v44
	v_add_f32_e32 v27, v27, v28
	v_add_f32_e32 v28, v154, v155
	v_add_f32_e32 v29, v156, v157
	v_add_f32_e32 v26, 0, v26
	v_add_f32_e32 v28, v28, v29
	v_add_f32_e32 v26, v26, v28
	v_mul_f32_e32 v28, v155, v155
	v_mul_f32_e32 v29, v157, v157
	v_pk_mul_f32 v[32:33], v[32:33], s[24:25] op_sel_hi:[1,0]
	v_pk_mul_f32 v[30:31], v[30:31], s[24:25] op_sel_hi:[1,0]
	v_fmac_f32_e32 v28, v154, v154
	v_fmac_f32_e32 v29, v156, v156
	v_pk_fma_f32 v[152:153], v[152:153], s[26:27], v[32:33] op_sel_hi:[1,0,1]
	v_pk_fma_f32 v[150:151], v[150:151], s[26:27], v[30:31] op_sel_hi:[1,0,1]
	v_add_f32_e32 v28, v28, v29
	v_add_f32_e32 v27, v27, v28
	v_add_f32_e32 v28, v150, v151
	v_add_f32_e32 v29, v152, v153
	v_add_f32_e32 v28, v28, v29
	v_add_f32_e32 v26, v26, v28
	v_mul_f32_e32 v28, v151, v151
	v_mul_f32_e32 v29, v153, v153
	v_fmac_f32_e32 v28, v150, v150
	v_fmac_f32_e32 v29, v152, v152
	v_add_f32_e32 v28, v28, v29
	v_add_f32_e32 v27, v27, v28
	v_add_f32_e32 v28, v146, v147
	v_add_f32_e32 v29, v148, v149
	v_add_f32_e32 v28, v28, v29
	v_add_f32_e32 v26, v26, v28
	v_mul_f32_e32 v28, v147, v147
	v_mul_f32_e32 v29, v149, v149
	v_fmac_f32_e32 v28, v146, v146
	v_fmac_f32_e32 v29, v148, v148
	v_add_f32_e32 v28, v28, v29
	v_add_f32_e32 v27, v27, v28
	v_mov_b32_e32 v28, v26
	v_mov_b32_e32 v29, v27
	s_nop 0
	v_permlane16_swap_b32_e32 v26, v28
	v_permlane16_swap_b32_e32 v27, v29
	v_add_f32_e32 v26, v26, v28
	v_add_f32_e32 v27, v27, v29
	v_mov_b32_e32 v28, v26
	v_mov_b32_e32 v29, v27
	s_nop 0
	v_permlane32_swap_b32_e32 v26, v28
	v_permlane32_swap_b32_e32 v27, v29
	s_and_saveexec_b64 s[38:39], s[4:5]
	s_cbranch_execz .LBB0_585
	v_pk_add_f32 v[26:27], v[26:27], v[28:29]
	v_lshlrev_b64 v[28:29], 7, v[208:209]
	v_lshl_add_u64 v[28:29], s[16:17], 0, v[28:29]
	v_lshl_add_u64 v[28:29], s[34:35], 3, v[28:29]
	global_store_dwordx2 v[28:29], v[26:27], off nt
.LBB0_585:
	s_or_b64 exec, exec, s[38:39]
	v_pk_mul_f32 v[20:21], v[20:21], s[24:25] op_sel_hi:[1,0]
	v_pk_mul_f32 v[18:19], v[18:19], s[24:25] op_sel_hi:[1,0]
	v_pk_fma_f32 v[60:61], v[144:145], s[26:27], v[20:21] op_sel_hi:[1,0,1]
	v_pk_fma_f32 v[58:59], v[142:143], s[26:27], v[18:19] op_sel_hi:[1,0,1]
	v_pk_mul_f32 v[6:7], v[6:7], s[24:25] op_sel_hi:[1,0]
	v_pk_mul_f32 v[8:9], v[8:9], s[24:25] op_sel_hi:[1,0]
	v_pk_fma_f32 v[174:175], v[130:131], s[26:27], v[6:7] op_sel_hi:[1,0,1]
	v_add_f32_e32 v6, v58, v59
	v_add_f32_e32 v7, v60, v61
	v_pk_mul_f32 v[16:17], v[16:17], s[24:25] op_sel_hi:[1,0]
	v_pk_mul_f32 v[14:15], v[14:15], s[24:25] op_sel_hi:[1,0]
	v_pk_fma_f32 v[158:159], v[132:133], s[26:27], v[8:9] op_sel_hi:[1,0,1]
	v_add_f32_e32 v6, v6, v7
	v_mul_f32_e32 v7, v59, v59
	v_mul_f32_e32 v8, v61, v61
	v_pk_fma_f32 v[142:143], v[140:141], s[26:27], v[16:17] op_sel_hi:[1,0,1]
	v_pk_fma_f32 v[160:161], v[138:139], s[26:27], v[14:15] op_sel_hi:[1,0,1]
	v_fmac_f32_e32 v7, v58, v58
	v_fmac_f32_e32 v8, v60, v60
	v_add_f32_e32 v7, v7, v8
	v_add_f32_e32 v8, v160, v161
	v_add_f32_e32 v9, v142, v143
	v_add_f32_e32 v6, 0, v6
	v_add_f32_e32 v8, v8, v9
	v_add_f32_e32 v6, v6, v8
	v_mul_f32_e32 v8, v161, v161
	v_mul_f32_e32 v9, v143, v143
	v_pk_mul_f32 v[12:13], v[12:13], s[24:25] op_sel_hi:[1,0]
	v_pk_mul_f32 v[10:11], v[10:11], s[24:25] op_sel_hi:[1,0]
	v_fmac_f32_e32 v8, v160, v160
	v_fmac_f32_e32 v9, v142, v142
	v_pk_fma_f32 v[140:141], v[136:137], s[26:27], v[12:13] op_sel_hi:[1,0,1]
	v_pk_fma_f32 v[144:145], v[134:135], s[26:27], v[10:11] op_sel_hi:[1,0,1]
	v_add_f32_e32 v8, v8, v9
	v_add_f32_e32 v7, v7, v8
	v_add_f32_e32 v8, v144, v145
	v_add_f32_e32 v9, v140, v141
	v_add_f32_e32 v8, v8, v9
	v_add_f32_e32 v6, v6, v8
	v_mul_f32_e32 v8, v145, v145
	v_mul_f32_e32 v9, v141, v141
	v_fmac_f32_e32 v8, v144, v144
	v_fmac_f32_e32 v9, v140, v140
	v_add_f32_e32 v8, v8, v9
	v_add_f32_e32 v7, v7, v8
	v_add_f32_e32 v8, v174, v175
	v_add_f32_e32 v9, v158, v159
	v_add_f32_e32 v8, v8, v9
	v_add_f32_e32 v6, v6, v8
	v_mul_f32_e32 v8, v175, v175
	v_mul_f32_e32 v9, v159, v159
	v_fmac_f32_e32 v8, v174, v174
	v_fmac_f32_e32 v9, v158, v158
	v_add_f32_e32 v8, v8, v9
	v_add_f32_e32 v7, v7, v8
	v_mov_b32_e32 v8, v6
	v_mov_b32_e32 v9, v7
	s_nop 0
	v_permlane16_swap_b32_e32 v6, v8
	v_permlane16_swap_b32_e32 v7, v9
	v_add_f32_e32 v6, v6, v8
	v_add_f32_e32 v7, v7, v9
	v_mov_b32_e32 v8, v6
	v_mov_b32_e32 v9, v7
	s_nop 0
	v_permlane32_swap_b32_e32 v6, v8
	v_permlane32_swap_b32_e32 v7, v9
	s_and_saveexec_b64 s[38:39], s[4:5]
	s_cbranch_execz .LBB0_587
	v_pk_add_f32 v[6:7], v[6:7], v[8:9]
	v_lshlrev_b64 v[8:9], 7, v[206:207]
	v_lshl_add_u64 v[8:9], s[16:17], 0, v[8:9]
	v_lshl_add_u64 v[8:9], s[34:35], 3, v[8:9]
	global_store_dwordx2 v[8:9], v[6:7], off nt
.LBB0_587:
	s_or_b64 exec, exec, s[38:39]
	v_add_u32_e32 v138, s2, v221
	v_ashrrev_i32_e32 v139, 31, v138
	v_lshlrev_b64 v[6:7], 12, v[138:139]
	v_lshl_add_u64 v[6:7], v[214:215], 0, v[6:7]
	global_load_dwordx4 v[190:193], v[6:7], off nt
	global_load_dwordx4 v[226:229], v[6:7], off offset:64 nt
	global_load_dwordx4 v[230:233], v[6:7], off offset:128 nt
	global_load_dwordx4 v[234:237], v[6:7], off offset:192 nt
	v_or_b32_e32 v136, 16, v138
	v_ashrrev_i32_e32 v137, 31, v136
	v_lshlrev_b64 v[6:7], 12, v[136:137]
	v_or_b32_e32 v134, 32, v138
	v_lshl_add_u64 v[6:7], v[214:215], 0, v[6:7]
	v_ashrrev_i32_e32 v135, 31, v134
	global_load_dwordx4 v[62:65], v[6:7], off nt
	global_load_dwordx4 v[54:57], v[6:7], off offset:64 nt
	global_load_dwordx4 v[50:53], v[6:7], off offset:128 nt
	global_load_dwordx4 v[46:49], v[6:7], off offset:192 nt
	v_lshlrev_b64 v[6:7], 12, v[134:135]
	v_or_b32_e32 v130, 48, v138
	v_lshl_add_u64 v[6:7], v[214:215], 0, v[6:7]
	v_ashrrev_i32_e32 v131, 31, v130
	global_load_dwordx4 v[38:41], v[6:7], off nt
	global_load_dwordx4 v[34:37], v[6:7], off offset:64 nt
	global_load_dwordx4 v[30:33], v[6:7], off offset:128 nt
	global_load_dwordx4 v[26:29], v[6:7], off offset:192 nt
	v_lshlrev_b64 v[6:7], 12, v[130:131]
	v_lshl_add_u64 v[6:7], v[214:215], 0, v[6:7]
	global_load_dwordx4 v[18:21], v[6:7], off nt
	global_load_dwordx4 v[14:17], v[6:7], off offset:64 nt
	global_load_dwordx4 v[10:13], v[6:7], off offset:128 nt
	s_nop 0
	global_load_dwordx4 v[6:9], v[6:7], off offset:192 nt
	s_ashr_i32 s37, s36, 31
	v_lshl_add_u64 v[132:133], s[36:37], 1, v[202:203]
	v_lshlrev_b64 v[176:177], 11, v[212:213]
	v_cvt_pk_bf16_f32 v212, v2, v3
	v_cvt_pk_bf16_f32 v213, v4, v5
	v_cvt_pk_bf16_f32 v2, v182, v183
	v_cvt_pk_bf16_f32 v4, v178, v179
	v_cvt_pk_bf16_f32 v3, v184, v185
	v_cvt_pk_bf16_f32 v5, v180, v181
	v_lshl_add_u64 v[176:177], v[132:133], 0, v[176:177]
	v_cvt_pk_bf16_f32 v214, v186, v187
	v_cvt_pk_bf16_f32 v215, v188, v189
	v_permlane16_swap_b32_e32 v2, v4
	v_permlane16_swap_b32_e32 v3, v5
	v_permlane16_swap_b32_e32 v212, v214
	v_permlane16_swap_b32_e32 v213, v215
	global_store_dwordx4 v[176:177], v[2:5], off offset:64 nt
	global_store_dwordx4 v[176:177], v[212:215], off nt
	s_nop 0
	v_lshlrev_b64 v[2:3], 11, v[210:211]
	v_lshl_add_u64 v[176:177], v[132:133], 0, v[2:3]
	v_cvt_pk_bf16_f32 v2, v22, v23
	v_cvt_pk_bf16_f32 v4, v170, v171
	v_cvt_pk_bf16_f32 v3, v24, v25
	v_cvt_pk_bf16_f32 v5, v172, v173
	v_permlane16_swap_b32_e32 v2, v4
	s_nop 0
	v_permlane16_swap_b32_e32 v3, v5
	global_store_dwordx4 v[176:177], v[2:5], off nt
	s_nop 1
	v_cvt_pk_bf16_f32 v2, v166, v167
	v_cvt_pk_bf16_f32 v4, v162, v163
	v_cvt_pk_bf16_f32 v3, v168, v169
	v_cvt_pk_bf16_f32 v5, v164, v165
	v_permlane16_swap_b32_e32 v2, v4
	s_nop 0
	v_permlane16_swap_b32_e32 v3, v5
	global_store_dwordx4 v[176:177], v[2:5], off offset:64 nt
	s_nop 1
	v_lshlrev_b64 v[2:3], 11, v[208:209]
	v_lshl_add_u64 v[22:23], v[132:133], 0, v[2:3]
	v_cvt_pk_bf16_f32 v2, v42, v43
	v_cvt_pk_bf16_f32 v4, v154, v155
	v_cvt_pk_bf16_f32 v3, v44, v45
	v_cvt_pk_bf16_f32 v5, v156, v157
	v_permlane16_swap_b32_e32 v2, v4
	s_nop 0
	v_permlane16_swap_b32_e32 v3, v5
	global_store_dwordx4 v[22:23], v[2:5], off nt
	s_waitcnt vmcnt(19)
	v_pk_mul_f32 v[42:43], v[226:227], s[24:25] op_sel_hi:[1,0]
	v_cvt_pk_bf16_f32 v2, v150, v151
	v_cvt_pk_bf16_f32 v4, v146, v147
	v_cvt_pk_bf16_f32 v3, v152, v153
	v_cvt_pk_bf16_f32 v5, v148, v149
	v_permlane16_swap_b32_e32 v2, v4
	s_nop 0
	v_permlane16_swap_b32_e32 v3, v5
	global_store_dwordx4 v[22:23], v[2:5], off offset:64 nt
	s_waitcnt vmcnt(18)
	v_pk_mul_f32 v[44:45], v[236:237], s[24:25] op_sel_hi:[1,0]
	v_lshlrev_b64 v[2:3], 11, v[206:207]
	v_lshl_add_u64 v[22:23], v[132:133], 0, v[2:3]
	v_cvt_pk_bf16_f32 v2, v58, v59
	v_cvt_pk_bf16_f32 v4, v160, v161
	v_cvt_pk_bf16_f32 v3, v60, v61
	v_cvt_pk_bf16_f32 v5, v142, v143
	v_permlane16_swap_b32_e32 v2, v4
	s_nop 0
	v_permlane16_swap_b32_e32 v3, v5
	global_store_dwordx4 v[22:23], v[2:5], off nt
	v_pk_mul_f32 v[60:61], v[234:235], s[24:25] op_sel_hi:[1,0]
	v_pk_fma_f32 v[44:45], v[116:117], s[26:27], v[44:45] op_sel_hi:[1,0,1]
	v_cvt_pk_bf16_f32 v2, v144, v145
	v_cvt_pk_bf16_f32 v4, v174, v175
	v_cvt_pk_bf16_f32 v3, v140, v141
	v_cvt_pk_bf16_f32 v5, v158, v159
	v_permlane16_swap_b32_e32 v2, v4
	s_nop 0
	v_permlane16_swap_b32_e32 v3, v5
	global_store_dwordx4 v[22:23], v[2:5], off offset:64 nt
	v_pk_fma_f32 v[60:61], v[114:115], s[26:27], v[60:61] op_sel_hi:[1,0,1]
	v_pk_fma_f32 v[58:59], v[122:123], s[26:27], v[42:43] op_sel_hi:[1,0,1]
	v_pk_mul_f32 v[2:3], v[192:193], s[24:25] op_sel_hi:[1,0]
	v_pk_mul_f32 v[4:5], v[190:191], s[24:25] op_sel_hi:[1,0]
	v_pk_fma_f32 v[2:3], v[128:129], s[26:27], v[2:3] op_sel_hi:[1,0,1]
	v_pk_fma_f32 v[22:23], v[126:127], s[26:27], v[4:5] op_sel_hi:[1,0,1]
	v_add_f32_e32 v115, v2, v3
	v_add_f32_e32 v114, v22, v23
	v_pk_mul_f32 v[4:5], v[228:229], s[24:25] op_sel_hi:[1,0]
	v_add_f32_e32 v114, v114, v115
	v_mul_f32_e32 v115, v23, v23
	v_mul_f32_e32 v116, v3, v3
	v_pk_fma_f32 v[24:25], v[124:125], s[26:27], v[4:5] op_sel_hi:[1,0,1]
	v_fmac_f32_e32 v115, v22, v22
	v_fmac_f32_e32 v116, v2, v2
	v_add_f32_e32 v115, v115, v116
	v_add_f32_e32 v116, v58, v59
	v_add_f32_e32 v117, v24, v25
	v_add_f32_e32 v114, 0, v114
	v_add_f32_e32 v116, v116, v117
	v_add_f32_e32 v114, v114, v116
	v_mul_f32_e32 v116, v59, v59
	v_mul_f32_e32 v117, v25, v25
	v_pk_mul_f32 v[4:5], v[232:233], s[24:25] op_sel_hi:[1,0]
	v_pk_mul_f32 v[42:43], v[230:231], s[24:25] op_sel_hi:[1,0]
	v_fmac_f32_e32 v116, v58, v58
	v_fmac_f32_e32 v117, v24, v24
	v_pk_fma_f32 v[4:5], v[120:121], s[26:27], v[4:5] op_sel_hi:[1,0,1]
	v_pk_fma_f32 v[42:43], v[118:119], s[26:27], v[42:43] op_sel_hi:[1,0,1]
	v_add_f32_e32 v116, v116, v117
	v_add_f32_e32 v115, v115, v116
	v_add_f32_e32 v116, v42, v43
	v_add_f32_e32 v117, v4, v5
	v_add_f32_e32 v116, v116, v117
	v_add_f32_e32 v114, v114, v116
	v_mul_f32_e32 v116, v43, v43
	v_mul_f32_e32 v117, v5, v5
	v_fmac_f32_e32 v116, v42, v42
	v_fmac_f32_e32 v117, v4, v4
	v_add_f32_e32 v116, v116, v117
	v_add_f32_e32 v115, v115, v116
	v_add_f32_e32 v116, v60, v61
	v_add_f32_e32 v117, v44, v45
	v_add_f32_e32 v116, v116, v117
	v_add_f32_e32 v114, v114, v116
	v_mul_f32_e32 v116, v61, v61
	v_mul_f32_e32 v117, v45, v45
	v_fmac_f32_e32 v116, v60, v60
	v_fmac_f32_e32 v117, v44, v44
	v_add_f32_e32 v116, v116, v117
	v_add_f32_e32 v115, v115, v116
	v_mov_b32_e32 v116, v114
	v_mov_b32_e32 v117, v115
	s_nop 0
	v_permlane16_swap_b32_e32 v114, v116
	v_permlane16_swap_b32_e32 v115, v117
	v_add_f32_e32 v114, v114, v116
	v_add_f32_e32 v115, v115, v117
	v_mov_b32_e32 v116, v114
	v_mov_b32_e32 v117, v115
	s_nop 0
	v_permlane32_swap_b32_e32 v114, v116
	v_permlane32_swap_b32_e32 v115, v117
	s_and_saveexec_b64 s[36:37], s[4:5]
	s_cbranch_execz .LBB0_589
	v_pk_add_f32 v[114:115], v[114:115], v[116:117]
	v_lshlrev_b64 v[116:117], 7, v[138:139]
	v_lshl_add_u64 v[116:117], s[16:17], 0, v[116:117]
	v_lshl_add_u64 v[116:117], s[34:35], 3, v[116:117]
	global_store_dwordx2 v[116:117], v[114:115], off nt
.LBB0_589:
	s_or_b64 exec, exec, s[36:37]
	s_waitcnt vmcnt(19)
	v_pk_mul_f32 v[64:65], v[64:65], s[24:25] op_sel_hi:[1,0]
	v_pk_mul_f32 v[114:115], v[62:63], s[24:25] op_sel_hi:[1,0]
	v_pk_fma_f32 v[62:63], v[112:113], s[26:27], v[64:65] op_sel_hi:[1,0,1]
	v_pk_fma_f32 v[64:65], v[110:111], s[26:27], v[114:115] op_sel_hi:[1,0,1]
	s_waitcnt vmcnt(18)
	v_pk_mul_f32 v[56:57], v[56:57], s[24:25] op_sel_hi:[1,0]
	v_pk_mul_f32 v[110:111], v[54:55], s[24:25] op_sel_hi:[1,0]
	v_pk_fma_f32 v[54:55], v[108:109], s[26:27], v[56:57] op_sel_hi:[1,0,1]
	v_pk_fma_f32 v[56:57], v[106:107], s[26:27], v[110:111] op_sel_hi:[1,0,1]
	s_waitcnt vmcnt(17)
	v_pk_mul_f32 v[52:53], v[52:53], s[24:25] op_sel_hi:[1,0]
	v_pk_mul_f32 v[106:107], v[50:51], s[24:25] op_sel_hi:[1,0]
	v_pk_fma_f32 v[50:51], v[104:105], s[26:27], v[52:53] op_sel_hi:[1,0,1]
	v_pk_fma_f32 v[52:53], v[102:103], s[26:27], v[106:107] op_sel_hi:[1,0,1]
	s_waitcnt vmcnt(16)
	v_pk_mul_f32 v[48:49], v[48:49], s[24:25] op_sel_hi:[1,0]
	v_pk_mul_f32 v[102:103], v[46:47], s[24:25] op_sel_hi:[1,0]
	v_pk_fma_f32 v[46:47], v[92:93], s[26:27], v[48:49] op_sel_hi:[1,0,1]
	v_pk_fma_f32 v[48:49], v[90:91], s[26:27], v[102:103] op_sel_hi:[1,0,1]
	v_add_f32_e32 v90, v64, v65
	v_add_f32_e32 v91, v62, v63
	v_add_f32_e32 v90, v90, v91
	v_mul_f32_e32 v91, v65, v65
	v_mul_f32_e32 v92, v63, v63
	v_fmac_f32_e32 v91, v64, v64
	v_fmac_f32_e32 v92, v62, v62
	v_add_f32_e32 v91, v91, v92
	v_add_f32_e32 v92, v56, v57
	v_add_f32_e32 v93, v54, v55
	v_add_f32_e32 v90, 0, v90
	v_add_f32_e32 v92, v92, v93
	v_add_f32_e32 v90, v90, v92
	v_mul_f32_e32 v92, v57, v57
	v_mul_f32_e32 v93, v55, v55
	v_fmac_f32_e32 v92, v56, v56
	v_fmac_f32_e32 v93, v54, v54
	v_add_f32_e32 v92, v92, v93
	v_add_f32_e32 v91, v91, v92
	v_add_f32_e32 v92, v52, v53
	v_add_f32_e32 v93, v50, v51
	v_add_f32_e32 v92, v92, v93
	v_add_f32_e32 v90, v90, v92
	v_mul_f32_e32 v92, v53, v53
	v_mul_f32_e32 v93, v51, v51
	v_fmac_f32_e32 v92, v52, v52
	v_fmac_f32_e32 v93, v50, v50
	v_add_f32_e32 v92, v92, v93
	v_add_f32_e32 v91, v91, v92
	v_add_f32_e32 v92, v48, v49
	v_add_f32_e32 v93, v46, v47
	v_add_f32_e32 v92, v92, v93
	v_add_f32_e32 v90, v90, v92
	v_mul_f32_e32 v92, v49, v49
	v_mul_f32_e32 v93, v47, v47
	v_fmac_f32_e32 v92, v48, v48
	v_fmac_f32_e32 v93, v46, v46
	v_add_f32_e32 v92, v92, v93
	v_add_f32_e32 v91, v91, v92
	v_mov_b32_e32 v92, v90
	v_mov_b32_e32 v93, v91
	s_nop 0
	v_permlane16_swap_b32_e32 v90, v92
	v_permlane16_swap_b32_e32 v91, v93
	v_add_f32_e32 v90, v90, v92
	v_add_f32_e32 v91, v91, v93
	v_mov_b32_e32 v92, v90
	v_mov_b32_e32 v93, v91
	s_nop 0
	v_permlane32_swap_b32_e32 v90, v92
	v_permlane32_swap_b32_e32 v91, v93
	s_and_saveexec_b64 s[36:37], s[4:5]
	s_cbranch_execz .LBB0_591
	v_pk_add_f32 v[90:91], v[90:91], v[92:93]
	v_lshlrev_b64 v[92:93], 7, v[136:137]
	v_lshl_add_u64 v[92:93], s[16:17], 0, v[92:93]
	v_lshl_add_u64 v[92:93], s[34:35], 3, v[92:93]
	global_store_dwordx2 v[92:93], v[90:91], off nt
.LBB0_591:
	s_or_b64 exec, exec, s[36:37]
	s_waitcnt vmcnt(15)
	v_pk_mul_f32 v[40:41], v[40:41], s[24:25] op_sel_hi:[1,0]
	v_pk_mul_f32 v[90:91], v[38:39], s[24:25] op_sel_hi:[1,0]
	v_pk_fma_f32 v[38:39], v[88:89], s[26:27], v[40:41] op_sel_hi:[1,0,1]
	v_pk_fma_f32 v[40:41], v[86:87], s[26:27], v[90:91] op_sel_hi:[1,0,1]
	s_waitcnt vmcnt(14)
	v_pk_mul_f32 v[36:37], v[36:37], s[24:25] op_sel_hi:[1,0]
	v_pk_mul_f32 v[86:87], v[34:35], s[24:25] op_sel_hi:[1,0]
	v_pk_fma_f32 v[34:35], v[84:85], s[26:27], v[36:37] op_sel_hi:[1,0,1]
	v_pk_fma_f32 v[36:37], v[82:83], s[26:27], v[86:87] op_sel_hi:[1,0,1]
	s_waitcnt vmcnt(13)
	v_pk_mul_f32 v[32:33], v[32:33], s[24:25] op_sel_hi:[1,0]
	v_pk_mul_f32 v[82:83], v[30:31], s[24:25] op_sel_hi:[1,0]
	v_pk_fma_f32 v[30:31], v[100:101], s[26:27], v[32:33] op_sel_hi:[1,0,1]
	v_pk_fma_f32 v[32:33], v[98:99], s[26:27], v[82:83] op_sel_hi:[1,0,1]
	s_waitcnt vmcnt(12)
	v_pk_mul_f32 v[28:29], v[28:29], s[24:25] op_sel_hi:[1,0]
	v_pk_mul_f32 v[82:83], v[26:27], s[24:25] op_sel_hi:[1,0]
	v_pk_fma_f32 v[26:27], v[96:97], s[26:27], v[28:29] op_sel_hi:[1,0,1]
	v_pk_fma_f32 v[28:29], v[94:95], s[26:27], v[82:83] op_sel_hi:[1,0,1]
	v_add_f32_e32 v82, v40, v41
	v_add_f32_e32 v83, v38, v39
	v_add_f32_e32 v82, v82, v83
	v_mul_f32_e32 v83, v41, v41
	v_mul_f32_e32 v84, v39, v39
	v_fmac_f32_e32 v83, v40, v40
	v_fmac_f32_e32 v84, v38, v38
	v_add_f32_e32 v83, v83, v84
	v_add_f32_e32 v84, v36, v37
	v_add_f32_e32 v85, v34, v35
	v_add_f32_e32 v82, 0, v82
	v_add_f32_e32 v84, v84, v85
	v_add_f32_e32 v82, v82, v84
	v_mul_f32_e32 v84, v37, v37
	v_mul_f32_e32 v85, v35, v35
	v_fmac_f32_e32 v84, v36, v36
	v_fmac_f32_e32 v85, v34, v34
	v_add_f32_e32 v84, v84, v85
	v_add_f32_e32 v83, v83, v84
	v_add_f32_e32 v84, v32, v33
	v_add_f32_e32 v85, v30, v31
	v_add_f32_e32 v84, v84, v85
	v_add_f32_e32 v82, v82, v84
	v_mul_f32_e32 v84, v33, v33
	v_mul_f32_e32 v85, v31, v31
	v_fmac_f32_e32 v84, v32, v32
	v_fmac_f32_e32 v85, v30, v30
	v_add_f32_e32 v84, v84, v85
	v_add_f32_e32 v83, v83, v84
	v_add_f32_e32 v84, v28, v29
	v_add_f32_e32 v85, v26, v27
	v_add_f32_e32 v84, v84, v85
	v_add_f32_e32 v82, v82, v84
	v_mul_f32_e32 v84, v29, v29
	v_mul_f32_e32 v85, v27, v27
	v_fmac_f32_e32 v84, v28, v28
	v_fmac_f32_e32 v85, v26, v26
	v_add_f32_e32 v84, v84, v85
	v_add_f32_e32 v83, v83, v84
	v_mov_b32_e32 v84, v82
	v_mov_b32_e32 v85, v83
	s_nop 0
	v_permlane16_swap_b32_e32 v82, v84
	v_permlane16_swap_b32_e32 v83, v85
	v_add_f32_e32 v82, v82, v84
	v_add_f32_e32 v83, v83, v85
	v_mov_b32_e32 v84, v82
	v_mov_b32_e32 v85, v83
	s_nop 0
	v_permlane32_swap_b32_e32 v82, v84
	v_permlane32_swap_b32_e32 v83, v85
	s_and_saveexec_b64 s[36:37], s[4:5]
	s_cbranch_execz .LBB0_593
	v_pk_add_f32 v[82:83], v[82:83], v[84:85]
	v_lshlrev_b64 v[84:85], 7, v[134:135]
	v_lshl_add_u64 v[84:85], s[16:17], 0, v[84:85]
	v_lshl_add_u64 v[84:85], s[34:35], 3, v[84:85]
	global_store_dwordx2 v[84:85], v[82:83], off nt
.LBB0_593:
	s_or_b64 exec, exec, s[36:37]
	s_waitcnt vmcnt(11)
	v_pk_mul_f32 v[20:21], v[20:21], s[24:25] op_sel_hi:[1,0]
	v_pk_mul_f32 v[82:83], v[18:19], s[24:25] op_sel_hi:[1,0]
	v_pk_fma_f32 v[18:19], v[72:73], s[26:27], v[20:21] op_sel_hi:[1,0,1]
	v_pk_fma_f32 v[20:21], v[70:71], s[26:27], v[82:83] op_sel_hi:[1,0,1]
	s_waitcnt vmcnt(10)
	v_pk_mul_f32 v[16:17], v[16:17], s[24:25] op_sel_hi:[1,0]
	v_pk_mul_f32 v[70:71], v[14:15], s[24:25] op_sel_hi:[1,0]
	v_pk_fma_f32 v[14:15], v[68:69], s[26:27], v[16:17] op_sel_hi:[1,0,1]
	v_pk_fma_f32 v[16:17], v[66:67], s[26:27], v[70:71] op_sel_hi:[1,0,1]
	s_waitcnt vmcnt(9)
	v_pk_mul_f32 v[12:13], v[12:13], s[24:25] op_sel_hi:[1,0]
	v_pk_mul_f32 v[66:67], v[10:11], s[24:25] op_sel_hi:[1,0]
	v_pk_fma_f32 v[10:11], v[80:81], s[26:27], v[12:13] op_sel_hi:[1,0,1]
	v_pk_fma_f32 v[12:13], v[78:79], s[26:27], v[66:67] op_sel_hi:[1,0,1]
	s_waitcnt vmcnt(8)
	v_pk_mul_f32 v[8:9], v[8:9], s[24:25] op_sel_hi:[1,0]
	v_pk_mul_f32 v[66:67], v[6:7], s[24:25] op_sel_hi:[1,0]
	v_pk_fma_f32 v[6:7], v[76:77], s[26:27], v[8:9] op_sel_hi:[1,0,1]
	v_pk_fma_f32 v[8:9], v[74:75], s[26:27], v[66:67] op_sel_hi:[1,0,1]
	v_add_f32_e32 v66, v20, v21
	v_add_f32_e32 v67, v18, v19
	v_add_f32_e32 v66, v66, v67
	v_mul_f32_e32 v67, v21, v21
	v_mul_f32_e32 v68, v19, v19
	v_fmac_f32_e32 v67, v20, v20
	v_fmac_f32_e32 v68, v18, v18
	v_add_f32_e32 v67, v67, v68
	v_add_f32_e32 v68, v16, v17
	v_add_f32_e32 v69, v14, v15
	v_add_f32_e32 v66, 0, v66
	v_add_f32_e32 v68, v68, v69
	v_add_f32_e32 v66, v66, v68
	v_mul_f32_e32 v68, v17, v17
	v_mul_f32_e32 v69, v15, v15
	v_fmac_f32_e32 v68, v16, v16
	v_fmac_f32_e32 v69, v14, v14
	v_add_f32_e32 v68, v68, v69
	v_add_f32_e32 v67, v67, v68
	v_add_f32_e32 v68, v12, v13
	v_add_f32_e32 v69, v10, v11
	v_add_f32_e32 v68, v68, v69
	v_add_f32_e32 v66, v66, v68
	v_mul_f32_e32 v68, v13, v13
	v_mul_f32_e32 v69, v11, v11
	v_fmac_f32_e32 v68, v12, v12
	v_fmac_f32_e32 v69, v10, v10
	v_add_f32_e32 v68, v68, v69
	v_add_f32_e32 v67, v67, v68
	v_add_f32_e32 v68, v8, v9
	v_add_f32_e32 v69, v6, v7
	v_add_f32_e32 v68, v68, v69
	v_add_f32_e32 v66, v66, v68
	v_mul_f32_e32 v68, v9, v9
	v_mul_f32_e32 v69, v7, v7
	v_fmac_f32_e32 v68, v8, v8
	v_fmac_f32_e32 v69, v6, v6
	v_add_f32_e32 v68, v68, v69
	v_add_f32_e32 v67, v67, v68
	v_mov_b32_e32 v68, v66
	v_mov_b32_e32 v69, v67
	s_nop 0
	v_permlane16_swap_b32_e32 v66, v68
	v_permlane16_swap_b32_e32 v67, v69
	v_add_f32_e32 v66, v66, v68
	v_add_f32_e32 v67, v67, v69
	v_mov_b32_e32 v68, v66
	v_mov_b32_e32 v69, v67
	s_nop 0
	v_permlane32_swap_b32_e32 v66, v68
	v_permlane32_swap_b32_e32 v67, v69
	s_and_saveexec_b64 s[36:37], s[4:5]
	s_cbranch_execz .LBB0_595
	v_pk_add_f32 v[66:67], v[66:67], v[68:69]
	v_lshlrev_b64 v[68:69], 7, v[130:131]
	v_lshl_add_u64 v[68:69], s[16:17], 0, v[68:69]
	v_lshl_add_u64 v[68:69], s[34:35], 3, v[68:69]
	global_store_dwordx2 v[68:69], v[66:67], off nt
.LBB0_595:
	s_or_b64 exec, exec, s[36:37]
	v_lshlrev_b64 v[66:67], 11, v[138:139]
	v_lshl_add_u64 v[70:71], v[132:133], 0, v[66:67]
	v_cvt_pk_bf16_f32 v66, v22, v23
	v_cvt_pk_bf16_f32 v69, v24, v25
	v_cvt_pk_bf16_f32 v22, v42, v43
	v_cvt_pk_bf16_f32 v24, v60, v61
	v_cvt_pk_bf16_f32 v23, v4, v5
	v_cvt_pk_bf16_f32 v25, v44, v45
	v_cvt_pk_bf16_f32 v67, v2, v3
	v_permlane16_swap_b32_e32 v22, v24
	v_permlane16_swap_b32_e32 v23, v25
	v_lshlrev_b64 v[2:3], 11, v[136:137]
	global_store_dwordx4 v[70:71], v[22:25], off offset:64 nt
	v_cvt_pk_bf16_f32 v4, v56, v57
	v_cvt_pk_bf16_f32 v5, v54, v55
	v_lshl_add_u64 v[22:23], v[132:133], 0, v[2:3]
	v_cvt_pk_bf16_f32 v2, v64, v65
	v_cvt_pk_bf16_f32 v3, v62, v63
	s_nop 0
	v_permlane16_swap_b32_e32 v2, v4
	v_permlane16_swap_b32_e32 v3, v5
	global_store_dwordx4 v[22:23], v[2:5], off nt
	v_cvt_pk_bf16_f32 v68, v58, v59
	s_nop 1
	v_permlane16_swap_b32_e32 v66, v68
	v_cvt_pk_bf16_f32 v2, v52, v53
	v_cvt_pk_bf16_f32 v4, v48, v49
	v_cvt_pk_bf16_f32 v3, v50, v51
	v_cvt_pk_bf16_f32 v5, v46, v47
	v_permlane16_swap_b32_e32 v2, v4
	s_nop 0
	v_permlane16_swap_b32_e32 v3, v5
	global_store_dwordx4 v[22:23], v[2:5], off offset:64 nt
	v_permlane16_swap_b32_e32 v67, v69
	s_nop 0
	v_lshlrev_b64 v[2:3], 11, v[134:135]
	v_lshl_add_u64 v[22:23], v[132:133], 0, v[2:3]
	v_cvt_pk_bf16_f32 v2, v40, v41
	v_cvt_pk_bf16_f32 v4, v36, v37
	v_cvt_pk_bf16_f32 v3, v38, v39
	v_cvt_pk_bf16_f32 v5, v34, v35
	v_permlane16_swap_b32_e32 v2, v4
	s_nop 0
	v_permlane16_swap_b32_e32 v3, v5
	global_store_dwordx4 v[22:23], v[2:5], off nt
	s_and_b64 vcc, exec, s[6:7]
	s_mov_b64 s[6:7], -1
	v_cvt_pk_bf16_f32 v2, v32, v33
	v_cvt_pk_bf16_f32 v4, v28, v29
	v_cvt_pk_bf16_f32 v3, v30, v31
	v_cvt_pk_bf16_f32 v5, v26, v27
	v_permlane16_swap_b32_e32 v2, v4
	s_nop 0
	v_permlane16_swap_b32_e32 v3, v5
	global_store_dwordx4 v[22:23], v[2:5], off offset:64 nt
	global_store_dwordx4 v[70:71], v[66:69], off nt
	s_nop 0
	v_lshlrev_b64 v[2:3], 11, v[130:131]
	v_lshl_add_u64 v[22:23], v[132:133], 0, v[2:3]
	v_cvt_pk_bf16_f32 v2, v20, v21
	v_cvt_pk_bf16_f32 v4, v16, v17
	v_cvt_pk_bf16_f32 v3, v18, v19
	v_cvt_pk_bf16_f32 v5, v14, v15
	v_permlane16_swap_b32_e32 v2, v4
	s_nop 0
	v_permlane16_swap_b32_e32 v3, v5
	global_store_dwordx4 v[22:23], v[2:5], off nt
	s_nop 1
	v_cvt_pk_bf16_f32 v2, v12, v13
	v_cvt_pk_bf16_f32 v4, v8, v9
	v_cvt_pk_bf16_f32 v3, v10, v11
	v_cvt_pk_bf16_f32 v5, v6, v7
	v_permlane16_swap_b32_e32 v2, v4
	s_nop 0
	v_permlane16_swap_b32_e32 v3, v5
	global_store_dwordx4 v[22:23], v[2:5], off offset:64 nt
	s_cbranch_vccnz .LBB0_561
	s_andn2_b64 vcc, exec, s[14:15]
	s_cbranch_vccnz .LBB0_560
	s_barrier
	s_branch .LBB0_560

.LBB0_994:
	s_ashr_i32 s36, s34, 3
	s_lshl_b32 s2, s34, 7
	s_ashr_i32 s37, s36, 31
	v_readlane_b32 s80, v239, 7
	s_and_b32 s2, s2, 0x380
	s_lshl_b64 s[36:37], s[36:37], 13
	v_readlane_b32 s86, v239, 13
	v_or_b32_e32 v2, s2, v219
	v_readlane_b32 s87, v239, 14
	s_add_u32 s36, s86, s36
	s_waitcnt vmcnt(0)
	s_addc_u32 s37, s87, s37
	v_lshlrev_b32_e32 v4, 2, v2
	v_mov_b32_e32 v5, v199
	global_load_dwordx4 v[26:29], v4, s[36:37]
	global_load_dwordx4 v[30:33], v4, s[36:37] offset:16
	v_lshl_add_u64 v[4:5], s[36:37], 0, v[4:5]
	s_mov_b64 s[36:37], 0x1000
	s_movk_i32 s2, 0x1000
	v_lshl_add_u64 v[6:7], v[4:5], 0, s[36:37]
	v_add_co_u32_e32 v4, vcc, s2, v4
	v_mov_b32_e32 v8, v186
	s_nop 0
	v_addc_co_u32_e32 v5, vcc, 0, v5, vcc
	global_load_dwordx4 v[34:37], v[4:5], off
	global_load_dwordx4 v[38:41], v[6:7], off offset:16
	v_mov_b32_e32 v6, v190
	v_mov_b32_e32 v14, v178
	v_mov_b32_e32 v24, v183
	v_mov_b32_e32 v20, v192
	v_lshl_add_u32 v4, s96, 8, v218
	v_ashrrev_i32_e32 v5, 31, v4
	v_lshlrev_b64 v[4:5], 10, v[4:5]
	v_mov_b32_e32 v3, v199
	v_mov_b32_e32 v12, v182
	v_mov_b32_e32 v42, v179
	v_mov_b32_e32 v22, v188
	v_lshl_add_u64 v[4:5], s[58:59], 0, v[4:5]
	v_lshl_add_u64 v[2:3], v[4:5], 0, v[2:3]
	v_lshl_add_u64 v[2:3], v[2:3], 0, v[204:205]
	s_mov_b32 s2, 0x8000
	v_readlane_b32 s81, v239, 8
	v_readlane_b32 s82, v239, 9
	v_readlane_b32 s83, v239, 10
	v_readlane_b32 s84, v239, 11
	v_readlane_b32 s85, v239, 12
	v_readlane_b32 s88, v239, 15
	v_readlane_b32 s89, v239, 16
	v_readlane_b32 s90, v239, 17
	v_readlane_b32 s91, v239, 18
	v_readlane_b32 s92, v239, 19
	v_readlane_b32 s93, v239, 20
	v_readlane_b32 s94, v239, 21
	v_readlane_b32 s95, v239, 22
	s_waitcnt vmcnt(0)
	v_mov_b32_e32 v7, v26
	v_mov_b32_e32 v9, v30
	v_pk_mul_f32 v[16:17], v[8:9], s[24:25]
	v_mov_b32_e32 v26, v191
	v_sub_f32_e32 v16, v16, v17
	v_mov_b32_e32 v21, v28
	v_pk_mul_f32 v[10:11], v[26:27], s[24:25]
	v_max_f32_e32 v16, 0xc1898193, v16
	v_pk_mul_f32 v[18:19], v[6:7], s[24:25]
	v_pk_mul_f32 v[6:7], v[20:21], s[24:25]
	v_add_f32_e32 v25, 1.0, v35
	v_add_f32_e32 v15, 1.0, v38
	v_sub_f32_e32 v10, v10, v11
	v_pk_mul_f32 v[20:21], v[14:15], s[26:27]
	v_pk_mul_f32 v[14:15], v[24:25], s[26:27]
	v_exp_f32_e32 v25, v16
	v_max_f32_e32 v10, 0xc1898193, v10
	v_sub_f32_e32 v18, v18, v19
	v_sub_f32_e32 v6, v6, v7
	v_exp_f32_e32 v26, v10
	v_sub_f32_e32 v14, v14, v15
	v_max_f32_e32 v18, 0xc1898193, v18
	v_max_f32_e32 v6, 0xc1898193, v6
	v_med3_f32 v14, v14, s71, v223
	v_mov_b32_e32 v30, v187
	v_mov_b32_e32 v23, v32
	v_add_f32_e32 v13, 1.0, v34
	v_add_f32_e32 v43, 1.0, v39
	v_exp_f32_e32 v24, v18
	v_sub_f32_e32 v20, v20, v21
	v_exp_f32_e32 v28, v6
	v_mul_f32_e32 v10, v10, v14
	v_add_f32_e32 v14, 1.0, v25
	v_pk_mul_f32 v[8:9], v[30:31], s[24:25]
	v_pk_mul_f32 v[4:5], v[22:23], s[24:25]
	v_pk_mul_f32 v[22:23], v[12:13], s[26:27]
	v_pk_mul_f32 v[12:13], v[42:43], s[26:27]
	v_med3_f32 v20, v20, s71, v223
	v_rcp_f32_e32 v14, v14
	v_sub_f32_e32 v8, v8, v9
	v_sub_f32_e32 v12, v12, v13
	v_mul_f32_e32 v16, v16, v20
	v_add_f32_e32 v20, 1.0, v26
	v_max_f32_e32 v8, 0xc1898193, v8
	v_med3_f32 v12, v12, s71, v223
	v_rcp_f32_e32 v20, v20
	v_exp_f32_e32 v27, v8
	v_mul_f32_e32 v8, v8, v12
	v_add_f32_e32 v12, 1.0, v24
	v_add_f32_e32 v24, 1.0, v28
	v_mul_f32_e32 v14, v14, v16
	v_rcp_f32_e32 v16, v24
	v_add_f32_e32 v25, 1.0, v36
	v_mov_b32_e32 v24, v184
	v_sub_f32_e32 v22, v22, v23
	v_pk_mul_f32 v[24:25], v[24:25], s[26:27]
	v_sub_f32_e32 v4, v4, v5
	v_med3_f32 v22, v22, s71, v223
	v_mul_f32_e32 v10, v20, v10
	v_sub_f32_e32 v20, v24, v25
	v_max_f32_e32 v4, 0xc1898193, v4
	v_mul_f32_e32 v18, v18, v22
	v_add_f32_e32 v22, 1.0, v27
	v_med3_f32 v20, v20, s71, v223
	v_add_f32_e32 v27, 1.0, v40
	v_mov_b32_e32 v26, v180
	v_exp_f32_e32 v30, v4
	v_rcp_f32_e32 v12, v12
	v_mul_f32_e32 v6, v6, v20
	v_pk_mul_f32 v[26:27], v[26:27], s[26:27]
	v_rcp_f32_e32 v22, v22
	v_mul_f32_e32 v6, v16, v6
	v_sub_f32_e32 v16, v26, v27
	v_mov_b32_e32 v28, v193
	v_med3_f32 v16, v16, s71, v223
	v_pk_mul_f32 v[28:29], v[28:29], s[24:25]
	v_mul_f32_e32 v4, v4, v16
	v_sub_f32_e32 v16, v28, v29
	v_mov_b32_e32 v32, v189
	v_mul_f32_e32 v12, v12, v18
	v_add_f32_e32 v18, 1.0, v30
	v_max_f32_e32 v16, 0xc1898193, v16
	v_pk_mul_f32 v[30:31], v[32:33], s[24:25]
	v_mul_f32_e32 v8, v22, v8
	v_rcp_f32_e32 v18, v18
	v_sub_f32_e32 v20, v30, v31
	v_exp_f32_e32 v22, v16
	v_max_f32_e32 v20, 0xc1898193, v20
	v_exp_f32_e32 v24, v20
	v_mul_f32_e32 v4, v18, v4
	v_add_f32_e32 v18, 1.0, v22
	v_add_f32_e32 v33, 1.0, v37
	v_mov_b32_e32 v32, v185
	v_rcp_f32_e32 v18, v18
	v_pk_mul_f32 v[32:33], v[32:33], s[26:27]
	v_mov_b32_e32 v36, v199
	v_add_f32_e32 v22, 1.0, v24
	v_sub_f32_e32 v24, v32, v33
	v_cvt_pk_fp8_f32 v36, v12, v10
	v_med3_f32 v24, v24, s71, v223
	v_mul_f32_e32 v16, v16, v24
	v_mul_f32_e32 v16, v18, v16
	v_add_f32_e32 v35, 1.0, v41
	v_mov_b32_e32 v34, v181
	v_cvt_pk_fp8_f32 v36, v6, v16 op_sel:[0,0,1]
	v_fma_f32 v6, v174, s24, -v19
	v_rcp_f32_e32 v22, v22
	v_pk_mul_f32 v[34:35], v[34:35], s[26:27]
	v_mov_b32_e32 v37, v199
	v_max_f32_e32 v6, 0xc1898193, v6
	v_sub_f32_e32 v18, v34, v35
	v_cvt_pk_fp8_f32 v37, v14, v8
	v_exp_f32_e32 v12, v6
	v_med3_f32 v10, v18, s71, v223
	v_mul_f32_e32 v10, v20, v10
	v_mul_f32_e32 v10, v22, v10
	v_cvt_pk_fp8_f32 v37, v4, v10 op_sel:[0,0,1]
	v_add_f32_e32 v4, 1.0, v12
	v_rcp_f32_e32 v4, v4
	v_fma_f32 v8, v170, s24, -v17
	v_fma_f32 v12, v166, s26, -v23
	v_max_f32_e32 v8, 0xc1898193, v8
	v_med3_f32 v12, v12, s71, v223
	v_exp_f32_e32 v14, v8
	v_mul_f32_e32 v6, v6, v12
	v_mul_f32_e32 v4, v4, v6
	v_fma_f32 v6, v162, s26, -v21
	v_med3_f32 v6, v6, s71, v223
	v_mul_f32_e32 v6, v8, v6
	v_fma_f32 v8, v175, s24, -v11
	v_add_f32_e32 v10, 1.0, v14
	v_max_f32_e32 v8, 0xc1898193, v8
	v_rcp_f32_e32 v10, v10
	v_fma_f32 v12, v171, s24, -v9
	v_exp_f32_e32 v14, v8
	v_max_f32_e32 v12, 0xc1898193, v12
	v_exp_f32_e32 v16, v12
	v_mul_f32_e32 v6, v10, v6
	v_add_f32_e32 v10, 1.0, v14
	v_rcp_f32_e32 v10, v10
	v_add_f32_e32 v14, 1.0, v16
	v_fma_f32 v16, v167, s26, -v15
	v_med3_f32 v16, v16, s71, v223
	v_mul_f32_e32 v8, v8, v16
	v_mul_f32_e32 v8, v10, v8
	v_fma_f32 v10, v163, s26, -v13
	v_med3_f32 v10, v10, s71, v223
	v_mul_f32_e32 v10, v12, v10
	v_fma_f32 v12, v176, s24, -v7
	v_max_f32_e32 v12, 0xc1898193, v12
	v_rcp_f32_e32 v14, v14
	v_fma_f32 v16, v172, s24, -v5
	v_exp_f32_e32 v18, v12
	v_max_f32_e32 v16, 0xc1898193, v16
	v_exp_f32_e32 v20, v16
	v_mul_f32_e32 v10, v14, v10
	v_add_f32_e32 v14, 1.0, v18
	v_rcp_f32_e32 v14, v14
	v_add_f32_e32 v18, 1.0, v20
	v_fma_f32 v20, v168, s26, -v25
	v_med3_f32 v20, v20, s71, v223
	v_mul_f32_e32 v12, v12, v20
	v_mul_f32_e32 v12, v14, v12
	v_fma_f32 v14, v164, s26, -v27
	v_med3_f32 v14, v14, s71, v223
	v_mul_f32_e32 v14, v16, v14
	v_fma_f32 v16, v177, s24, -v29
	v_max_f32_e32 v16, 0xc1898193, v16
	v_rcp_f32_e32 v18, v18
	v_fma_f32 v20, v173, s24, -v31
	v_exp_f32_e32 v22, v16
	v_max_f32_e32 v20, 0xc1898193, v20
	v_exp_f32_e32 v24, v20
	v_mul_f32_e32 v14, v18, v14
	v_add_f32_e32 v18, 1.0, v22
	v_rcp_f32_e32 v18, v18
	v_add_f32_e32 v22, 1.0, v24
	v_fma_f32 v24, v169, s26, -v33
	v_med3_f32 v24, v24, s71, v223
	v_rcp_f32_e32 v22, v22
	v_mul_f32_e32 v16, v16, v24
	v_mov_b32_e32 v39, v199
	v_mul_f32_e32 v16, v18, v16
	v_fma_f32 v18, v165, s26, -v35
	v_cvt_pk_fp8_f32 v39, v6, v10
	v_med3_f32 v18, v18, s71, v223
	v_mov_b32_e32 v38, v199
	v_cvt_pk_fp8_f32 v38, v4, v8
	v_mul_f32_e32 v4, v20, v18
	v_mul_f32_e32 v4, v22, v4
	v_cvt_pk_fp8_f32 v39, v14, v4 op_sel:[0,0,1]
	v_fma_f32 v4, v158, s24, -v19
	v_max_f32_e32 v4, 0xc1898193, v4
	v_exp_f32_e32 v8, v4
	v_cvt_pk_fp8_f32 v38, v12, v16 op_sel:[0,0,1]
	v_fma_f32 v6, v154, s24, -v17
	v_fma_f32 v12, v150, s26, -v23
	v_add_f32_e32 v8, 1.0, v8
	v_rcp_f32_e32 v8, v8
	v_max_f32_e32 v6, 0xc1898193, v6
	v_med3_f32 v12, v12, s71, v223
	v_exp_f32_e32 v10, v6
	v_mul_f32_e32 v4, v4, v12
	v_mul_f32_e32 v4, v8, v4
	v_fma_f32 v8, v146, s26, -v21
	v_med3_f32 v8, v8, s71, v223
	v_mul_f32_e32 v6, v6, v8
	v_fma_f32 v8, v159, s24, -v11
	v_add_f32_e32 v10, 1.0, v10
	v_max_f32_e32 v8, 0xc1898193, v8
	v_rcp_f32_e32 v10, v10
	v_fma_f32 v12, v155, s24, -v9
	v_exp_f32_e32 v14, v8
	v_max_f32_e32 v12, 0xc1898193, v12
	v_exp_f32_e32 v16, v12
	v_mul_f32_e32 v6, v10, v6
	v_add_f32_e32 v10, 1.0, v14
	v_rcp_f32_e32 v10, v10
	v_add_f32_e32 v14, 1.0, v16
	v_fma_f32 v16, v151, s26, -v15
	v_med3_f32 v16, v16, s71, v223
	v_mul_f32_e32 v8, v8, v16
	v_mul_f32_e32 v8, v10, v8
	v_fma_f32 v10, v147, s26, -v13
	v_med3_f32 v10, v10, s71, v223
	v_mul_f32_e32 v10, v12, v10
	v_fma_f32 v12, v160, s24, -v7
	v_max_f32_e32 v12, 0xc1898193, v12
	v_rcp_f32_e32 v14, v14
	v_fma_f32 v16, v156, s24, -v5
	v_exp_f32_e32 v18, v12
	v_max_f32_e32 v16, 0xc1898193, v16
	v_exp_f32_e32 v20, v16
	v_mul_f32_e32 v10, v14, v10
	v_add_f32_e32 v14, 1.0, v18
	v_rcp_f32_e32 v14, v14
	v_add_f32_e32 v18, 1.0, v20
	v_fma_f32 v20, v152, s26, -v25
	v_med3_f32 v20, v20, s71, v223
	v_mul_f32_e32 v12, v12, v20
	v_mul_f32_e32 v12, v14, v12
	v_fma_f32 v14, v148, s26, -v27
	v_med3_f32 v14, v14, s71, v223
	v_mul_f32_e32 v14, v16, v14
	v_fma_f32 v16, v161, s24, -v29
	v_max_f32_e32 v16, 0xc1898193, v16
	v_rcp_f32_e32 v18, v18
	v_fma_f32 v20, v157, s24, -v31
	v_exp_f32_e32 v22, v16
	v_max_f32_e32 v20, 0xc1898193, v20
	v_exp_f32_e32 v24, v20
	v_mul_f32_e32 v14, v18, v14
	v_add_f32_e32 v18, 1.0, v22
	v_permlane16_swap_b32_e32 v36, v38
	v_permlane16_swap_b32_e32 v37, v39
	v_rcp_f32_e32 v18, v18
	global_store_dwordx4 v[2:3], v[36:39], off nt
	v_add_f32_e32 v22, 1.0, v24
	v_fma_f32 v24, v153, s26, -v33
	v_mov_b32_e32 v36, v199
	v_mov_b32_e32 v37, v199
	v_med3_f32 v24, v24, s71, v223
	v_cvt_pk_fp8_f32 v36, v4, v8
	v_cvt_pk_fp8_f32 v37, v6, v10
	v_fma_f32 v6, v142, s24, -v19
	v_rcp_f32_e32 v22, v22
	v_mul_f32_e32 v16, v16, v24
	v_max_f32_e32 v6, 0xc1898193, v6
	v_mul_f32_e32 v16, v18, v16
	v_fma_f32 v18, v149, s26, -v35
	v_fma_f32 v8, v138, s24, -v17
	v_exp_f32_e32 v10, v6
	v_med3_f32 v4, v18, s71, v223
	v_max_f32_e32 v8, 0xc1898193, v8
	v_mul_f32_e32 v4, v20, v4
	v_cvt_pk_fp8_f32 v36, v12, v16 op_sel:[0,0,1]
	v_exp_f32_e32 v12, v8
	v_mul_f32_e32 v4, v22, v4
	v_cvt_pk_fp8_f32 v37, v14, v4 op_sel:[0,0,1]
	v_add_f32_e32 v4, 1.0, v10
	v_rcp_f32_e32 v4, v4
	v_add_f32_e32 v10, 1.0, v12
	v_fma_f32 v12, v134, s26, -v23
	v_med3_f32 v12, v12, s71, v223
	v_mul_f32_e32 v6, v6, v12
	v_mul_f32_e32 v4, v4, v6
	v_fma_f32 v6, v130, s26, -v21
	v_med3_f32 v6, v6, s71, v223
	v_mul_f32_e32 v6, v8, v6
	v_fma_f32 v8, v143, s24, -v11
	v_max_f32_e32 v8, 0xc1898193, v8
	v_rcp_f32_e32 v10, v10
	v_fma_f32 v12, v139, s24, -v9
	v_exp_f32_e32 v14, v8
	v_max_f32_e32 v12, 0xc1898193, v12
	v_exp_f32_e32 v16, v12
	v_mul_f32_e32 v6, v10, v6
	v_add_f32_e32 v10, 1.0, v14
	v_rcp_f32_e32 v10, v10
	v_add_f32_e32 v14, 1.0, v16
	v_fma_f32 v16, v135, s26, -v15
	v_med3_f32 v16, v16, s71, v223
	v_mul_f32_e32 v8, v8, v16
	v_mul_f32_e32 v8, v10, v8
	v_fma_f32 v10, v131, s26, -v13
	v_med3_f32 v10, v10, s71, v223
	v_mul_f32_e32 v10, v12, v10
	v_fma_f32 v12, v144, s24, -v7
	v_max_f32_e32 v12, 0xc1898193, v12
	v_rcp_f32_e32 v14, v14
	v_fma_f32 v16, v140, s24, -v5
	v_exp_f32_e32 v18, v12
	v_max_f32_e32 v16, 0xc1898193, v16
	v_exp_f32_e32 v20, v16
	v_mul_f32_e32 v10, v14, v10
	v_add_f32_e32 v14, 1.0, v18
	v_rcp_f32_e32 v14, v14
	v_add_f32_e32 v18, 1.0, v20
	v_fma_f32 v20, v136, s26, -v25
	v_med3_f32 v20, v20, s71, v223
	v_mul_f32_e32 v12, v12, v20
	v_mul_f32_e32 v12, v14, v12
	v_fma_f32 v14, v132, s26, -v27
	v_med3_f32 v14, v14, s71, v223
	v_mul_f32_e32 v14, v16, v14
	v_fma_f32 v16, v145, s24, -v29
	v_max_f32_e32 v16, 0xc1898193, v16
	v_rcp_f32_e32 v18, v18
	v_fma_f32 v20, v141, s24, -v31
	v_exp_f32_e32 v22, v16
	v_max_f32_e32 v20, 0xc1898193, v20
	v_exp_f32_e32 v24, v20
	v_mul_f32_e32 v14, v18, v14
	v_add_f32_e32 v18, 1.0, v22
	v_rcp_f32_e32 v18, v18
	v_add_f32_e32 v22, 1.0, v24
	v_fma_f32 v24, v137, s26, -v33
	v_med3_f32 v24, v24, s71, v223
	v_rcp_f32_e32 v22, v22
	v_mul_f32_e32 v16, v16, v24
	v_mov_b32_e32 v39, v199
	v_mul_f32_e32 v16, v18, v16
	v_fma_f32 v18, v133, s26, -v35
	v_cvt_pk_fp8_f32 v39, v6, v10
	v_med3_f32 v18, v18, s71, v223
	v_mov_b32_e32 v38, v199
	v_cvt_pk_fp8_f32 v38, v4, v8
	v_mul_f32_e32 v4, v20, v18
	v_mul_f32_e32 v4, v22, v4
	v_cvt_pk_fp8_f32 v39, v14, v4 op_sel:[0,0,1]
	v_fma_f32 v4, v126, s24, -v19
	v_max_f32_e32 v4, 0xc1898193, v4
	v_exp_f32_e32 v8, v4
	v_cvt_pk_fp8_f32 v38, v12, v16 op_sel:[0,0,1]
	v_fma_f32 v6, v122, s24, -v17
	v_fma_f32 v12, v118, s26, -v23
	v_add_f32_e32 v8, 1.0, v8
	v_rcp_f32_e32 v8, v8
	v_max_f32_e32 v6, 0xc1898193, v6
	v_med3_f32 v12, v12, s71, v223
	v_exp_f32_e32 v10, v6
	v_mul_f32_e32 v4, v4, v12
	v_mul_f32_e32 v4, v8, v4
	v_fma_f32 v8, v114, s26, -v21
	v_med3_f32 v8, v8, s71, v223
	v_mul_f32_e32 v6, v6, v8
	v_fma_f32 v8, v127, s24, -v11
	v_add_f32_e32 v10, 1.0, v10
	v_max_f32_e32 v8, 0xc1898193, v8
	v_rcp_f32_e32 v10, v10
	v_fma_f32 v12, v123, s24, -v9
	v_exp_f32_e32 v14, v8
	v_max_f32_e32 v12, 0xc1898193, v12
	v_exp_f32_e32 v16, v12
	v_mul_f32_e32 v6, v10, v6
	v_add_f32_e32 v10, 1.0, v14
	v_rcp_f32_e32 v10, v10
	v_add_f32_e32 v14, 1.0, v16
	v_fma_f32 v16, v119, s26, -v15
	v_med3_f32 v16, v16, s71, v223
	v_mul_f32_e32 v8, v8, v16
	v_mul_f32_e32 v8, v10, v8
	v_fma_f32 v10, v115, s26, -v13
	v_med3_f32 v10, v10, s71, v223
	v_mul_f32_e32 v10, v12, v10
	v_fma_f32 v12, v128, s24, -v7
	v_max_f32_e32 v12, 0xc1898193, v12
	v_rcp_f32_e32 v14, v14
	v_fma_f32 v16, v124, s24, -v5
	v_exp_f32_e32 v18, v12
	v_max_f32_e32 v16, 0xc1898193, v16
	v_exp_f32_e32 v20, v16
	v_mul_f32_e32 v10, v14, v10
	v_add_f32_e32 v14, 1.0, v18
	v_rcp_f32_e32 v14, v14
	v_add_f32_e32 v18, 1.0, v20
	v_fma_f32 v20, v120, s26, -v25
	v_med3_f32 v20, v20, s71, v223
	v_mul_f32_e32 v12, v12, v20
	v_mul_f32_e32 v12, v14, v12
	v_fma_f32 v14, v116, s26, -v27
	v_med3_f32 v14, v14, s71, v223
	v_mul_f32_e32 v14, v16, v14
	v_fma_f32 v16, v129, s24, -v29
	v_max_f32_e32 v16, 0xc1898193, v16
	v_rcp_f32_e32 v18, v18
	v_fma_f32 v20, v125, s24, -v31
	v_exp_f32_e32 v22, v16
	v_max_f32_e32 v20, 0xc1898193, v20
	v_exp_f32_e32 v24, v20
	v_add_co_u32_e32 v40, vcc, s2, v2
	v_mul_f32_e32 v14, v18, v14
	v_add_f32_e32 v18, 1.0, v22
	v_permlane16_swap_b32_e32 v36, v38
	v_permlane16_swap_b32_e32 v37, v39
	v_addc_co_u32_e32 v41, vcc, 0, v3, vcc
	v_rcp_f32_e32 v18, v18
	global_store_dwordx4 v[40:41], v[36:39], off nt
	v_add_f32_e32 v22, 1.0, v24
	v_fma_f32 v24, v121, s26, -v33
	v_mov_b32_e32 v36, v199
	v_mov_b32_e32 v37, v199
	v_med3_f32 v24, v24, s71, v223
	v_cvt_pk_fp8_f32 v36, v4, v8
	v_cvt_pk_fp8_f32 v37, v6, v10
	v_fma_f32 v6, v110, s24, -v19
	v_rcp_f32_e32 v22, v22
	v_mul_f32_e32 v16, v16, v24
	v_max_f32_e32 v6, 0xc1898193, v6
	v_mul_f32_e32 v16, v18, v16
	v_fma_f32 v18, v117, s26, -v35
	v_fma_f32 v8, v106, s24, -v17
	v_exp_f32_e32 v10, v6
	v_med3_f32 v4, v18, s71, v223
	v_max_f32_e32 v8, 0xc1898193, v8
	v_mul_f32_e32 v4, v20, v4
	v_cvt_pk_fp8_f32 v36, v12, v16 op_sel:[0,0,1]
	v_exp_f32_e32 v12, v8
	v_mul_f32_e32 v4, v22, v4
	v_cvt_pk_fp8_f32 v37, v14, v4 op_sel:[0,0,1]
	v_add_f32_e32 v4, 1.0, v10
	v_rcp_f32_e32 v4, v4
	v_add_f32_e32 v10, 1.0, v12
	v_fma_f32 v12, v102, s26, -v23
	v_med3_f32 v12, v12, s71, v223
	v_mul_f32_e32 v6, v6, v12
	v_mul_f32_e32 v4, v4, v6
	v_fma_f32 v6, v90, s26, -v21
	v_med3_f32 v6, v6, s71, v223
	v_mul_f32_e32 v6, v8, v6
	v_fma_f32 v8, v111, s24, -v11
	v_max_f32_e32 v8, 0xc1898193, v8
	v_rcp_f32_e32 v10, v10
	v_fma_f32 v12, v107, s24, -v9
	v_exp_f32_e32 v14, v8
	v_max_f32_e32 v12, 0xc1898193, v12
	v_exp_f32_e32 v16, v12
	v_mul_f32_e32 v6, v10, v6
	v_add_f32_e32 v10, 1.0, v14
	v_rcp_f32_e32 v10, v10
	v_add_f32_e32 v14, 1.0, v16
	v_fma_f32 v16, v103, s26, -v15
	v_med3_f32 v16, v16, s71, v223
	v_mul_f32_e32 v8, v8, v16
	v_mul_f32_e32 v8, v10, v8
	v_fma_f32 v10, v91, s26, -v13
	v_med3_f32 v10, v10, s71, v223
	v_mul_f32_e32 v10, v12, v10
	v_fma_f32 v12, v112, s24, -v7
	v_max_f32_e32 v12, 0xc1898193, v12
	v_rcp_f32_e32 v14, v14
	v_fma_f32 v16, v108, s24, -v5
	v_exp_f32_e32 v18, v12
	v_max_f32_e32 v16, 0xc1898193, v16
	v_exp_f32_e32 v20, v16
	v_mul_f32_e32 v10, v14, v10
	v_add_f32_e32 v14, 1.0, v18
	v_rcp_f32_e32 v14, v14
	v_add_f32_e32 v18, 1.0, v20
	v_fma_f32 v20, v104, s26, -v25
	v_med3_f32 v20, v20, s71, v223
	v_mul_f32_e32 v12, v12, v20
	v_mul_f32_e32 v12, v14, v12
	v_fma_f32 v14, v92, s26, -v27
	v_med3_f32 v14, v14, s71, v223
	v_mul_f32_e32 v14, v16, v14
	v_fma_f32 v16, v113, s24, -v29
	v_max_f32_e32 v16, 0xc1898193, v16
	v_rcp_f32_e32 v18, v18
	v_fma_f32 v20, v109, s24, -v31
	v_exp_f32_e32 v22, v16
	v_max_f32_e32 v20, 0xc1898193, v20
	v_exp_f32_e32 v24, v20
	v_mul_f32_e32 v14, v18, v14
	v_add_f32_e32 v18, 1.0, v22
	v_rcp_f32_e32 v18, v18
	v_add_f32_e32 v22, 1.0, v24
	v_fma_f32 v24, v105, s26, -v33
	v_med3_f32 v24, v24, s71, v223
	v_rcp_f32_e32 v22, v22
	v_mul_f32_e32 v16, v16, v24
	v_mov_b32_e32 v39, v199
	v_mul_f32_e32 v16, v18, v16
	v_fma_f32 v18, v93, s26, -v35
	v_cvt_pk_fp8_f32 v39, v6, v10
	v_med3_f32 v18, v18, s71, v223
	v_mov_b32_e32 v38, v199
	v_cvt_pk_fp8_f32 v38, v4, v8
	v_mul_f32_e32 v4, v20, v18
	v_mul_f32_e32 v4, v22, v4
	v_cvt_pk_fp8_f32 v39, v14, v4 op_sel:[0,0,1]
	v_fma_f32 v4, v86, s24, -v19
	v_max_f32_e32 v4, 0xc1898193, v4
	v_exp_f32_e32 v8, v4
	v_cvt_pk_fp8_f32 v38, v12, v16 op_sel:[0,0,1]
	v_fma_f32 v6, v82, s24, -v17
	v_fma_f32 v12, v94, s26, -v23
	v_add_f32_e32 v8, 1.0, v8
	v_rcp_f32_e32 v8, v8
	v_max_f32_e32 v6, 0xc1898193, v6
	v_med3_f32 v12, v12, s71, v223
	v_exp_f32_e32 v10, v6
	v_mul_f32_e32 v4, v4, v12
	v_mul_f32_e32 v4, v8, v4
	v_fma_f32 v8, v98, s26, -v21
	v_med3_f32 v8, v8, s71, v223
	v_mul_f32_e32 v6, v6, v8
	v_fma_f32 v8, v87, s24, -v11
	v_add_f32_e32 v10, 1.0, v10
	v_max_f32_e32 v8, 0xc1898193, v8
	v_rcp_f32_e32 v10, v10
	v_fma_f32 v12, v83, s24, -v9
	v_exp_f32_e32 v14, v8
	v_max_f32_e32 v12, 0xc1898193, v12
	v_exp_f32_e32 v16, v12
	v_mul_f32_e32 v6, v10, v6
	v_add_f32_e32 v10, 1.0, v14
	v_rcp_f32_e32 v10, v10
	v_add_f32_e32 v14, 1.0, v16
	v_fma_f32 v16, v95, s26, -v15
	v_med3_f32 v16, v16, s71, v223
	v_mul_f32_e32 v8, v8, v16
	v_mul_f32_e32 v8, v10, v8
	v_fma_f32 v10, v99, s26, -v13
	v_med3_f32 v10, v10, s71, v223
	v_mul_f32_e32 v10, v12, v10
	v_fma_f32 v12, v88, s24, -v7
	v_max_f32_e32 v12, 0xc1898193, v12
	v_rcp_f32_e32 v14, v14
	v_fma_f32 v16, v84, s24, -v5
	v_exp_f32_e32 v18, v12
	v_max_f32_e32 v16, 0xc1898193, v16
	v_exp_f32_e32 v20, v16
	v_mul_f32_e32 v10, v14, v10
	v_add_f32_e32 v14, 1.0, v18
	v_rcp_f32_e32 v14, v14
	v_add_f32_e32 v18, 1.0, v20
	v_fma_f32 v20, v96, s26, -v25
	v_med3_f32 v20, v20, s71, v223
	v_mul_f32_e32 v12, v12, v20
	v_mul_f32_e32 v12, v14, v12
	v_fma_f32 v14, v100, s26, -v27
	v_med3_f32 v14, v14, s71, v223
	v_mul_f32_e32 v14, v16, v14
	v_fma_f32 v16, v89, s24, -v29
	v_max_f32_e32 v16, 0xc1898193, v16
	v_rcp_f32_e32 v18, v18
	v_fma_f32 v20, v85, s24, -v31
	v_exp_f32_e32 v22, v16
	v_max_f32_e32 v20, 0xc1898193, v20
	v_exp_f32_e32 v24, v20
	s_mov_b32 s2, 0x20000
	v_add_co_u32_e32 v40, vcc, s2, v2
	v_mul_f32_e32 v14, v18, v14
	v_add_f32_e32 v18, 1.0, v22
	v_permlane16_swap_b32_e32 v36, v38
	v_permlane16_swap_b32_e32 v37, v39
	v_addc_co_u32_e32 v41, vcc, 0, v3, vcc
	v_rcp_f32_e32 v18, v18
	global_store_dwordx4 v[40:41], v[36:39], off nt
	v_add_f32_e32 v22, 1.0, v24
	v_fma_f32 v24, v97, s26, -v33
	v_mov_b32_e32 v36, v199
	v_mov_b32_e32 v37, v199
	v_med3_f32 v24, v24, s71, v223
	v_cvt_pk_fp8_f32 v36, v4, v8
	v_cvt_pk_fp8_f32 v37, v6, v10
	v_fma_f32 v6, v70, s24, -v19
	v_rcp_f32_e32 v22, v22
	v_mul_f32_e32 v16, v16, v24
	v_max_f32_e32 v6, 0xc1898193, v6
	v_mul_f32_e32 v16, v18, v16
	v_fma_f32 v18, v101, s26, -v35
	v_fma_f32 v8, v66, s24, -v17
	v_exp_f32_e32 v10, v6
	v_med3_f32 v4, v18, s71, v223
	v_max_f32_e32 v8, 0xc1898193, v8
	v_mul_f32_e32 v4, v20, v4
	v_cvt_pk_fp8_f32 v36, v12, v16 op_sel:[0,0,1]
	v_exp_f32_e32 v12, v8
	v_mul_f32_e32 v4, v22, v4
	v_cvt_pk_fp8_f32 v37, v14, v4 op_sel:[0,0,1]
	v_add_f32_e32 v4, 1.0, v10
	v_rcp_f32_e32 v4, v4
	v_add_f32_e32 v10, 1.0, v12
	v_fma_f32 v12, v74, s26, -v23
	v_med3_f32 v12, v12, s71, v223
	v_mul_f32_e32 v6, v6, v12
	v_mul_f32_e32 v4, v4, v6
	v_fma_f32 v6, v78, s26, -v21
	v_med3_f32 v6, v6, s71, v223
	v_mul_f32_e32 v6, v8, v6
	v_fma_f32 v8, v71, s24, -v11
	v_max_f32_e32 v8, 0xc1898193, v8
	v_rcp_f32_e32 v10, v10
	v_fma_f32 v9, v67, s24, -v9
	v_exp_f32_e32 v11, v8
	v_max_f32_e32 v9, 0xc1898193, v9
	v_exp_f32_e32 v12, v9
	v_mul_f32_e32 v6, v10, v6
	v_add_f32_e32 v10, 1.0, v11
	v_rcp_f32_e32 v10, v10
	v_add_f32_e32 v11, 1.0, v12
	v_fma_f32 v12, v75, s26, -v15
	v_med3_f32 v12, v12, s71, v223
	v_mul_f32_e32 v8, v8, v12
	v_mul_f32_e32 v8, v10, v8
	v_fma_f32 v10, v79, s26, -v13
	v_fma_f32 v7, v72, s24, -v7
	v_med3_f32 v10, v10, s71, v223
	v_max_f32_e32 v7, 0xc1898193, v7
	v_mul_f32_e32 v9, v9, v10
	v_fma_f32 v5, v68, s24, -v5
	v_exp_f32_e32 v10, v7
	v_max_f32_e32 v5, 0xc1898193, v5
	v_rcp_f32_e32 v11, v11
	v_exp_f32_e32 v12, v5
	v_add_f32_e32 v10, 1.0, v10
	v_rcp_f32_e32 v10, v10
	v_mul_f32_e32 v9, v11, v9
	v_add_f32_e32 v11, 1.0, v12
	v_fma_f32 v12, v76, s26, -v25
	v_med3_f32 v12, v12, s71, v223
	v_mul_f32_e32 v7, v7, v12
	v_mul_f32_e32 v7, v10, v7
	v_fma_f32 v10, v80, s26, -v27
	v_med3_f32 v10, v10, s71, v223
	v_mul_f32_e32 v5, v5, v10
	v_fma_f32 v10, v73, s24, -v29
	v_max_f32_e32 v10, 0xc1898193, v10
	v_rcp_f32_e32 v11, v11
	v_fma_f32 v12, v69, s24, -v31
	v_exp_f32_e32 v13, v10
	v_max_f32_e32 v12, 0xc1898193, v12
	v_exp_f32_e32 v14, v12
	v_mul_f32_e32 v5, v11, v5
	v_add_f32_e32 v11, 1.0, v13
	v_rcp_f32_e32 v11, v11
	v_add_f32_e32 v13, 1.0, v14
	v_fma_f32 v14, v77, s26, -v33
	v_med3_f32 v14, v14, s71, v223
	v_rcp_f32_e32 v13, v13
	v_mul_f32_e32 v10, v10, v14
	v_mov_b32_e32 v38, v199
	v_mov_b32_e32 v39, v199
	v_mul_f32_e32 v10, v11, v10
	v_fma_f32 v11, v81, s26, -v35
	v_cvt_pk_fp8_f32 v38, v4, v8
	v_cvt_pk_fp8_f32 v39, v6, v9
	v_med3_f32 v11, v11, s71, v223
	v_mul_f32_e32 v4, v12, v11
	v_mul_f32_e32 v4, v13, v4
	v_cvt_pk_fp8_f32 v38, v7, v10 op_sel:[0,0,1]
	v_cvt_pk_fp8_f32 v39, v5, v4 op_sel:[0,0,1]
	v_add_co_u32_e32 v2, vcc, 0x28000, v2
	v_permlane16_swap_b32_e32 v36, v38
	s_nop 0
	v_addc_co_u32_e32 v3, vcc, 0, v3, vcc
	v_permlane16_swap_b32_e32 v37, v39
	s_and_b64 vcc, exec, s[4:5]
	s_mov_b64 s[4:5], -1
	global_store_dwordx4 v[2:3], v[36:39], off nt
	s_cbranch_vccnz .LBB0_975
	s_andn2_b64 vcc, exec, s[16:17]
	s_cbranch_vccnz .LBB0_974
	s_barrier
	s_branch .LBB0_974

.LBB0_1090:
	v_lshl_add_u32 v2, s27, 8, v215
	v_ashrrev_i32_e32 v3, 31, v2
	s_ashr_i32 s0, s84, 2
	s_lshl_b32 s1, s84, 8
	v_lshl_add_u64 v[4:5], v[2:3], 2, s[92:93]
	v_add_u32_e32 v6, 0x80, v2
	v_add_u32_e32 v8, 0x90, v2
	v_add_u32_e32 v10, 0xa0, v2
	v_add_u32_e32 v2, 0xb0, v2
	s_and_b32 s84, s1, 0x300
	v_ashrrev_i32_e32 v3, 31, v2
	s_ashr_i32 s1, s0, 31
	v_readlane_b32 s40, v239, 7
	s_waitcnt vmcnt(0)
	v_ashrrev_i32_e32 v7, 31, v6
	v_ashrrev_i32_e32 v9, 31, v8
	v_ashrrev_i32_e32 v11, 31, v10
	v_lshl_add_u64 v[2:3], v[2:3], 2, s[92:93]
	s_lshl_b64 s[0:1], s[0:1], 12
	v_readlane_b32 s50, v239, 17
	v_lshl_add_u64 v[6:7], v[6:7], 2, s[92:93]
	v_lshl_add_u64 v[8:9], v[8:9], 2, s[92:93]
	v_lshl_add_u64 v[10:11], v[10:11], 2, s[92:93]
	global_load_dword v34, v[4:5], off
	global_load_dword v36, v[4:5], off offset:64
	global_load_dword v38, v[4:5], off offset:128
	global_load_dword v26, v[4:5], off offset:192
	global_load_dword v24, v[6:7], off
	global_load_dword v22, v[8:9], off
	global_load_dword v20, v[10:11], off
	global_load_dword v18, v[2:3], off
	v_or_b32_e32 v2, s84, v217
	v_readlane_b32 s51, v239, 18
	s_add_u32 s0, s50, s0
	s_addc_u32 s1, s51, s1
	v_lshlrev_b32_e32 v2, 2, v2
	global_load_dwordx4 v[14:17], v2, s[0:1]
	global_load_dwordx4 v[10:13], v2, s[0:1] offset:16
	global_load_dwordx4 v[6:9], v2, s[0:1] offset:128
	s_nop 0
	global_load_dwordx4 v[2:5], v2, s[0:1] offset:144
	v_mov_b32_e32 v28, v199
	v_mov_b32_e32 v29, v199
	v_mov_b32_e32 v30, v199
	v_mov_b32_e32 v31, v199
	v_mov_b32_e32 v32, v199
	v_mov_b32_e32 v33, v199
	v_readlane_b32 s41, v239, 8
	v_readlane_b32 s42, v239, 9
	v_readlane_b32 s43, v239, 10
	v_readlane_b32 s44, v239, 11
	v_readlane_b32 s45, v239, 12
	v_readlane_b32 s46, v239, 13
	v_readlane_b32 s47, v239, 14
	v_readlane_b32 s48, v239, 15
	v_readlane_b32 s49, v239, 16
	v_readlane_b32 s52, v239, 19
	v_readlane_b32 s53, v239, 20
	v_readlane_b32 s54, v239, 21
	v_readlane_b32 s55, v239, 22
	s_waitcnt vmcnt(0)
	v_ashrrev_i32_e32 v35, 31, v34
	v_lshlrev_b64 v[40:41], 10, v[34:35]
	v_cmp_lt_i64_e32 vcc, -1, v[34:35]
	v_ashrrev_i32_e32 v37, 31, v36
	v_lshlrev_b64 v[42:43], 10, v[36:37]
	v_cndmask_b32_e32 v35, 0, v41, vcc
	v_cndmask_b32_e32 v34, v221, v40, vcc
	v_cmp_lt_i64_e64 s[0:1], -1, v[36:37]
	v_lshl_add_u64 v[34:35], s[94:95], 0, v[34:35]
	v_lshl_add_u64 v[34:35], v[34:35], 0, s[84:85]
	v_pk_fma_f32 v[40:41], v[190:191], s[8:9], v[14:15] op_sel_hi:[1,0,1]
	v_pk_fma_f32 v[46:47], v[186:187], s[8:9], v[10:11] op_sel_hi:[1,0,1]
	v_pk_fma_f32 v[50:51], v[174:175], s[8:9], v[6:7] op_sel_hi:[1,0,1]
	v_pk_fma_f32 v[54:55], v[170:171], s[8:9], v[2:3] op_sel_hi:[1,0,1]
	v_cvt_pk_fp8_f32 v28, v40, v41
	v_cvt_pk_fp8_f32 v29, v46, v47
	v_cvt_pk_fp8_f32 v30, v50, v51
	v_cvt_pk_fp8_f32 v31, v54, v55
	v_pk_fma_f32 v[36:37], v[192:193], s[8:9], v[16:17] op_sel_hi:[1,0,1]
	v_pk_fma_f32 v[44:45], v[188:189], s[8:9], v[12:13] op_sel_hi:[1,0,1]
	v_pk_fma_f32 v[48:49], v[176:177], s[8:9], v[8:9] op_sel_hi:[1,0,1]
	v_pk_fma_f32 v[52:53], v[172:173], s[8:9], v[4:5] op_sel_hi:[1,0,1]
	v_cvt_pk_fp8_f32 v28, v36, v37 op_sel:[0,0,1]
	v_cvt_pk_fp8_f32 v29, v44, v45 op_sel:[0,0,1]
	v_cvt_pk_fp8_f32 v30, v48, v49 op_sel:[0,0,1]
	v_cvt_pk_fp8_f32 v31, v52, v53 op_sel:[0,0,1]
	v_lshl_add_u64 v[34:35], v[34:35], 0, s[6:7]
	v_lshl_add_u64 v[34:35], v[34:35], 0, v[202:203]
	v_permlane16_swap_b32_e32 v28, v30
	v_permlane16_swap_b32_e32 v29, v31
	v_pk_fma_f32 v[58:59], v[182:183], s[8:9], v[14:15] op_sel_hi:[1,0,1]
	v_pk_fma_f32 v[62:63], v[178:179], s[8:9], v[10:11] op_sel_hi:[1,0,1]
	global_store_dwordx4 v[34:35], v[28:31], off nt
	v_mov_b32_e32 v34, v199
	v_mov_b32_e32 v35, v199
	v_pk_fma_f32 v[28:29], v[166:167], s[8:9], v[6:7] op_sel_hi:[1,0,1]
	v_pk_fma_f32 v[30:31], v[162:163], s[8:9], v[2:3] op_sel_hi:[1,0,1]
	v_cvt_pk_fp8_f32 v32, v58, v59
	v_cvt_pk_fp8_f32 v33, v62, v63
	v_cvt_pk_fp8_f32 v34, v28, v29
	v_cvt_pk_fp8_f32 v35, v30, v31
	v_pk_fma_f32 v[56:57], v[184:185], s[8:9], v[16:17] op_sel_hi:[1,0,1]
	v_pk_fma_f32 v[60:61], v[180:181], s[8:9], v[12:13] op_sel_hi:[1,0,1]
	v_pk_fma_f32 v[28:29], v[168:169], s[8:9], v[8:9] op_sel_hi:[1,0,1]
	v_pk_fma_f32 v[30:31], v[164:165], s[8:9], v[4:5] op_sel_hi:[1,0,1]
	v_cndmask_b32_e64 v43, 0, v43, s[0:1]
	v_cndmask_b32_e64 v42, v221, v42, s[0:1]
	v_cvt_pk_fp8_f32 v32, v56, v57 op_sel:[0,0,1]
	v_cvt_pk_fp8_f32 v33, v60, v61 op_sel:[0,0,1]
	v_cvt_pk_fp8_f32 v34, v28, v29 op_sel:[0,0,1]
	v_cvt_pk_fp8_f32 v35, v30, v31 op_sel:[0,0,1]
	v_lshl_add_u64 v[40:41], s[94:95], 0, v[42:43]
	v_lshl_add_u64 v[40:41], v[40:41], 0, s[84:85]
	v_lshl_add_u64 v[40:41], v[40:41], 0, s[6:7]
	v_ashrrev_i32_e32 v39, 31, v38
	v_lshl_add_u64 v[28:29], v[40:41], 0, v[202:203]
	v_permlane16_swap_b32_e32 v32, v34
	v_permlane16_swap_b32_e32 v33, v35
	global_store_dwordx4 v[28:29], v[32:35], off nt
	v_lshlrev_b64 v[28:29], 10, v[38:39]
	v_cmp_lt_i64_e32 vcc, -1, v[38:39]
	v_pk_fma_f32 v[30:31], v[158:159], s[8:9], v[14:15] op_sel_hi:[1,0,1]
	v_pk_fma_f32 v[34:35], v[154:155], s[8:9], v[10:11] op_sel_hi:[1,0,1]
	v_cndmask_b32_e32 v29, 0, v29, vcc
	v_cndmask_b32_e32 v28, v221, v28, vcc
	v_lshl_add_u64 v[28:29], s[94:95], 0, v[28:29]
	v_lshl_add_u64 v[28:29], v[28:29], 0, s[84:85]
	v_lshl_add_u64 v[32:33], v[28:29], 0, s[6:7]
	v_mov_b32_e32 v28, v199
	v_mov_b32_e32 v29, v199
	v_cvt_pk_fp8_f32 v28, v30, v31
	v_cvt_pk_fp8_f32 v29, v34, v35
	v_pk_fma_f32 v[30:31], v[160:161], s[8:9], v[16:17] op_sel_hi:[1,0,1]
	v_pk_fma_f32 v[34:35], v[156:157], s[8:9], v[12:13] op_sel_hi:[1,0,1]
	v_cvt_pk_fp8_f32 v28, v30, v31 op_sel:[0,0,1]
	v_cvt_pk_fp8_f32 v29, v34, v35 op_sel:[0,0,1]
	v_pk_fma_f32 v[34:35], v[150:151], s[8:9], v[6:7] op_sel_hi:[1,0,1]
	v_pk_fma_f32 v[36:37], v[146:147], s[8:9], v[2:3] op_sel_hi:[1,0,1]
	v_mov_b32_e32 v30, v199
	v_mov_b32_e32 v31, v199
	v_cvt_pk_fp8_f32 v30, v34, v35
	v_cvt_pk_fp8_f32 v31, v36, v37
	v_pk_fma_f32 v[34:35], v[152:153], s[8:9], v[8:9] op_sel_hi:[1,0,1]
	v_pk_fma_f32 v[36:37], v[148:149], s[8:9], v[4:5] op_sel_hi:[1,0,1]
	v_cvt_pk_fp8_f32 v30, v34, v35 op_sel:[0,0,1]
	v_cvt_pk_fp8_f32 v31, v36, v37 op_sel:[0,0,1]
	v_ashrrev_i32_e32 v27, 31, v26
	v_lshl_add_u64 v[32:33], v[32:33], 0, v[202:203]
	v_permlane16_swap_b32_e32 v28, v30
	v_permlane16_swap_b32_e32 v29, v31
	global_store_dwordx4 v[32:33], v[28:31], off nt
	v_cmp_lt_i64_e32 vcc, -1, v[26:27]
	v_pk_fma_f32 v[32:33], v[138:139], s[8:9], v[10:11] op_sel_hi:[1,0,1]
	v_lshlrev_b64 v[28:29], 10, v[26:27]
	v_cndmask_b32_e32 v27, 0, v29, vcc
	v_cndmask_b32_e32 v26, v221, v28, vcc
	v_lshl_add_u64 v[26:27], s[94:95], 0, v[26:27]
	v_lshl_add_u64 v[26:27], v[26:27], 0, s[84:85]
	v_lshl_add_u64 v[30:31], v[26:27], 0, s[6:7]
	v_pk_fma_f32 v[28:29], v[142:143], s[8:9], v[14:15] op_sel_hi:[1,0,1]
	v_mov_b32_e32 v26, v199
	v_mov_b32_e32 v27, v199
	v_cvt_pk_fp8_f32 v26, v28, v29
	v_cvt_pk_fp8_f32 v27, v32, v33
	v_pk_fma_f32 v[28:29], v[144:145], s[8:9], v[16:17] op_sel_hi:[1,0,1]
	v_pk_fma_f32 v[32:33], v[140:141], s[8:9], v[12:13] op_sel_hi:[1,0,1]
	v_cvt_pk_fp8_f32 v26, v28, v29 op_sel:[0,0,1]
	v_cvt_pk_fp8_f32 v27, v32, v33 op_sel:[0,0,1]
	v_pk_fma_f32 v[32:33], v[134:135], s[8:9], v[6:7] op_sel_hi:[1,0,1]
	v_pk_fma_f32 v[34:35], v[130:131], s[8:9], v[2:3] op_sel_hi:[1,0,1]
	v_mov_b32_e32 v28, v199
	v_mov_b32_e32 v29, v199
	v_cvt_pk_fp8_f32 v28, v32, v33
	v_cvt_pk_fp8_f32 v29, v34, v35
	v_pk_fma_f32 v[32:33], v[136:137], s[8:9], v[8:9] op_sel_hi:[1,0,1]
	v_pk_fma_f32 v[34:35], v[132:133], s[8:9], v[4:5] op_sel_hi:[1,0,1]
	v_cvt_pk_fp8_f32 v28, v32, v33 op_sel:[0,0,1]
	v_cvt_pk_fp8_f32 v29, v34, v35 op_sel:[0,0,1]
	v_ashrrev_i32_e32 v25, 31, v24
	v_lshl_add_u64 v[30:31], v[30:31], 0, v[202:203]
	v_permlane16_swap_b32_e32 v26, v28
	v_permlane16_swap_b32_e32 v27, v29
	global_store_dwordx4 v[30:31], v[26:29], off nt
	v_cmp_lt_i64_e32 vcc, -1, v[24:25]
	v_pk_fma_f32 v[30:31], v[122:123], s[8:9], v[10:11] op_sel_hi:[1,0,1]
	v_lshlrev_b64 v[26:27], 10, v[24:25]
	v_cndmask_b32_e32 v25, 0, v27, vcc
	v_cndmask_b32_e32 v24, v221, v26, vcc
	v_lshl_add_u64 v[24:25], s[94:95], 0, v[24:25]
	v_lshl_add_u64 v[24:25], v[24:25], 0, s[84:85]
	v_lshl_add_u64 v[28:29], v[24:25], 0, s[6:7]
	v_pk_fma_f32 v[26:27], v[126:127], s[8:9], v[14:15] op_sel_hi:[1,0,1]
	v_mov_b32_e32 v24, v199
	v_mov_b32_e32 v25, v199
	v_cvt_pk_fp8_f32 v24, v26, v27
	v_cvt_pk_fp8_f32 v25, v30, v31
	v_pk_fma_f32 v[26:27], v[128:129], s[8:9], v[16:17] op_sel_hi:[1,0,1]
	v_pk_fma_f32 v[30:31], v[124:125], s[8:9], v[12:13] op_sel_hi:[1,0,1]
	v_cvt_pk_fp8_f32 v24, v26, v27 op_sel:[0,0,1]
	v_cvt_pk_fp8_f32 v25, v30, v31 op_sel:[0,0,1]
	v_pk_fma_f32 v[30:31], v[118:119], s[8:9], v[6:7] op_sel_hi:[1,0,1]
	v_pk_fma_f32 v[32:33], v[114:115], s[8:9], v[2:3] op_sel_hi:[1,0,1]
	v_mov_b32_e32 v26, v199
	v_mov_b32_e32 v27, v199
	v_cvt_pk_fp8_f32 v26, v30, v31
	v_cvt_pk_fp8_f32 v27, v32, v33
	v_pk_fma_f32 v[30:31], v[120:121], s[8:9], v[8:9] op_sel_hi:[1,0,1]
	v_pk_fma_f32 v[32:33], v[116:117], s[8:9], v[4:5] op_sel_hi:[1,0,1]
	v_cvt_pk_fp8_f32 v26, v30, v31 op_sel:[0,0,1]
	v_cvt_pk_fp8_f32 v27, v32, v33 op_sel:[0,0,1]
	v_ashrrev_i32_e32 v23, 31, v22
	v_lshl_add_u64 v[28:29], v[28:29], 0, v[202:203]
	v_permlane16_swap_b32_e32 v24, v26
	v_permlane16_swap_b32_e32 v25, v27
	global_store_dwordx4 v[28:29], v[24:27], off nt
	v_cmp_lt_i64_e32 vcc, -1, v[22:23]
	v_pk_fma_f32 v[28:29], v[98:99], s[8:9], v[10:11] op_sel_hi:[1,0,1]
	v_lshlrev_b64 v[24:25], 10, v[22:23]
	v_cndmask_b32_e32 v23, 0, v25, vcc
	v_cndmask_b32_e32 v22, v221, v24, vcc
	v_lshl_add_u64 v[22:23], s[94:95], 0, v[22:23]
	v_lshl_add_u64 v[22:23], v[22:23], 0, s[84:85]
	v_lshl_add_u64 v[26:27], v[22:23], 0, s[6:7]
	v_pk_fma_f32 v[24:25], v[106:107], s[8:9], v[14:15] op_sel_hi:[1,0,1]
	v_mov_b32_e32 v22, v199
	v_mov_b32_e32 v23, v199
	v_cvt_pk_fp8_f32 v22, v24, v25
	v_cvt_pk_fp8_f32 v23, v28, v29
	v_pk_fma_f32 v[24:25], v[108:109], s[8:9], v[16:17] op_sel_hi:[1,0,1]
	v_pk_fma_f32 v[28:29], v[100:101], s[8:9], v[12:13] op_sel_hi:[1,0,1]
	v_cvt_pk_fp8_f32 v22, v24, v25 op_sel:[0,0,1]
	v_cvt_pk_fp8_f32 v23, v28, v29 op_sel:[0,0,1]
	v_pk_fma_f32 v[28:29], v[90:91], s[8:9], v[6:7] op_sel_hi:[1,0,1]
	v_pk_fma_f32 v[30:31], v[82:83], s[8:9], v[2:3] op_sel_hi:[1,0,1]
	v_mov_b32_e32 v24, v199
	v_mov_b32_e32 v25, v199
	v_cvt_pk_fp8_f32 v24, v28, v29
	v_cvt_pk_fp8_f32 v25, v30, v31
	v_pk_fma_f32 v[28:29], v[92:93], s[8:9], v[8:9] op_sel_hi:[1,0,1]
	v_pk_fma_f32 v[30:31], v[84:85], s[8:9], v[4:5] op_sel_hi:[1,0,1]
	v_cvt_pk_fp8_f32 v24, v28, v29 op_sel:[0,0,1]
	v_cvt_pk_fp8_f32 v25, v30, v31 op_sel:[0,0,1]
	v_ashrrev_i32_e32 v21, 31, v20
	v_lshl_add_u64 v[26:27], v[26:27], 0, v[202:203]
	v_permlane16_swap_b32_e32 v22, v24
	v_permlane16_swap_b32_e32 v23, v25
	global_store_dwordx4 v[26:27], v[22:25], off nt
	v_cmp_lt_i64_e32 vcc, -1, v[20:21]
	v_pk_fma_f32 v[26:27], v[74:75], s[8:9], v[10:11] op_sel_hi:[1,0,1]
	v_lshlrev_b64 v[22:23], 10, v[20:21]
	v_cndmask_b32_e32 v21, 0, v23, vcc
	v_cndmask_b32_e32 v20, v221, v22, vcc
	v_lshl_add_u64 v[20:21], s[94:95], 0, v[20:21]
	v_lshl_add_u64 v[20:21], v[20:21], 0, s[84:85]
	v_lshl_add_u64 v[24:25], v[20:21], 0, s[6:7]
	v_pk_fma_f32 v[22:23], v[78:79], s[8:9], v[14:15] op_sel_hi:[1,0,1]
	v_mov_b32_e32 v20, v199
	v_mov_b32_e32 v21, v199
	v_cvt_pk_fp8_f32 v20, v22, v23
	v_cvt_pk_fp8_f32 v21, v26, v27
	v_pk_fma_f32 v[22:23], v[80:81], s[8:9], v[16:17] op_sel_hi:[1,0,1]
	v_pk_fma_f32 v[26:27], v[76:77], s[8:9], v[12:13] op_sel_hi:[1,0,1]
	v_cvt_pk_fp8_f32 v20, v22, v23 op_sel:[0,0,1]
	v_cvt_pk_fp8_f32 v21, v26, v27 op_sel:[0,0,1]
	v_pk_fma_f32 v[26:27], v[102:103], s[8:9], v[6:7] op_sel_hi:[1,0,1]
	v_pk_fma_f32 v[28:29], v[110:111], s[8:9], v[2:3] op_sel_hi:[1,0,1]
	v_mov_b32_e32 v22, v199
	v_mov_b32_e32 v23, v199
	v_cvt_pk_fp8_f32 v22, v26, v27
	v_cvt_pk_fp8_f32 v23, v28, v29
	v_pk_fma_f32 v[26:27], v[104:105], s[8:9], v[8:9] op_sel_hi:[1,0,1]
	v_pk_fma_f32 v[28:29], v[112:113], s[8:9], v[4:5] op_sel_hi:[1,0,1]
	v_cvt_pk_fp8_f32 v22, v26, v27 op_sel:[0,0,1]
	v_cvt_pk_fp8_f32 v23, v28, v29 op_sel:[0,0,1]
	v_ashrrev_i32_e32 v19, 31, v18
	v_lshl_add_u64 v[24:25], v[24:25], 0, v[202:203]
	v_permlane16_swap_b32_e32 v20, v22
	v_permlane16_swap_b32_e32 v21, v23
	global_store_dwordx4 v[24:25], v[20:23], off nt
	v_cmp_lt_i64_e32 vcc, -1, v[18:19]
	v_pk_fma_f32 v[12:13], v[68:69], s[8:9], v[12:13] op_sel_hi:[1,0,1]
	v_lshlrev_b64 v[20:21], 10, v[18:19]
	v_cndmask_b32_e32 v19, 0, v21, vcc
	v_cndmask_b32_e32 v18, v221, v20, vcc
	v_pk_fma_f32 v[20:21], v[66:67], s[8:9], v[10:11] op_sel_hi:[1,0,1]
	v_mov_b32_e32 v11, v199
	v_cvt_pk_fp8_f32 v11, v20, v21
	v_pk_fma_f32 v[14:15], v[70:71], s[8:9], v[14:15] op_sel_hi:[1,0,1]
	v_mov_b32_e32 v10, v199
	v_pk_fma_f32 v[6:7], v[86:87], s[8:9], v[6:7] op_sel_hi:[1,0,1]
	v_cvt_pk_fp8_f32 v11, v12, v13 op_sel:[0,0,1]
	v_pk_fma_f32 v[2:3], v[94:95], s[8:9], v[2:3] op_sel_hi:[1,0,1]
	v_mov_b32_e32 v12, v199
	v_mov_b32_e32 v13, v199
	v_cvt_pk_fp8_f32 v10, v14, v15
	v_cvt_pk_fp8_f32 v12, v6, v7
	v_cvt_pk_fp8_f32 v13, v2, v3
	v_pk_fma_f32 v[14:15], v[72:73], s[8:9], v[16:17] op_sel_hi:[1,0,1]
	v_pk_fma_f32 v[2:3], v[88:89], s[8:9], v[8:9] op_sel_hi:[1,0,1]
	v_pk_fma_f32 v[4:5], v[96:97], s[8:9], v[4:5] op_sel_hi:[1,0,1]
	v_cvt_pk_fp8_f32 v10, v14, v15 op_sel:[0,0,1]
	v_cvt_pk_fp8_f32 v12, v2, v3 op_sel:[0,0,1]
	v_cvt_pk_fp8_f32 v13, v4, v5 op_sel:[0,0,1]
	v_lshl_add_u64 v[18:19], s[94:95], 0, v[18:19]
	v_lshl_add_u64 v[18:19], v[18:19], 0, s[84:85]
	v_lshl_add_u64 v[18:19], v[18:19], 0, s[6:7]
	v_lshl_add_u64 v[2:3], v[18:19], 0, v[202:203]
	v_permlane16_swap_b32_e32 v10, v12
	v_permlane16_swap_b32_e32 v11, v13
	s_and_b64 vcc, exec, s[2:3]
	s_mov_b64 s[0:1], -1
	global_store_dwordx4 v[2:3], v[10:13], off nt
	s_cbranch_vccnz .LBB0_1076
	s_andn2_b64 vcc, exec, s[90:91]
	s_cbranch_vccnz .LBB0_1075
	s_barrier
	s_branch .LBB0_1075
